# GEMM K-loops: counted lgkmcnt waits in front of the MFMAs that first use each LDS fragment instead of lgkmcnt(0) before every MFMA block
# speedup vs baseline: 1.0052x; 1.0002x over previous
; #define PG8_STAGE(bufoff, gbase, voff) do { _Pragma("unroll") for (int _i = 0; _i < 2; ++_i) \
;         __builtin_amdgcn_global_load_lds((const unsigned*)((const char*)(gbase) + (voff)[_i]), (LAS unsigned*)(lds + (bufoff) + ldsw + _i * 8192), 16, 0, 0); } while (0)
; #define PG8_LDA(dst, b, h) do { _Pragma("unroll") for (int m = 0; m < 4; ++m) _Pragma("unroll") for (int k = 0; k < 2; ++k) dst[m][k] = *(const LAS bf16x8*)(lds + PG8_SA(b, h) + aoff + m * 2048 + k * 1024); } while (0)
; #define PG8_LDB(dst, b, h) do { _Pragma("unroll") for (int n = 0; n < 2; ++n) _Pragma("unroll") for (int k = 0; k < 2; ++k) dst[n][k] = *(const LAS bf16x8*)(lds + PG8_SB(b, h) + boff + n * 2048 + k * 1024); } while (0)
; #define PG8_MMA(ai, bj, At, Bt) do { __builtin_amdgcn_s_setprio(1); _Pragma("unroll") for (int m = 0; m < 4; ++m) _Pragma("unroll") for (int n = 0; n < 2; ++n) _Pragma("unroll") for (int k = 0; k < 2; ++k) \
;         acc[ai][bj][m][n] = __builtin_amdgcn_mfma_f32_16x16x32_bf16(Bt[n][k], At[m][k], acc[ai][bj][m][n], 0, 0, 0); __builtin_amdgcn_s_setprio(0); } while (0)
; #define PG8_WAIT_L(n) asm volatile("s_waitcnt lgkmcnt(" #n ")" ::: "memory")
; #define PG8_BAR __builtin_amdgcn_s_barrier()
; #define PG8_SCHED __builtin_amdgcn_sched_barrier(0)
; template <class Epi, class Sched>
; __device__ __forceinline__ void gemm_phase(LAS unsigned char* lds, const bf16_t* A, const int K, const Sched& S, const Epi& E, const int wv) {
;     ...
;             PG8_LDB(B0, 0, 0); PG8_SCHED; PG8_LDA(At, 0, 0); PG8_STAGE_A(PG8_SA(1, 1), 1, false, k1);
;             PG8_WAIT_L(8); PG8_BAR; PG8_WAIT_L(0); PG8_MMA(0, 0, At, B0); PG8_BAR; PG8_SCHED;
;             PG8_LDB(B1, 0, 1); PG8_STAGE(PG8_SB(0, 0), b2, voffB);
;             PG8_BAR; PG8_WAIT_L(0); PG8_MMA(0, 1, At, B1); PG8_BAR;
;             PG8_LDA(At, 0, 1); PG8_STAGE_A(PG8_SA(0, 0), 0, last, k2);
;             PG8_BAR; PG8_WAIT_L(0); PG8_MMA(1, 0, At, B0); PG8_BAR; PG8_SCHED;
.Lmy_ph_0:
.LBB0_319:
	s_add_u32 s42, s10, 0x100
	ds_read_b128 v[132:135], v208
	ds_read_b128 v[136:139], v208 offset:1024
	ds_read_b128 v[140:143], v208 offset:2048
	ds_read_b128 v[144:147], v208 offset:3072
	s_addc_u32 s43, s11, 0
	s_add_u32 s82, s17, s10
	s_addc_u32 s83, s33, s11
	s_cmp_eq_u32 s79, 28
	s_cselect_b64 s[80:81], -1, 0
	s_and_b64 s[54:55], s[80:81], exec
	s_cselect_b32 s84, 0, s42
	s_cselect_b32 s55, s15, s83
	s_cselect_b32 s54, s18, s82
	v_lshl_add_u64 v[218:219], v[128:129], 0, s[10:11]
	s_add_i32 m0, s65, 0xc000
	ds_read_b128 v[148:151], v209
	ds_read_b128 v[152:155], v209 offset:1024
	ds_read_b128 v[156:159], v209 offset:2048
	ds_read_b128 v[192:195], v209 offset:3072
	ds_read_b128 v[196:199], v209 offset:4096
	ds_read_b128 v[200:203], v209 offset:5120
	ds_read_b128 v[204:207], v209 offset:6144
	ds_read_b128 v[214:217], v209 offset:7168
	global_load_lds_dwordx4 v[218:219], off
	v_lshl_add_u64 v[218:219], v[130:131], 0, s[10:11]
	s_add_i32 m0, s65, 0xe000
	s_nop 0
	global_load_lds_dwordx4 v[218:219], off
	s_waitcnt lgkmcnt(8)
	s_barrier
	s_setprio 1
	s_waitcnt lgkmcnt(7)
	v_mfma_f32_16x16x32_bf16 v[124:127], v[132:135], v[148:151], v[124:127]
	v_mfma_f32_16x16x32_bf16 v[120:123], v[140:143], v[148:151], v[120:123]
	s_waitcnt lgkmcnt(5)
	v_mfma_f32_16x16x32_bf16 v[108:111], v[132:135], v[156:159], v[108:111]
	v_mfma_f32_16x16x32_bf16 v[104:107], v[140:143], v[156:159], v[104:107]
	s_waitcnt lgkmcnt(3)
	v_mfma_f32_16x16x32_bf16 v[92:95], v[132:135], v[196:199], v[92:95]
	v_mfma_f32_16x16x32_bf16 v[88:91], v[140:143], v[196:199], v[88:91]
	s_waitcnt lgkmcnt(1)
	v_mfma_f32_16x16x32_bf16 v[76:79], v[132:135], v[204:207], v[76:79]
	v_mfma_f32_16x16x32_bf16 v[72:75], v[140:143], v[204:207], v[72:75]
	v_mfma_f32_16x16x32_bf16 v[124:127], v[136:139], v[152:155], v[124:127]
	v_mfma_f32_16x16x32_bf16 v[120:123], v[144:147], v[152:155], v[120:123]
	v_mfma_f32_16x16x32_bf16 v[108:111], v[136:139], v[192:195], v[108:111]
	v_mfma_f32_16x16x32_bf16 v[104:107], v[144:147], v[192:195], v[104:107]
	v_mfma_f32_16x16x32_bf16 v[92:95], v[136:139], v[200:203], v[92:95]
	v_mfma_f32_16x16x32_bf16 v[88:91], v[144:147], v[200:203], v[88:91]
	s_waitcnt lgkmcnt(0)
	v_mfma_f32_16x16x32_bf16 v[76:79], v[136:139], v[214:217], v[76:79]
	v_mfma_f32_16x16x32_bf16 v[72:75], v[144:147], v[214:217], v[72:75]
	s_setprio 0
	s_barrier
	s_add_i32 s10, s74, s64
	v_lshl_add_u64 v[234:235], s[54:55], 0, v[162:163]
	s_mov_b32 m0, s10
	ds_read_b128 v[218:221], v210
	ds_read_b128 v[222:225], v210 offset:1024
	ds_read_b128 v[226:229], v210 offset:2048
	ds_read_b128 v[230:233], v210 offset:3072
	global_load_lds_dwordx4 v[234:235], off
	v_lshl_add_u64 v[236:237], s[54:55], 0, v[166:167]
	s_add_i32 m0, s10, 0x2000
	s_nop 0
	global_load_lds_dwordx4 v[236:237], off
	s_barrier
	s_setprio 1
	s_waitcnt lgkmcnt(3)
	v_mfma_f32_16x16x32_bf16 v[116:119], v[218:221], v[148:151], v[116:119]
	s_waitcnt lgkmcnt(1)
	v_mfma_f32_16x16x32_bf16 v[112:115], v[226:229], v[148:151], v[112:115]
	v_mfma_f32_16x16x32_bf16 v[100:103], v[218:221], v[156:159], v[100:103]
	v_mfma_f32_16x16x32_bf16 v[96:99], v[226:229], v[156:159], v[96:99]
	v_mfma_f32_16x16x32_bf16 v[84:87], v[218:221], v[196:199], v[84:87]
	v_mfma_f32_16x16x32_bf16 v[80:83], v[226:229], v[196:199], v[80:83]
	v_mfma_f32_16x16x32_bf16 v[68:71], v[218:221], v[204:207], v[68:71]
	v_mfma_f32_16x16x32_bf16 v[64:67], v[226:229], v[204:207], v[64:67]
	v_mfma_f32_16x16x32_bf16 v[116:119], v[222:225], v[152:155], v[116:119]
	s_waitcnt lgkmcnt(0)
	v_mfma_f32_16x16x32_bf16 v[112:115], v[230:233], v[152:155], v[112:115]
	v_mfma_f32_16x16x32_bf16 v[100:103], v[222:225], v[192:195], v[100:103]
	v_mfma_f32_16x16x32_bf16 v[96:99], v[230:233], v[192:195], v[96:99]
	v_mfma_f32_16x16x32_bf16 v[84:87], v[222:225], v[200:203], v[84:87]
	v_mfma_f32_16x16x32_bf16 v[80:83], v[230:233], v[200:203], v[80:83]
	v_mfma_f32_16x16x32_bf16 v[68:71], v[222:225], v[214:217], v[68:71]
	v_mfma_f32_16x16x32_bf16 v[64:67], v[230:233], v[214:217], v[64:67]
	s_setprio 0
	s_and_b64 s[10:11], s[8:9], s[80:81]
	s_and_b64 s[10:11], s[10:11], exec
	s_cselect_b32 s10, s28, s2
	s_cselect_b32 s11, s29, s3
	s_add_u32 s10, s10, s84
	s_addc_u32 s11, s11, 0
	s_mov_b32 m0, s65
	v_lshl_add_u64 v[238:239], s[10:11], 0, v[160:161]
	s_barrier
	ds_read_b128 v[148:151], v209 offset:16384
	ds_read_b128 v[152:155], v209 offset:17408
	ds_read_b128 v[156:159], v209 offset:18432
	ds_read_b128 v[192:195], v209 offset:19456
	ds_read_b128 v[196:199], v209 offset:20480
	ds_read_b128 v[200:203], v209 offset:21504
	ds_read_b128 v[204:207], v209 offset:22528
	ds_read_b128 v[214:217], v209 offset:23552
	global_load_lds_dwordx4 v[238:239], off
	v_lshl_add_u64 v[240:241], s[10:11], 0, v[164:165]
	s_mov_b32 m0, s66
	s_nop 0
	global_load_lds_dwordx4 v[240:241], off
	s_barrier
	s_setprio 1
	s_waitcnt lgkmcnt(7)
	v_mfma_f32_16x16x32_bf16 v[60:63], v[132:135], v[148:151], v[60:63]
	v_mfma_f32_16x16x32_bf16 v[56:59], v[140:143], v[148:151], v[56:59]
	s_waitcnt lgkmcnt(5)
	v_mfma_f32_16x16x32_bf16 v[44:47], v[132:135], v[156:159], v[44:47]
	v_mfma_f32_16x16x32_bf16 v[40:43], v[140:143], v[156:159], v[40:43]
	s_waitcnt lgkmcnt(3)
	v_mfma_f32_16x16x32_bf16 v[28:31], v[132:135], v[196:199], v[28:31]
	v_mfma_f32_16x16x32_bf16 v[24:27], v[140:143], v[196:199], v[24:27]
	s_waitcnt lgkmcnt(1)
	v_mfma_f32_16x16x32_bf16 v[12:15], v[132:135], v[204:207], v[12:15]
	v_mfma_f32_16x16x32_bf16 v[8:11], v[140:143], v[204:207], v[8:11]
	v_mfma_f32_16x16x32_bf16 v[60:63], v[136:139], v[152:155], v[60:63]
	v_mfma_f32_16x16x32_bf16 v[56:59], v[144:147], v[152:155], v[56:59]
	v_mfma_f32_16x16x32_bf16 v[44:47], v[136:139], v[192:195], v[44:47]
	v_mfma_f32_16x16x32_bf16 v[40:43], v[144:147], v[192:195], v[40:43]
	v_mfma_f32_16x16x32_bf16 v[28:31], v[136:139], v[200:203], v[28:31]
	v_mfma_f32_16x16x32_bf16 v[24:27], v[144:147], v[200:203], v[24:27]
	s_waitcnt lgkmcnt(0)
	v_mfma_f32_16x16x32_bf16 v[12:15], v[136:139], v[214:217], v[12:15]
	v_mfma_f32_16x16x32_bf16 v[8:11], v[144:147], v[214:217], v[8:11]
	s_setprio 0
	s_barrier
; #define PG8_STAGE(bufoff, gbase, voff) do { _Pragma("unroll") for (int _i = 0; _i < 2; ++_i) \
;         __builtin_amdgcn_global_load_lds((const unsigned*)((const char*)(gbase) + (voff)[_i]), (LAS unsigned*)(lds + (bufoff) + ldsw + _i * 8192), 16, 0, 0); } while (0)
; #define PG8_LDA(dst, b, h) do { _Pragma("unroll") for (int m = 0; m < 4; ++m) _Pragma("unroll") for (int k = 0; k < 2; ++k) dst[m][k] = *(const LAS bf16x8*)(lds + PG8_SA(b, h) + aoff + m * 2048 + k * 1024); } while (0)
; #define PG8_LDB(dst, b, h) do { _Pragma("unroll") for (int n = 0; n < 2; ++n) _Pragma("unroll") for (int k = 0; k < 2; ++k) dst[n][k] = *(const LAS bf16x8*)(lds + PG8_SB(b, h) + boff + n * 2048 + k * 1024); } while (0)
; #define PG8_MMA(ai, bj, At, Bt) do { __builtin_amdgcn_s_setprio(1); _Pragma("unroll") for (int m = 0; m < 4; ++m) _Pragma("unroll") for (int n = 0; n < 2; ++n) _Pragma("unroll") for (int k = 0; k < 2; ++k) \
;         acc[ai][bj][m][n] = __builtin_amdgcn_mfma_f32_16x16x32_bf16(Bt[n][k], At[m][k], acc[ai][bj][m][n], 0, 0, 0); __builtin_amdgcn_s_setprio(0); } while (0)
; #define PG8_WAIT_V(n) asm volatile("s_waitcnt vmcnt(" #n ")" ::: "memory")
; #define PG8_WAIT_L(n) asm volatile("s_waitcnt lgkmcnt(" #n ")" ::: "memory")
; #define PG8_BAR __builtin_amdgcn_s_barrier()
; #define PG8_SCHED __builtin_amdgcn_sched_barrier(0)
; template <class Epi, class Sched>
; __device__ __forceinline__ void gemm_phase(LAS unsigned char* lds, const bf16_t* A, const int K, const Sched& S, const Epi& E, const int wv) {
;     ...
;             PG8_STAGE(PG8_SB(0, 1), b2 + hstep, voffB);
;             PG8_WAIT_V(6); PG8_BAR; PG8_MMA(1, 1, At, B1); PG8_BAR;
;             PG8_LDB(B0, 1, 0); PG8_SCHED; PG8_LDA(At, 1, 0); PG8_STAGE_A(PG8_SA(0, 1), 1, last, k2);
;             PG8_WAIT_L(8); PG8_BAR; PG8_WAIT_L(0); PG8_MMA(0, 0, At, B0); PG8_BAR; PG8_SCHED;
;             PG8_LDB(B1, 1, 1); PG8_STAGE(PG8_SB(1, 0), b3, voffB);
	s_add_u32 s80, s54, 0x80000
	s_addc_u32 s81, s55, 0
	s_add_i32 s82, s75, s64
	v_lshl_add_u64 v[132:133], s[80:81], 0, v[162:163]
	s_mov_b32 m0, s82
	s_nop 0
	global_load_lds_dwordx4 v[132:133], off
	v_lshl_add_u64 v[132:133], s[80:81], 0, v[166:167]
	s_add_i32 m0, s82, 0x2000
	s_nop 0
	global_load_lds_dwordx4 v[132:133], off
	s_waitcnt vmcnt(6)
	s_barrier
	s_setprio 1
	v_mfma_f32_16x16x32_bf16 v[52:55], v[218:221], v[148:151], v[52:55]
	v_mfma_f32_16x16x32_bf16 v[48:51], v[226:229], v[148:151], v[48:51]
	v_mfma_f32_16x16x32_bf16 v[36:39], v[218:221], v[156:159], v[36:39]
	v_mfma_f32_16x16x32_bf16 v[32:35], v[226:229], v[156:159], v[32:35]
	v_mfma_f32_16x16x32_bf16 v[20:23], v[218:221], v[196:199], v[20:23]
	v_mfma_f32_16x16x32_bf16 v[16:19], v[226:229], v[196:199], v[16:19]
	v_mfma_f32_16x16x32_bf16 v[4:7], v[218:221], v[204:207], v[4:7]
	v_mfma_f32_16x16x32_bf16 v[0:3], v[226:229], v[204:207], v[0:3]
	v_mfma_f32_16x16x32_bf16 v[52:55], v[222:225], v[152:155], v[52:55]
	v_mfma_f32_16x16x32_bf16 v[48:51], v[230:233], v[152:155], v[48:51]
	v_mfma_f32_16x16x32_bf16 v[36:39], v[222:225], v[192:195], v[36:39]
	v_mfma_f32_16x16x32_bf16 v[32:35], v[230:233], v[192:195], v[32:35]
	v_mfma_f32_16x16x32_bf16 v[20:23], v[222:225], v[200:203], v[20:23]
	v_mfma_f32_16x16x32_bf16 v[16:19], v[230:233], v[200:203], v[16:19]
	v_mfma_f32_16x16x32_bf16 v[4:7], v[222:225], v[214:217], v[4:7]
	v_mfma_f32_16x16x32_bf16 v[0:3], v[230:233], v[214:217], v[0:3]
	s_setprio 0
	s_add_i32 s80, 0, 0x18000
	v_add_u32_e32 v144, s80, v173
	s_barrier
	ds_read_b128 v[132:135], v144
	ds_read_b128 v[136:139], v144 offset:1024
	ds_read_b128 v[140:143], v144 offset:2048
	ds_read_b128 v[144:147], v144 offset:3072
	s_add_u32 s10, s10, 0x80000
	s_addc_u32 s11, s11, 0
	s_mov_b32 m0, s67
	v_lshl_add_u64 v[218:219], s[10:11], 0, v[160:161]
	ds_read_b128 v[148:151], v209 offset:32768
	ds_read_b128 v[152:155], v209 offset:33792
	ds_read_b128 v[156:159], v209 offset:34816
	ds_read_b128 v[192:195], v209 offset:35840
	ds_read_b128 v[196:199], v209 offset:36864
	ds_read_b128 v[200:203], v209 offset:37888
	ds_read_b128 v[204:207], v209 offset:38912
	ds_read_b128 v[214:217], v209 offset:39936
	global_load_lds_dwordx4 v[218:219], off
	v_lshl_add_u64 v[218:219], s[10:11], 0, v[164:165]
	s_mov_b32 m0, s68
	s_nop 0
	global_load_lds_dwordx4 v[218:219], off
	s_waitcnt lgkmcnt(8)
	s_barrier
	s_setprio 1
	s_waitcnt lgkmcnt(7)
	v_mfma_f32_16x16x32_bf16 v[124:127], v[132:135], v[148:151], v[124:127]
	v_mfma_f32_16x16x32_bf16 v[120:123], v[140:143], v[148:151], v[120:123]
	s_waitcnt lgkmcnt(5)
	v_mfma_f32_16x16x32_bf16 v[108:111], v[132:135], v[156:159], v[108:111]
	v_mfma_f32_16x16x32_bf16 v[104:107], v[140:143], v[156:159], v[104:107]
	s_waitcnt lgkmcnt(3)
	v_mfma_f32_16x16x32_bf16 v[92:95], v[132:135], v[196:199], v[92:95]
	v_mfma_f32_16x16x32_bf16 v[88:91], v[140:143], v[196:199], v[88:91]
	s_waitcnt lgkmcnt(1)
	v_mfma_f32_16x16x32_bf16 v[76:79], v[132:135], v[204:207], v[76:79]
	v_mfma_f32_16x16x32_bf16 v[72:75], v[140:143], v[204:207], v[72:75]
	v_mfma_f32_16x16x32_bf16 v[124:127], v[136:139], v[152:155], v[124:127]
	v_mfma_f32_16x16x32_bf16 v[120:123], v[144:147], v[152:155], v[120:123]
	v_mfma_f32_16x16x32_bf16 v[108:111], v[136:139], v[192:195], v[108:111]
	v_mfma_f32_16x16x32_bf16 v[104:107], v[144:147], v[192:195], v[104:107]
	v_mfma_f32_16x16x32_bf16 v[92:95], v[136:139], v[200:203], v[92:95]
	v_mfma_f32_16x16x32_bf16 v[88:91], v[144:147], v[200:203], v[88:91]
	s_waitcnt lgkmcnt(0)
	v_mfma_f32_16x16x32_bf16 v[76:79], v[136:139], v[214:217], v[76:79]
	v_mfma_f32_16x16x32_bf16 v[72:75], v[144:147], v[214:217], v[72:75]
	s_setprio 0
	s_barrier
	s_add_i32 s81, 0, 0x1c000
	s_add_i32 s10, s80, s64
	v_add_u32_e32 v168, s81, v173
	v_lshl_add_u64 v[234:235], v[234:235], 0, s[26:27]
	s_mov_b32 m0, s10
	ds_read_b128 v[218:221], v168
	ds_read_b128 v[222:225], v168 offset:1024
	ds_read_b128 v[226:229], v168 offset:2048
	ds_read_b128 v[230:233], v168 offset:3072
	global_load_lds_dwordx4 v[234:235], off
	v_lshl_add_u64 v[234:235], v[236:237], 0, s[26:27]
	s_add_i32 m0, s10, 0x2000
	s_nop 0
	global_load_lds_dwordx4 v[234:235], off
	s_barrier
; #define PG8_STAGE(bufoff, gbase, voff) do { _Pragma("unroll") for (int _i = 0; _i < 2; ++_i) \
;         __builtin_amdgcn_global_load_lds((const unsigned*)((const char*)(gbase) + (voff)[_i]), (LAS unsigned*)(lds + (bufoff) + ldsw + _i * 8192), 16, 0, 0); } while (0)
; #define PG8_LDA(dst, b, h) do { _Pragma("unroll") for (int m = 0; m < 4; ++m) _Pragma("unroll") for (int k = 0; k < 2; ++k) dst[m][k] = *(const LAS bf16x8*)(lds + PG8_SA(b, h) + aoff + m * 2048 + k * 1024); } while (0)
; #define PG8_LDB(dst, b, h) do { _Pragma("unroll") for (int n = 0; n < 2; ++n) _Pragma("unroll") for (int k = 0; k < 2; ++k) dst[n][k] = *(const LAS bf16x8*)(lds + PG8_SB(b, h) + boff + n * 2048 + k * 1024); } while (0)
; #define PG8_MMA(ai, bj, At, Bt) do { __builtin_amdgcn_s_setprio(1); _Pragma("unroll") for (int m = 0; m < 4; ++m) _Pragma("unroll") for (int n = 0; n < 2; ++n) _Pragma("unroll") for (int k = 0; k < 2; ++k) \
;         acc[ai][bj][m][n] = __builtin_amdgcn_mfma_f32_16x16x32_bf16(Bt[n][k], At[m][k], acc[ai][bj][m][n], 0, 0, 0); __builtin_amdgcn_s_setprio(0); } while (0)
; #define PG8_WAIT_V(n) asm volatile("s_waitcnt vmcnt(" #n ")" ::: "memory")
; #define PG8_WAIT_L(n) asm volatile("s_waitcnt lgkmcnt(" #n ")" ::: "memory")
; #define PG8_BAR __builtin_amdgcn_s_barrier()
; #define PG8_SCHED __builtin_amdgcn_sched_barrier(0)
; template <class Epi, class Sched>
; __device__ __forceinline__ void gemm_phase(LAS unsigned char* lds, const bf16_t* A, const int K, const Sched& S, const Epi& E, const int wv) {
;     ...
;             PG8_LDB(B1, 1, 1); PG8_STAGE(PG8_SB(1, 0), b3, voffB);
;             PG8_BAR; PG8_WAIT_L(0); PG8_MMA(0, 1, At, B1); PG8_BAR;
;             PG8_LDA(At, 1, 1); PG8_STAGE_A(PG8_SA(1, 0), 0, last, k3);
;             PG8_BAR; PG8_WAIT_L(0); PG8_MMA(1, 0, At, B0); PG8_BAR; PG8_SCHED;
;             PG8_STAGE(PG8_SB(1, 1), b3 + hstep, voffB);
;             PG8_WAIT_V(6); PG8_BAR; PG8_MMA(1, 1, At, B1); PG8_BAR;
;         }
	s_setprio 1
	s_waitcnt lgkmcnt(3)
	v_mfma_f32_16x16x32_bf16 v[116:119], v[218:221], v[148:151], v[116:119]
	s_waitcnt lgkmcnt(1)
	v_mfma_f32_16x16x32_bf16 v[112:115], v[226:229], v[148:151], v[112:115]
	v_mfma_f32_16x16x32_bf16 v[100:103], v[218:221], v[156:159], v[100:103]
	v_mfma_f32_16x16x32_bf16 v[96:99], v[226:229], v[156:159], v[96:99]
	v_mfma_f32_16x16x32_bf16 v[84:87], v[218:221], v[196:199], v[84:87]
	v_mfma_f32_16x16x32_bf16 v[80:83], v[226:229], v[196:199], v[80:83]
	v_mfma_f32_16x16x32_bf16 v[68:71], v[218:221], v[204:207], v[68:71]
	v_mfma_f32_16x16x32_bf16 v[64:67], v[226:229], v[204:207], v[64:67]
	v_mfma_f32_16x16x32_bf16 v[116:119], v[222:225], v[152:155], v[116:119]
	s_waitcnt lgkmcnt(0)
	v_mfma_f32_16x16x32_bf16 v[112:115], v[230:233], v[152:155], v[112:115]
	v_mfma_f32_16x16x32_bf16 v[100:103], v[222:225], v[192:195], v[100:103]
	v_mfma_f32_16x16x32_bf16 v[96:99], v[230:233], v[192:195], v[96:99]
	v_mfma_f32_16x16x32_bf16 v[84:87], v[222:225], v[200:203], v[84:87]
	v_mfma_f32_16x16x32_bf16 v[80:83], v[230:233], v[200:203], v[80:83]
	v_mfma_f32_16x16x32_bf16 v[68:71], v[222:225], v[214:217], v[68:71]
	v_mfma_f32_16x16x32_bf16 v[64:67], v[230:233], v[214:217], v[64:67]
	s_setprio 0
	s_mov_b32 m0, s70
	v_lshl_add_u64 v[234:235], v[238:239], 0, s[26:27]
	s_barrier
	ds_read_b128 v[148:151], v209 offset:49152
	ds_read_b128 v[152:155], v209 offset:50176
	ds_read_b128 v[156:159], v209 offset:51200
	ds_read_b128 v[192:195], v209 offset:52224
	ds_read_b128 v[196:199], v209 offset:53248
	ds_read_b128 v[200:203], v209 offset:54272
	ds_read_b128 v[204:207], v209 offset:55296
	ds_read_b128 v[214:217], v209 offset:56320
	global_load_lds_dwordx4 v[234:235], off
	v_lshl_add_u64 v[234:235], v[240:241], 0, s[26:27]
	s_mov_b32 m0, s71
	s_nop 0
	global_load_lds_dwordx4 v[234:235], off
	s_barrier
	s_setprio 1
	s_waitcnt lgkmcnt(7)
	v_mfma_f32_16x16x32_bf16 v[60:63], v[132:135], v[148:151], v[60:63]
	v_mfma_f32_16x16x32_bf16 v[56:59], v[140:143], v[148:151], v[56:59]
	s_waitcnt lgkmcnt(5)
	v_mfma_f32_16x16x32_bf16 v[44:47], v[132:135], v[156:159], v[44:47]
	v_mfma_f32_16x16x32_bf16 v[40:43], v[140:143], v[156:159], v[40:43]
	s_waitcnt lgkmcnt(3)
	v_mfma_f32_16x16x32_bf16 v[28:31], v[132:135], v[196:199], v[28:31]
	v_mfma_f32_16x16x32_bf16 v[24:27], v[140:143], v[196:199], v[24:27]
	s_waitcnt lgkmcnt(1)
	v_mfma_f32_16x16x32_bf16 v[12:15], v[132:135], v[204:207], v[12:15]
	v_mfma_f32_16x16x32_bf16 v[8:11], v[140:143], v[204:207], v[8:11]
	v_mfma_f32_16x16x32_bf16 v[60:63], v[136:139], v[152:155], v[60:63]
	v_mfma_f32_16x16x32_bf16 v[56:59], v[144:147], v[152:155], v[56:59]
	v_mfma_f32_16x16x32_bf16 v[44:47], v[136:139], v[192:195], v[44:47]
	v_mfma_f32_16x16x32_bf16 v[40:43], v[144:147], v[192:195], v[40:43]
	v_mfma_f32_16x16x32_bf16 v[28:31], v[136:139], v[200:203], v[28:31]
	v_mfma_f32_16x16x32_bf16 v[24:27], v[144:147], v[200:203], v[24:27]
	s_waitcnt lgkmcnt(0)
	v_mfma_f32_16x16x32_bf16 v[12:15], v[136:139], v[214:217], v[12:15]
	v_mfma_f32_16x16x32_bf16 v[8:11], v[144:147], v[214:217], v[8:11]
	s_setprio 0
	s_barrier
	s_add_u32 s10, s54, 0x80080
	s_addc_u32 s11, s55, 0
	s_add_i32 s54, s81, s64
	v_lshl_add_u64 v[132:133], s[10:11], 0, v[162:163]
	s_mov_b32 m0, s54
	s_nop 0
	global_load_lds_dwordx4 v[132:133], off
	v_lshl_add_u64 v[132:133], s[10:11], 0, v[166:167]
	s_add_i32 m0, s54, 0x2000
	s_nop 0
	global_load_lds_dwordx4 v[132:133], off
	s_waitcnt vmcnt(6)
	s_barrier
	s_setprio 1
	v_mfma_f32_16x16x32_bf16 v[52:55], v[218:221], v[148:151], v[52:55]
	v_mfma_f32_16x16x32_bf16 v[48:51], v[226:229], v[148:151], v[48:51]
	v_mfma_f32_16x16x32_bf16 v[36:39], v[218:221], v[156:159], v[36:39]
	v_mfma_f32_16x16x32_bf16 v[32:35], v[226:229], v[156:159], v[32:35]
	v_mfma_f32_16x16x32_bf16 v[20:23], v[218:221], v[196:199], v[20:23]
	v_mfma_f32_16x16x32_bf16 v[16:19], v[226:229], v[196:199], v[16:19]
	v_mfma_f32_16x16x32_bf16 v[4:7], v[218:221], v[204:207], v[4:7]
	v_mfma_f32_16x16x32_bf16 v[0:3], v[226:229], v[204:207], v[0:3]
	v_mfma_f32_16x16x32_bf16 v[52:55], v[222:225], v[152:155], v[52:55]
	v_mfma_f32_16x16x32_bf16 v[48:51], v[230:233], v[152:155], v[48:51]
	v_mfma_f32_16x16x32_bf16 v[36:39], v[222:225], v[192:195], v[36:39]
	v_mfma_f32_16x16x32_bf16 v[32:35], v[230:233], v[192:195], v[32:35]
	v_mfma_f32_16x16x32_bf16 v[20:23], v[222:225], v[200:203], v[20:23]
	v_mfma_f32_16x16x32_bf16 v[16:19], v[230:233], v[200:203], v[16:19]
	v_mfma_f32_16x16x32_bf16 v[4:7], v[222:225], v[214:217], v[4:7]
	v_mfma_f32_16x16x32_bf16 v[0:3], v[230:233], v[214:217], v[0:3]
	s_setprio 0
	s_add_i32 s79, s79, 2
	s_cmp_gt_u32 s79, 29
	s_mov_b64 s[10:11], s[42:43]
	s_cbranch_scc1 .Lmy_kx_0
	s_barrier
	s_branch .LBB0_319

; #define PG8_STAGE(bufoff, gbase, voff) do { _Pragma("unroll") for (int _i = 0; _i < 2; ++_i) \
;         __builtin_amdgcn_global_load_lds((const unsigned*)((const char*)(gbase) + (voff)[_i]), (LAS unsigned*)(lds + (bufoff) + ldsw + _i * 8192), 16, 0, 0); } while (0)
; #define PG8_LDA(dst, b, h) do { _Pragma("unroll") for (int m = 0; m < 4; ++m) _Pragma("unroll") for (int k = 0; k < 2; ++k) dst[m][k] = *(const LAS bf16x8*)(lds + PG8_SA(b, h) + aoff + m * 2048 + k * 1024); } while (0)
; #define PG8_LDB(dst, b, h) do { _Pragma("unroll") for (int n = 0; n < 2; ++n) _Pragma("unroll") for (int k = 0; k < 2; ++k) dst[n][k] = *(const LAS bf16x8*)(lds + PG8_SB(b, h) + boff + n * 2048 + k * 1024); } while (0)
; #define PG8_MMA(ai, bj, At, Bt) do { __builtin_amdgcn_s_setprio(1); _Pragma("unroll") for (int m = 0; m < 4; ++m) _Pragma("unroll") for (int n = 0; n < 2; ++n) _Pragma("unroll") for (int k = 0; k < 2; ++k) \
;         acc[ai][bj][m][n] = __builtin_amdgcn_mfma_f32_16x16x32_bf16(Bt[n][k], At[m][k], acc[ai][bj][m][n], 0, 0, 0); __builtin_amdgcn_s_setprio(0); } while (0)
; #define PG8_WAIT_L(n) asm volatile("s_waitcnt lgkmcnt(" #n ")" ::: "memory")
; #define PG8_BAR __builtin_amdgcn_s_barrier()
; #define PG8_SCHED __builtin_amdgcn_sched_barrier(0)
; template <class Epi, class Sched>
; __device__ __forceinline__ void gemm_phase(LAS unsigned char* lds, const bf16_t* A, const int K, const Sched& S, const Epi& E, const int wv) {
;     ...
;             PG8_LDB(B0, 0, 0); PG8_SCHED; PG8_LDA(At, 0, 0); PG8_STAGE_A(PG8_SA(1, 1), 1, false, k1);
;             PG8_WAIT_L(8); PG8_BAR; PG8_WAIT_L(0); PG8_MMA(0, 0, At, B0); PG8_BAR; PG8_SCHED;
;             PG8_LDB(B1, 0, 1); PG8_STAGE(PG8_SB(0, 0), b2, voffB);
;             PG8_BAR; PG8_WAIT_L(0); PG8_MMA(0, 1, At, B1); PG8_BAR;
;             PG8_LDA(At, 0, 1); PG8_STAGE_A(PG8_SA(0, 0), 0, last, k2);
;             PG8_BAR; PG8_WAIT_L(0); PG8_MMA(1, 0, At, B0); PG8_BAR; PG8_SCHED;
.Lmy_ph_1:
.LBB0_833:
	s_add_u32 s30, s28, 0x100
	ds_read_b128 v[132:135], v165
	ds_read_b128 v[136:139], v165 offset:1024
	ds_read_b128 v[140:143], v165 offset:2048
	ds_read_b128 v[156:159], v165 offset:3072
	s_addc_u32 s31, s29, 0
	s_add_u32 s69, s19, s28
	s_addc_u32 s72, s67, s29
	s_cmp_eq_u32 s68, 28
	s_cselect_b64 s[70:71], -1, 0
	s_and_b64 s[34:35], s[70:71], exec
	s_cselect_b32 s73, 0, s30
	s_cselect_b32 s35, s17, s72
	s_cselect_b32 s34, s66, s69
	v_lshl_add_u64 v[160:161], v[128:129], 0, s[28:29]
	s_add_i32 m0, s25, 0xc000
	ds_read_b128 v[168:171], v166
	ds_read_b128 v[172:175], v166 offset:1024
	ds_read_b128 v[176:179], v166 offset:2048
	ds_read_b128 v[180:183], v166 offset:3072
	ds_read_b128 v[184:187], v166 offset:4096
	ds_read_b128 v[188:191], v166 offset:5120
	ds_read_b128 v[192:195], v166 offset:6144
	ds_read_b128 v[196:199], v166 offset:7168
	global_load_lds_dwordx4 v[160:161], off
	v_lshl_add_u64 v[160:161], v[130:131], 0, s[28:29]
	s_add_i32 m0, s25, 0xe000
	s_nop 0
	global_load_lds_dwordx4 v[160:161], off
	s_waitcnt lgkmcnt(8)
	s_barrier
	s_setprio 1
	s_waitcnt lgkmcnt(7)
	v_mfma_f32_16x16x32_bf16 v[124:127], v[132:135], v[168:171], v[124:127]
	v_mfma_f32_16x16x32_bf16 v[120:123], v[140:143], v[168:171], v[120:123]
	s_waitcnt lgkmcnt(5)
	v_mfma_f32_16x16x32_bf16 v[116:119], v[132:135], v[176:179], v[116:119]
	v_mfma_f32_16x16x32_bf16 v[112:115], v[140:143], v[176:179], v[112:115]
	s_waitcnt lgkmcnt(3)
	v_mfma_f32_16x16x32_bf16 v[108:111], v[132:135], v[184:187], v[108:111]
	v_mfma_f32_16x16x32_bf16 v[96:99], v[140:143], v[184:187], v[96:99]
	s_waitcnt lgkmcnt(1)
	v_mfma_f32_16x16x32_bf16 v[80:83], v[132:135], v[192:195], v[80:83]
	v_mfma_f32_16x16x32_bf16 v[72:75], v[140:143], v[192:195], v[72:75]
	v_mfma_f32_16x16x32_bf16 v[124:127], v[136:139], v[172:175], v[124:127]
	v_mfma_f32_16x16x32_bf16 v[120:123], v[156:159], v[172:175], v[120:123]
	v_mfma_f32_16x16x32_bf16 v[116:119], v[136:139], v[180:183], v[116:119]
	v_mfma_f32_16x16x32_bf16 v[112:115], v[156:159], v[180:183], v[112:115]
	v_mfma_f32_16x16x32_bf16 v[108:111], v[136:139], v[188:191], v[108:111]
	v_mfma_f32_16x16x32_bf16 v[96:99], v[156:159], v[188:191], v[96:99]
	s_waitcnt lgkmcnt(0)
	v_mfma_f32_16x16x32_bf16 v[80:83], v[136:139], v[196:199], v[80:83]
	v_mfma_f32_16x16x32_bf16 v[72:75], v[156:159], v[196:199], v[72:75]
	s_setprio 0
	s_barrier
	s_add_i32 s28, s63, s41
	v_lshl_add_u64 v[160:161], s[34:35], 0, v[144:145]
	s_mov_b32 m0, s28
	ds_read_b128 v[200:203], v167
	ds_read_b128 v[204:207], v167 offset:1024
	ds_read_b128 v[208:211], v167 offset:2048
	ds_read_b128 v[212:215], v167 offset:3072
	global_load_lds_dwordx4 v[160:161], off
	v_lshl_add_u64 v[216:217], s[34:35], 0, v[146:147]
	s_add_i32 m0, s28, 0x2000
	s_nop 0
	global_load_lds_dwordx4 v[216:217], off
	s_barrier
	s_setprio 1
	s_waitcnt lgkmcnt(3)
	v_mfma_f32_16x16x32_bf16 v[104:107], v[200:203], v[168:171], v[104:107]
	s_waitcnt lgkmcnt(1)
	v_mfma_f32_16x16x32_bf16 v[100:103], v[208:211], v[168:171], v[100:103]
	v_mfma_f32_16x16x32_bf16 v[92:95], v[200:203], v[176:179], v[92:95]
	v_mfma_f32_16x16x32_bf16 v[88:91], v[208:211], v[176:179], v[88:91]
	v_mfma_f32_16x16x32_bf16 v[84:87], v[200:203], v[184:187], v[84:87]
	v_mfma_f32_16x16x32_bf16 v[76:79], v[208:211], v[184:187], v[76:79]
	v_mfma_f32_16x16x32_bf16 v[68:71], v[200:203], v[192:195], v[68:71]
	v_mfma_f32_16x16x32_bf16 v[64:67], v[208:211], v[192:195], v[64:67]
	v_mfma_f32_16x16x32_bf16 v[104:107], v[204:207], v[172:175], v[104:107]
	s_waitcnt lgkmcnt(0)
	v_mfma_f32_16x16x32_bf16 v[100:103], v[212:215], v[172:175], v[100:103]
	v_mfma_f32_16x16x32_bf16 v[92:95], v[204:207], v[180:183], v[92:95]
	v_mfma_f32_16x16x32_bf16 v[88:91], v[212:215], v[180:183], v[88:91]
	v_mfma_f32_16x16x32_bf16 v[84:87], v[204:207], v[188:191], v[84:87]
	v_mfma_f32_16x16x32_bf16 v[76:79], v[212:215], v[188:191], v[76:79]
	v_mfma_f32_16x16x32_bf16 v[68:71], v[204:207], v[196:199], v[68:71]
	v_mfma_f32_16x16x32_bf16 v[64:67], v[212:215], v[196:199], v[64:67]
	s_setprio 0
	s_and_b64 s[28:29], s[4:5], s[70:71]
	s_and_b64 s[28:29], s[28:29], exec
	s_cselect_b32 s28, s22, s26
	s_cselect_b32 s29, s23, s27
	s_add_u32 s28, s28, s73
	s_addc_u32 s29, s29, 0
	s_mov_b32 m0, s25
	v_lshl_add_u64 v[218:219], s[28:29], 0, v[144:145]
	s_barrier
	ds_read_b128 v[168:171], v166 offset:16384
	ds_read_b128 v[172:175], v166 offset:17408
	ds_read_b128 v[176:179], v166 offset:18432
	ds_read_b128 v[180:183], v166 offset:19456
	ds_read_b128 v[184:187], v166 offset:20480
	ds_read_b128 v[188:191], v166 offset:21504
	ds_read_b128 v[192:195], v166 offset:22528
	ds_read_b128 v[196:199], v166 offset:23552
	global_load_lds_dwordx4 v[218:219], off
	v_lshl_add_u64 v[220:221], s[28:29], 0, v[146:147]
	s_mov_b32 m0, s42
	s_nop 0
	global_load_lds_dwordx4 v[220:221], off
	s_barrier
	s_setprio 1
	s_waitcnt lgkmcnt(7)
	v_mfma_f32_16x16x32_bf16 v[60:63], v[132:135], v[168:171], v[60:63]
	v_mfma_f32_16x16x32_bf16 v[56:59], v[140:143], v[168:171], v[56:59]
	s_waitcnt lgkmcnt(5)
	v_mfma_f32_16x16x32_bf16 v[52:55], v[132:135], v[176:179], v[52:55]
	v_mfma_f32_16x16x32_bf16 v[48:51], v[140:143], v[176:179], v[48:51]
	s_waitcnt lgkmcnt(3)
	v_mfma_f32_16x16x32_bf16 v[44:47], v[132:135], v[184:187], v[44:47]
	v_mfma_f32_16x16x32_bf16 v[32:35], v[140:143], v[184:187], v[32:35]
	s_waitcnt lgkmcnt(1)
	v_mfma_f32_16x16x32_bf16 v[16:19], v[132:135], v[192:195], v[16:19]
	v_mfma_f32_16x16x32_bf16 v[8:11], v[140:143], v[192:195], v[8:11]
	v_mfma_f32_16x16x32_bf16 v[60:63], v[136:139], v[172:175], v[60:63]
	v_mfma_f32_16x16x32_bf16 v[56:59], v[156:159], v[172:175], v[56:59]
	v_mfma_f32_16x16x32_bf16 v[52:55], v[136:139], v[180:183], v[52:55]
	v_mfma_f32_16x16x32_bf16 v[48:51], v[156:159], v[180:183], v[48:51]
	v_mfma_f32_16x16x32_bf16 v[44:47], v[136:139], v[188:191], v[44:47]
	v_mfma_f32_16x16x32_bf16 v[32:35], v[156:159], v[188:191], v[32:35]
	s_waitcnt lgkmcnt(0)
	v_mfma_f32_16x16x32_bf16 v[16:19], v[136:139], v[196:199], v[16:19]
	v_mfma_f32_16x16x32_bf16 v[8:11], v[156:159], v[196:199], v[8:11]
	s_setprio 0
	s_barrier
; #define PG8_STAGE(bufoff, gbase, voff) do { _Pragma("unroll") for (int _i = 0; _i < 2; ++_i) \
;         __builtin_amdgcn_global_load_lds((const unsigned*)((const char*)(gbase) + (voff)[_i]), (LAS unsigned*)(lds + (bufoff) + ldsw + _i * 8192), 16, 0, 0); } while (0)
; #define PG8_LDA(dst, b, h) do { _Pragma("unroll") for (int m = 0; m < 4; ++m) _Pragma("unroll") for (int k = 0; k < 2; ++k) dst[m][k] = *(const LAS bf16x8*)(lds + PG8_SA(b, h) + aoff + m * 2048 + k * 1024); } while (0)
; #define PG8_LDB(dst, b, h) do { _Pragma("unroll") for (int n = 0; n < 2; ++n) _Pragma("unroll") for (int k = 0; k < 2; ++k) dst[n][k] = *(const LAS bf16x8*)(lds + PG8_SB(b, h) + boff + n * 2048 + k * 1024); } while (0)
; #define PG8_MMA(ai, bj, At, Bt) do { __builtin_amdgcn_s_setprio(1); _Pragma("unroll") for (int m = 0; m < 4; ++m) _Pragma("unroll") for (int n = 0; n < 2; ++n) _Pragma("unroll") for (int k = 0; k < 2; ++k) \
;         acc[ai][bj][m][n] = __builtin_amdgcn_mfma_f32_16x16x32_bf16(Bt[n][k], At[m][k], acc[ai][bj][m][n], 0, 0, 0); __builtin_amdgcn_s_setprio(0); } while (0)
; #define PG8_WAIT_V(n) asm volatile("s_waitcnt vmcnt(" #n ")" ::: "memory")
; #define PG8_WAIT_L(n) asm volatile("s_waitcnt lgkmcnt(" #n ")" ::: "memory")
; #define PG8_BAR __builtin_amdgcn_s_barrier()
; #define PG8_SCHED __builtin_amdgcn_sched_barrier(0)
; template <class Epi, class Sched>
; __device__ __forceinline__ void gemm_phase(LAS unsigned char* lds, const bf16_t* A, const int K, const Sched& S, const Epi& E, const int wv) {
;     ...
;             PG8_STAGE(PG8_SB(0, 1), b2 + hstep, voffB);
;             PG8_WAIT_V(6); PG8_BAR; PG8_MMA(1, 1, At, B1); PG8_BAR;
;             PG8_LDB(B0, 1, 0); PG8_SCHED; PG8_LDA(At, 1, 0); PG8_STAGE_A(PG8_SA(0, 1), 1, last, k2);
;             PG8_WAIT_L(8); PG8_BAR; PG8_WAIT_L(0); PG8_MMA(0, 0, At, B0); PG8_BAR; PG8_SCHED;
;             PG8_LDB(B1, 1, 1); PG8_STAGE(PG8_SB(1, 0), b3, voffB);
	s_add_u32 s70, s34, 0x80000
	s_addc_u32 s71, s35, 0
	s_add_i32 s69, s64, s41
	v_lshl_add_u64 v[132:133], s[70:71], 0, v[144:145]
	s_mov_b32 m0, s69
	s_nop 0
	global_load_lds_dwordx4 v[132:133], off
	v_lshl_add_u64 v[132:133], s[70:71], 0, v[146:147]
	s_add_i32 m0, s69, 0x2000
	s_nop 0
	global_load_lds_dwordx4 v[132:133], off
	s_waitcnt vmcnt(6)
	s_barrier
	s_setprio 1
	v_mfma_f32_16x16x32_bf16 v[40:43], v[200:203], v[168:171], v[40:43]
	v_mfma_f32_16x16x32_bf16 v[36:39], v[208:211], v[168:171], v[36:39]
	v_mfma_f32_16x16x32_bf16 v[28:31], v[200:203], v[176:179], v[28:31]
	v_mfma_f32_16x16x32_bf16 v[24:27], v[208:211], v[176:179], v[24:27]
	v_mfma_f32_16x16x32_bf16 v[20:23], v[200:203], v[184:187], v[20:23]
	v_mfma_f32_16x16x32_bf16 v[12:15], v[208:211], v[184:187], v[12:15]
	v_mfma_f32_16x16x32_bf16 v[4:7], v[200:203], v[192:195], v[4:7]
	v_mfma_f32_16x16x32_bf16 v[0:3], v[208:211], v[192:195], v[0:3]
	v_mfma_f32_16x16x32_bf16 v[40:43], v[204:207], v[172:175], v[40:43]
	v_mfma_f32_16x16x32_bf16 v[36:39], v[212:215], v[172:175], v[36:39]
	v_mfma_f32_16x16x32_bf16 v[28:31], v[204:207], v[180:183], v[28:31]
	v_mfma_f32_16x16x32_bf16 v[24:27], v[212:215], v[180:183], v[24:27]
	v_mfma_f32_16x16x32_bf16 v[20:23], v[204:207], v[188:191], v[20:23]
	v_mfma_f32_16x16x32_bf16 v[12:15], v[212:215], v[188:191], v[12:15]
	v_mfma_f32_16x16x32_bf16 v[4:7], v[204:207], v[196:199], v[4:7]
	v_mfma_f32_16x16x32_bf16 v[0:3], v[212:215], v[196:199], v[0:3]
	s_setprio 0
	s_add_i32 s69, 0, 0x18000
	v_add_u32_e32 v156, s69, v163
	s_barrier
	ds_read_b128 v[132:135], v156
	ds_read_b128 v[136:139], v156 offset:1024
	ds_read_b128 v[140:143], v156 offset:2048
	ds_read_b128 v[156:159], v156 offset:3072
	s_add_u32 s28, s28, 0x80000
	s_addc_u32 s29, s29, 0
	s_mov_b32 m0, s43
	v_lshl_add_u64 v[200:201], s[28:29], 0, v[144:145]
	ds_read_b128 v[168:171], v166 offset:32768
	ds_read_b128 v[172:175], v166 offset:33792
	ds_read_b128 v[176:179], v166 offset:34816
	ds_read_b128 v[180:183], v166 offset:35840
	ds_read_b128 v[184:187], v166 offset:36864
	ds_read_b128 v[188:191], v166 offset:37888
	ds_read_b128 v[192:195], v166 offset:38912
	ds_read_b128 v[196:199], v166 offset:39936
	global_load_lds_dwordx4 v[200:201], off
	v_lshl_add_u64 v[200:201], s[28:29], 0, v[146:147]
	s_mov_b32 m0, s50
	s_nop 0
	global_load_lds_dwordx4 v[200:201], off
	s_waitcnt lgkmcnt(8)
	s_barrier
	s_setprio 1
	s_waitcnt lgkmcnt(7)
	v_mfma_f32_16x16x32_bf16 v[124:127], v[132:135], v[168:171], v[124:127]
	v_mfma_f32_16x16x32_bf16 v[120:123], v[140:143], v[168:171], v[120:123]
	s_waitcnt lgkmcnt(5)
	v_mfma_f32_16x16x32_bf16 v[116:119], v[132:135], v[176:179], v[116:119]
	v_mfma_f32_16x16x32_bf16 v[112:115], v[140:143], v[176:179], v[112:115]
	s_waitcnt lgkmcnt(3)
	v_mfma_f32_16x16x32_bf16 v[108:111], v[132:135], v[184:187], v[108:111]
	v_mfma_f32_16x16x32_bf16 v[96:99], v[140:143], v[184:187], v[96:99]
	s_waitcnt lgkmcnt(1)
	v_mfma_f32_16x16x32_bf16 v[80:83], v[132:135], v[192:195], v[80:83]
	v_mfma_f32_16x16x32_bf16 v[72:75], v[140:143], v[192:195], v[72:75]
	v_mfma_f32_16x16x32_bf16 v[124:127], v[136:139], v[172:175], v[124:127]
	v_mfma_f32_16x16x32_bf16 v[120:123], v[156:159], v[172:175], v[120:123]
	v_mfma_f32_16x16x32_bf16 v[116:119], v[136:139], v[180:183], v[116:119]
	v_mfma_f32_16x16x32_bf16 v[112:115], v[156:159], v[180:183], v[112:115]
	v_mfma_f32_16x16x32_bf16 v[108:111], v[136:139], v[188:191], v[108:111]
	v_mfma_f32_16x16x32_bf16 v[96:99], v[156:159], v[188:191], v[96:99]
	s_waitcnt lgkmcnt(0)
	v_mfma_f32_16x16x32_bf16 v[80:83], v[136:139], v[196:199], v[80:83]
	v_mfma_f32_16x16x32_bf16 v[72:75], v[156:159], v[196:199], v[72:75]
	s_setprio 0
	s_barrier
	s_add_i32 s70, 0, 0x1c000
	s_add_i32 s28, s69, s41
	v_add_u32_e32 v212, s70, v163
	v_lshl_add_u64 v[160:161], v[160:161], 0, s[8:9]
	s_mov_b32 m0, s28
	ds_read_b128 v[200:203], v212
	ds_read_b128 v[204:207], v212 offset:1024
	ds_read_b128 v[208:211], v212 offset:2048
	ds_read_b128 v[212:215], v212 offset:3072
	global_load_lds_dwordx4 v[160:161], off
	v_lshl_add_u64 v[160:161], v[216:217], 0, s[8:9]
	s_add_i32 m0, s28, 0x2000
	s_nop 0
	global_load_lds_dwordx4 v[160:161], off
	s_barrier
; #define PG8_STAGE(bufoff, gbase, voff) do { _Pragma("unroll") for (int _i = 0; _i < 2; ++_i) \
;         __builtin_amdgcn_global_load_lds((const unsigned*)((const char*)(gbase) + (voff)[_i]), (LAS unsigned*)(lds + (bufoff) + ldsw + _i * 8192), 16, 0, 0); } while (0)
; #define PG8_LDA(dst, b, h) do { _Pragma("unroll") for (int m = 0; m < 4; ++m) _Pragma("unroll") for (int k = 0; k < 2; ++k) dst[m][k] = *(const LAS bf16x8*)(lds + PG8_SA(b, h) + aoff + m * 2048 + k * 1024); } while (0)
; #define PG8_LDB(dst, b, h) do { _Pragma("unroll") for (int n = 0; n < 2; ++n) _Pragma("unroll") for (int k = 0; k < 2; ++k) dst[n][k] = *(const LAS bf16x8*)(lds + PG8_SB(b, h) + boff + n * 2048 + k * 1024); } while (0)
; #define PG8_MMA(ai, bj, At, Bt) do { __builtin_amdgcn_s_setprio(1); _Pragma("unroll") for (int m = 0; m < 4; ++m) _Pragma("unroll") for (int n = 0; n < 2; ++n) _Pragma("unroll") for (int k = 0; k < 2; ++k) \
;         acc[ai][bj][m][n] = __builtin_amdgcn_mfma_f32_16x16x32_bf16(Bt[n][k], At[m][k], acc[ai][bj][m][n], 0, 0, 0); __builtin_amdgcn_s_setprio(0); } while (0)
; #define PG8_WAIT_V(n) asm volatile("s_waitcnt vmcnt(" #n ")" ::: "memory")
; #define PG8_WAIT_L(n) asm volatile("s_waitcnt lgkmcnt(" #n ")" ::: "memory")
; #define PG8_BAR __builtin_amdgcn_s_barrier()
; #define PG8_SCHED __builtin_amdgcn_sched_barrier(0)
; template <class Epi, class Sched>
; __device__ __forceinline__ void gemm_phase(LAS unsigned char* lds, const bf16_t* A, const int K, const Sched& S, const Epi& E, const int wv) {
;     ...
;             PG8_LDB(B1, 1, 1); PG8_STAGE(PG8_SB(1, 0), b3, voffB);
;             PG8_BAR; PG8_WAIT_L(0); PG8_MMA(0, 1, At, B1); PG8_BAR;
;             PG8_LDA(At, 1, 1); PG8_STAGE_A(PG8_SA(1, 0), 0, last, k3);
;             PG8_BAR; PG8_WAIT_L(0); PG8_MMA(1, 0, At, B0); PG8_BAR; PG8_SCHED;
;             PG8_STAGE(PG8_SB(1, 1), b3 + hstep, voffB);
;             PG8_WAIT_V(6); PG8_BAR; PG8_MMA(1, 1, At, B1); PG8_BAR;
;         }
	s_setprio 1
	s_waitcnt lgkmcnt(3)
	v_mfma_f32_16x16x32_bf16 v[104:107], v[200:203], v[168:171], v[104:107]
	s_waitcnt lgkmcnt(1)
	v_mfma_f32_16x16x32_bf16 v[100:103], v[208:211], v[168:171], v[100:103]
	v_mfma_f32_16x16x32_bf16 v[92:95], v[200:203], v[176:179], v[92:95]
	v_mfma_f32_16x16x32_bf16 v[88:91], v[208:211], v[176:179], v[88:91]
	v_mfma_f32_16x16x32_bf16 v[84:87], v[200:203], v[184:187], v[84:87]
	v_mfma_f32_16x16x32_bf16 v[76:79], v[208:211], v[184:187], v[76:79]
	v_mfma_f32_16x16x32_bf16 v[68:71], v[200:203], v[192:195], v[68:71]
	v_mfma_f32_16x16x32_bf16 v[64:67], v[208:211], v[192:195], v[64:67]
	v_mfma_f32_16x16x32_bf16 v[104:107], v[204:207], v[172:175], v[104:107]
	s_waitcnt lgkmcnt(0)
	v_mfma_f32_16x16x32_bf16 v[100:103], v[212:215], v[172:175], v[100:103]
	v_mfma_f32_16x16x32_bf16 v[92:95], v[204:207], v[180:183], v[92:95]
	v_mfma_f32_16x16x32_bf16 v[88:91], v[212:215], v[180:183], v[88:91]
	v_mfma_f32_16x16x32_bf16 v[84:87], v[204:207], v[188:191], v[84:87]
	v_mfma_f32_16x16x32_bf16 v[76:79], v[212:215], v[188:191], v[76:79]
	v_mfma_f32_16x16x32_bf16 v[68:71], v[204:207], v[196:199], v[68:71]
	v_mfma_f32_16x16x32_bf16 v[64:67], v[212:215], v[196:199], v[64:67]
	s_setprio 0
	s_mov_b32 m0, s60
	v_lshl_add_u64 v[160:161], v[218:219], 0, s[8:9]
	s_barrier
	ds_read_b128 v[168:171], v166 offset:49152
	ds_read_b128 v[172:175], v166 offset:50176
	ds_read_b128 v[176:179], v166 offset:51200
	ds_read_b128 v[180:183], v166 offset:52224
	ds_read_b128 v[184:187], v166 offset:53248
	ds_read_b128 v[188:191], v166 offset:54272
	ds_read_b128 v[192:195], v166 offset:55296
	ds_read_b128 v[196:199], v166 offset:56320
	global_load_lds_dwordx4 v[160:161], off
	v_lshl_add_u64 v[160:161], v[220:221], 0, s[8:9]
	s_mov_b32 m0, s61
	s_nop 0
	global_load_lds_dwordx4 v[160:161], off
	s_barrier
	s_setprio 1
	s_waitcnt lgkmcnt(7)
	v_mfma_f32_16x16x32_bf16 v[60:63], v[132:135], v[168:171], v[60:63]
	v_mfma_f32_16x16x32_bf16 v[56:59], v[140:143], v[168:171], v[56:59]
	s_waitcnt lgkmcnt(5)
	v_mfma_f32_16x16x32_bf16 v[52:55], v[132:135], v[176:179], v[52:55]
	v_mfma_f32_16x16x32_bf16 v[48:51], v[140:143], v[176:179], v[48:51]
	s_waitcnt lgkmcnt(3)
	v_mfma_f32_16x16x32_bf16 v[44:47], v[132:135], v[184:187], v[44:47]
	v_mfma_f32_16x16x32_bf16 v[32:35], v[140:143], v[184:187], v[32:35]
	s_waitcnt lgkmcnt(1)
	v_mfma_f32_16x16x32_bf16 v[16:19], v[132:135], v[192:195], v[16:19]
	v_mfma_f32_16x16x32_bf16 v[8:11], v[140:143], v[192:195], v[8:11]
	v_mfma_f32_16x16x32_bf16 v[60:63], v[136:139], v[172:175], v[60:63]
	v_mfma_f32_16x16x32_bf16 v[56:59], v[156:159], v[172:175], v[56:59]
	v_mfma_f32_16x16x32_bf16 v[52:55], v[136:139], v[180:183], v[52:55]
	v_mfma_f32_16x16x32_bf16 v[48:51], v[156:159], v[180:183], v[48:51]
	v_mfma_f32_16x16x32_bf16 v[44:47], v[136:139], v[188:191], v[44:47]
	v_mfma_f32_16x16x32_bf16 v[32:35], v[156:159], v[188:191], v[32:35]
	s_waitcnt lgkmcnt(0)
	v_mfma_f32_16x16x32_bf16 v[16:19], v[136:139], v[196:199], v[16:19]
	v_mfma_f32_16x16x32_bf16 v[8:11], v[156:159], v[196:199], v[8:11]
	s_setprio 0
	s_barrier
	s_add_u32 s28, s34, 0x80080
	s_addc_u32 s29, s35, 0
	s_add_i32 s34, s70, s41
	v_lshl_add_u64 v[132:133], s[28:29], 0, v[144:145]
	s_mov_b32 m0, s34
	s_nop 0
	global_load_lds_dwordx4 v[132:133], off
	v_lshl_add_u64 v[132:133], s[28:29], 0, v[146:147]
	s_add_i32 m0, s34, 0x2000
	s_nop 0
	global_load_lds_dwordx4 v[132:133], off
	s_waitcnt vmcnt(6)
	s_barrier
	s_setprio 1
	v_mfma_f32_16x16x32_bf16 v[40:43], v[200:203], v[168:171], v[40:43]
	v_mfma_f32_16x16x32_bf16 v[36:39], v[208:211], v[168:171], v[36:39]
	v_mfma_f32_16x16x32_bf16 v[28:31], v[200:203], v[176:179], v[28:31]
	v_mfma_f32_16x16x32_bf16 v[24:27], v[208:211], v[176:179], v[24:27]
	v_mfma_f32_16x16x32_bf16 v[20:23], v[200:203], v[184:187], v[20:23]
	v_mfma_f32_16x16x32_bf16 v[12:15], v[208:211], v[184:187], v[12:15]
	v_mfma_f32_16x16x32_bf16 v[4:7], v[200:203], v[192:195], v[4:7]
	v_mfma_f32_16x16x32_bf16 v[0:3], v[208:211], v[192:195], v[0:3]
	v_mfma_f32_16x16x32_bf16 v[40:43], v[204:207], v[172:175], v[40:43]
	v_mfma_f32_16x16x32_bf16 v[36:39], v[212:215], v[172:175], v[36:39]
	v_mfma_f32_16x16x32_bf16 v[28:31], v[204:207], v[180:183], v[28:31]
	v_mfma_f32_16x16x32_bf16 v[24:27], v[212:215], v[180:183], v[24:27]
	v_mfma_f32_16x16x32_bf16 v[20:23], v[204:207], v[188:191], v[20:23]
	v_mfma_f32_16x16x32_bf16 v[12:15], v[212:215], v[188:191], v[12:15]
	v_mfma_f32_16x16x32_bf16 v[4:7], v[204:207], v[196:199], v[4:7]
	v_mfma_f32_16x16x32_bf16 v[0:3], v[212:215], v[196:199], v[0:3]
	s_setprio 0
	s_add_i32 s68, s68, 2
	s_cmp_gt_u32 s68, 29
	s_mov_b64 s[28:29], s[30:31]
	s_cbranch_scc1 .Lmy_kx_1
	s_barrier
	s_branch .LBB0_833

; #define PG8_STAGE(bufoff, gbase, voff) do { _Pragma("unroll") for (int _i = 0; _i < 2; ++_i) \
;         __builtin_amdgcn_global_load_lds((const unsigned*)((const char*)(gbase) + (voff)[_i]), (LAS unsigned*)(lds + (bufoff) + ldsw + _i * 8192), 16, 0, 0); } while (0)
; #define PG8_LDA(dst, b, h) do { _Pragma("unroll") for (int m = 0; m < 4; ++m) _Pragma("unroll") for (int k = 0; k < 2; ++k) dst[m][k] = *(const LAS bf16x8*)(lds + PG8_SA(b, h) + aoff + m * 2048 + k * 1024); } while (0)
; #define PG8_LDB(dst, b, h) do { _Pragma("unroll") for (int n = 0; n < 2; ++n) _Pragma("unroll") for (int k = 0; k < 2; ++k) dst[n][k] = *(const LAS bf16x8*)(lds + PG8_SB(b, h) + boff + n * 2048 + k * 1024); } while (0)
; #define PG8_MMA(ai, bj, At, Bt) do { __builtin_amdgcn_s_setprio(1); _Pragma("unroll") for (int m = 0; m < 4; ++m) _Pragma("unroll") for (int n = 0; n < 2; ++n) _Pragma("unroll") for (int k = 0; k < 2; ++k) \
;         acc[ai][bj][m][n] = __builtin_amdgcn_mfma_f32_16x16x32_bf16(Bt[n][k], At[m][k], acc[ai][bj][m][n], 0, 0, 0); __builtin_amdgcn_s_setprio(0); } while (0)
; #define PG8_WAIT_L(n) asm volatile("s_waitcnt lgkmcnt(" #n ")" ::: "memory")
; #define PG8_BAR __builtin_amdgcn_s_barrier()
; #define PG8_SCHED __builtin_amdgcn_sched_barrier(0)
; template <class Epi, class Sched>
; __device__ __forceinline__ void gemm_phase(LAS unsigned char* lds, const bf16_t* A, const int K, const Sched& S, const Epi& E, const int wv) {
;     ...
;             PG8_LDB(B0, 0, 0); PG8_SCHED; PG8_LDA(At, 0, 0); PG8_STAGE_A(PG8_SA(1, 1), 1, false, k1);
;             PG8_WAIT_L(8); PG8_BAR; PG8_WAIT_L(0); PG8_MMA(0, 0, At, B0); PG8_BAR; PG8_SCHED;
;             PG8_LDB(B1, 0, 1); PG8_STAGE(PG8_SB(0, 0), b2, voffB);
;             PG8_BAR; PG8_WAIT_L(0); PG8_MMA(0, 1, At, B1); PG8_BAR;
;             PG8_LDA(At, 0, 1); PG8_STAGE_A(PG8_SA(0, 0), 0, last, k2);
;             PG8_BAR; PG8_WAIT_L(0); PG8_MMA(1, 0, At, B0); PG8_BAR; PG8_SCHED;
.Lmy_ph_2:
.LBB0_1008:
	v_add_u32_e32 v132, s64, v149
	s_add_u32 s22, s0, 0x100
	ds_read_b128 v[174:177], v132
	ds_read_b128 v[178:181], v132 offset:1024
	ds_read_b128 v[182:185], v132 offset:2048
	ds_read_b128 v[186:189], v132 offset:3072
	s_addc_u32 s23, s1, 0
	s_add_u32 s81, s15, s0
	s_addc_u32 s82, s17, s1
	s_cmpk_eq_i32 s0, 0xf00
	s_cselect_b64 vcc, -1, 0
	s_and_b64 s[24:25], vcc, exec
	s_cselect_b32 s83, 0, s22
	s_cselect_b32 s25, s19, s82
	s_cselect_b32 s24, s18, s81
	s_mov_b32 m0, s66
	v_lshl_add_u64 v[222:223], v[142:143], 0, s[0:1]
	ds_read_b128 v[190:193], v167
	ds_read_b128 v[194:197], v167 offset:1024
	ds_read_b128 v[198:201], v167 offset:2048
	ds_read_b128 v[202:205], v167 offset:3072
	ds_read_b128 v[206:209], v167 offset:4096
	ds_read_b128 v[210:213], v167 offset:5120
	ds_read_b128 v[214:217], v167 offset:6144
	ds_read_b128 v[218:221], v167 offset:7168
	global_load_lds_dwordx4 v[222:223], off
	v_lshl_add_u64 v[222:223], v[140:141], 0, s[0:1]
	s_mov_b32 m0, s67
	s_nop 0
	global_load_lds_dwordx4 v[222:223], off
	s_waitcnt lgkmcnt(8)
	s_barrier
	s_setprio 1
	s_waitcnt lgkmcnt(7)
	v_mfma_f32_16x16x32_bf16 v[124:127], v[174:177], v[190:193], v[124:127]
	v_mfma_f32_16x16x32_bf16 v[120:123], v[182:185], v[190:193], v[120:123]
	s_waitcnt lgkmcnt(5)
	v_mfma_f32_16x16x32_bf16 v[108:111], v[174:177], v[198:201], v[108:111]
	v_mfma_f32_16x16x32_bf16 v[104:107], v[182:185], v[198:201], v[104:107]
	s_waitcnt lgkmcnt(3)
	v_mfma_f32_16x16x32_bf16 v[92:95], v[174:177], v[206:209], v[92:95]
	v_mfma_f32_16x16x32_bf16 v[88:91], v[182:185], v[206:209], v[88:91]
	s_waitcnt lgkmcnt(1)
	v_mfma_f32_16x16x32_bf16 v[76:79], v[174:177], v[214:217], v[76:79]
	v_mfma_f32_16x16x32_bf16 v[72:75], v[182:185], v[214:217], v[72:75]
	v_mfma_f32_16x16x32_bf16 v[124:127], v[178:181], v[194:197], v[124:127]
	v_mfma_f32_16x16x32_bf16 v[120:123], v[186:189], v[194:197], v[120:123]
	v_mfma_f32_16x16x32_bf16 v[108:111], v[178:181], v[202:205], v[108:111]
	v_mfma_f32_16x16x32_bf16 v[104:107], v[186:189], v[202:205], v[104:107]
	v_mfma_f32_16x16x32_bf16 v[92:95], v[178:181], v[210:213], v[92:95]
	v_mfma_f32_16x16x32_bf16 v[88:91], v[186:189], v[210:213], v[88:91]
	s_waitcnt lgkmcnt(0)
	v_mfma_f32_16x16x32_bf16 v[76:79], v[178:181], v[218:221], v[76:79]
	v_mfma_f32_16x16x32_bf16 v[72:75], v[186:189], v[218:221], v[72:75]
	s_setprio 0
	s_barrier
	s_mov_b32 m0, s68
	v_add_u32_e32 v132, s65, v149
	v_lshl_add_u64 v[238:239], s[24:25], 0, v[128:129]
	ds_read_b128 v[222:225], v132
	ds_read_b128 v[226:229], v132 offset:1024
	ds_read_b128 v[230:233], v132 offset:2048
	ds_read_b128 v[234:237], v132 offset:3072
	global_load_lds_dwordx4 v[238:239], off
	v_lshl_add_u64 v[240:241], s[24:25], 0, v[130:131]
	s_mov_b32 m0, s69
	s_nop 0
	global_load_lds_dwordx4 v[240:241], off
	s_barrier
	s_setprio 1
	s_waitcnt lgkmcnt(3)
	v_mfma_f32_16x16x32_bf16 v[116:119], v[222:225], v[190:193], v[116:119]
	s_waitcnt lgkmcnt(1)
	v_mfma_f32_16x16x32_bf16 v[112:115], v[230:233], v[190:193], v[112:115]
	v_mfma_f32_16x16x32_bf16 v[100:103], v[222:225], v[198:201], v[100:103]
	v_mfma_f32_16x16x32_bf16 v[96:99], v[230:233], v[198:201], v[96:99]
	v_mfma_f32_16x16x32_bf16 v[84:87], v[222:225], v[206:209], v[84:87]
	v_mfma_f32_16x16x32_bf16 v[80:83], v[230:233], v[206:209], v[80:83]
	v_mfma_f32_16x16x32_bf16 v[68:71], v[222:225], v[214:217], v[68:71]
	v_mfma_f32_16x16x32_bf16 v[64:67], v[230:233], v[214:217], v[64:67]
	v_mfma_f32_16x16x32_bf16 v[116:119], v[226:229], v[194:197], v[116:119]
	s_waitcnt lgkmcnt(0)
	v_mfma_f32_16x16x32_bf16 v[112:115], v[234:237], v[194:197], v[112:115]
	v_mfma_f32_16x16x32_bf16 v[100:103], v[226:229], v[202:205], v[100:103]
	v_mfma_f32_16x16x32_bf16 v[96:99], v[234:237], v[202:205], v[96:99]
	v_mfma_f32_16x16x32_bf16 v[84:87], v[226:229], v[210:213], v[84:87]
	v_mfma_f32_16x16x32_bf16 v[80:83], v[234:237], v[210:213], v[80:83]
	v_mfma_f32_16x16x32_bf16 v[68:71], v[226:229], v[218:221], v[68:71]
	v_mfma_f32_16x16x32_bf16 v[64:67], v[234:237], v[218:221], v[64:67]
	s_setprio 0
	s_add_u32 s0, s2, s83
	s_mov_b32 m0, s21
	s_addc_u32 s1, s3, 0
	v_cndmask_b32_e32 v132, v173, v169, vcc
	s_barrier
	ds_read_b128 v[190:193], v167 offset:16384
	ds_read_b128 v[194:197], v167 offset:17408
	ds_read_b128 v[198:201], v167 offset:18432
	ds_read_b128 v[202:205], v167 offset:19456
	ds_read_b128 v[206:209], v167 offset:20480
	ds_read_b128 v[210:213], v167 offset:21504
	ds_read_b128 v[214:217], v167 offset:22528
	ds_read_b128 v[218:221], v167 offset:23552
	v_cndmask_b32_e32 v242, v136, v171, vcc
	global_load_lds_dwordx4 v132, s[0:1]
	s_mov_b32 m0, s29
	v_mov_b32_e32 v243, v133
	global_load_lds_dwordx4 v242, s[0:1]
	s_barrier
	v_lshl_add_u64 v[244:245], s[0:1], 0, v[132:133]
	v_lshl_add_u64 v[242:243], s[0:1], 0, v[242:243]
	s_setprio 1
	s_waitcnt lgkmcnt(7)
	v_mfma_f32_16x16x32_bf16 v[52:55], v[174:177], v[190:193], v[52:55]
	v_mfma_f32_16x16x32_bf16 v[36:39], v[182:185], v[190:193], v[36:39]
	s_waitcnt lgkmcnt(5)
	v_mfma_f32_16x16x32_bf16 v[40:43], v[174:177], v[198:201], v[40:43]
	v_mfma_f32_16x16x32_bf16 v[32:35], v[182:185], v[198:201], v[32:35]
	s_waitcnt lgkmcnt(3)
	v_mfma_f32_16x16x32_bf16 v[20:23], v[174:177], v[206:209], v[20:23]
	v_mfma_f32_16x16x32_bf16 v[16:19], v[182:185], v[206:209], v[16:19]
	s_waitcnt lgkmcnt(1)
	v_mfma_f32_16x16x32_bf16 v[4:7], v[174:177], v[214:217], v[4:7]
	v_mfma_f32_16x16x32_bf16 v[0:3], v[182:185], v[214:217], v[0:3]
	v_mfma_f32_16x16x32_bf16 v[52:55], v[178:181], v[194:197], v[52:55]
	v_mfma_f32_16x16x32_bf16 v[36:39], v[186:189], v[194:197], v[36:39]
	v_mfma_f32_16x16x32_bf16 v[40:43], v[178:181], v[202:205], v[40:43]
	v_mfma_f32_16x16x32_bf16 v[32:35], v[186:189], v[202:205], v[32:35]
	v_mfma_f32_16x16x32_bf16 v[20:23], v[178:181], v[210:213], v[20:23]
	v_mfma_f32_16x16x32_bf16 v[16:19], v[186:189], v[210:213], v[16:19]
	s_waitcnt lgkmcnt(0)
	v_mfma_f32_16x16x32_bf16 v[4:7], v[178:181], v[218:221], v[4:7]
	v_mfma_f32_16x16x32_bf16 v[0:3], v[186:189], v[218:221], v[0:3]
	s_setprio 0
	s_barrier
; #define PG8_STAGE(bufoff, gbase, voff) do { _Pragma("unroll") for (int _i = 0; _i < 2; ++_i) \
;         __builtin_amdgcn_global_load_lds((const unsigned*)((const char*)(gbase) + (voff)[_i]), (LAS unsigned*)(lds + (bufoff) + ldsw + _i * 8192), 16, 0, 0); } while (0)
; #define PG8_LDA(dst, b, h) do { _Pragma("unroll") for (int m = 0; m < 4; ++m) _Pragma("unroll") for (int k = 0; k < 2; ++k) dst[m][k] = *(const LAS bf16x8*)(lds + PG8_SA(b, h) + aoff + m * 2048 + k * 1024); } while (0)
; #define PG8_LDB(dst, b, h) do { _Pragma("unroll") for (int n = 0; n < 2; ++n) _Pragma("unroll") for (int k = 0; k < 2; ++k) dst[n][k] = *(const LAS bf16x8*)(lds + PG8_SB(b, h) + boff + n * 2048 + k * 1024); } while (0)
; #define PG8_MMA(ai, bj, At, Bt) do { __builtin_amdgcn_s_setprio(1); _Pragma("unroll") for (int m = 0; m < 4; ++m) _Pragma("unroll") for (int n = 0; n < 2; ++n) _Pragma("unroll") for (int k = 0; k < 2; ++k) \
;         acc[ai][bj][m][n] = __builtin_amdgcn_mfma_f32_16x16x32_bf16(Bt[n][k], At[m][k], acc[ai][bj][m][n], 0, 0, 0); __builtin_amdgcn_s_setprio(0); } while (0)
; #define PG8_WAIT_V(n) asm volatile("s_waitcnt vmcnt(" #n ")" ::: "memory")
; #define PG8_WAIT_L(n) asm volatile("s_waitcnt lgkmcnt(" #n ")" ::: "memory")
; #define PG8_BAR __builtin_amdgcn_s_barrier()
; #define PG8_SCHED __builtin_amdgcn_sched_barrier(0)
; template <class Epi, class Sched>
; __device__ __forceinline__ void gemm_phase(LAS unsigned char* lds, const bf16_t* A, const int K, const Sched& S, const Epi& E, const int wv) {
;     ...
;             PG8_STAGE(PG8_SB(0, 1), b2 + hstep, voffB);
;             PG8_WAIT_V(6); PG8_BAR; PG8_MMA(1, 1, At, B1); PG8_BAR;
;             PG8_LDB(B0, 1, 0); PG8_SCHED; PG8_LDA(At, 1, 0); PG8_STAGE_A(PG8_SA(0, 1), 1, last, k2);
;             PG8_WAIT_L(8); PG8_BAR; PG8_WAIT_L(0); PG8_MMA(0, 0, At, B0); PG8_BAR; PG8_SCHED;
;             PG8_LDB(B1, 1, 1); PG8_STAGE(PG8_SB(1, 0), b3, voffB);
	s_add_u32 s82, s24, 0x80000
	s_addc_u32 s83, s25, 0
	s_mov_b32 m0, s70
	v_lshl_add_u64 v[174:175], s[82:83], 0, v[128:129]
	global_load_lds_dwordx4 v[174:175], off
	v_lshl_add_u64 v[174:175], s[82:83], 0, v[130:131]
	s_mov_b32 m0, s71
	s_nop 0
	global_load_lds_dwordx4 v[174:175], off
	s_waitcnt vmcnt(6)
	s_barrier
	s_setprio 1
	v_mfma_f32_16x16x32_bf16 v[60:63], v[222:225], v[190:193], v[60:63]
	v_mfma_f32_16x16x32_bf16 v[56:59], v[230:233], v[190:193], v[56:59]
	v_mfma_f32_16x16x32_bf16 v[48:51], v[222:225], v[198:201], v[48:51]
	v_mfma_f32_16x16x32_bf16 v[44:47], v[230:233], v[198:201], v[44:47]
	v_mfma_f32_16x16x32_bf16 v[28:31], v[222:225], v[206:209], v[28:31]
	v_mfma_f32_16x16x32_bf16 v[24:27], v[230:233], v[206:209], v[24:27]
	v_mfma_f32_16x16x32_bf16 v[12:15], v[222:225], v[214:217], v[12:15]
	v_mfma_f32_16x16x32_bf16 v[8:11], v[230:233], v[214:217], v[8:11]
	v_mfma_f32_16x16x32_bf16 v[60:63], v[226:229], v[194:197], v[60:63]
	v_mfma_f32_16x16x32_bf16 v[56:59], v[234:237], v[194:197], v[56:59]
	v_mfma_f32_16x16x32_bf16 v[48:51], v[226:229], v[202:205], v[48:51]
	v_mfma_f32_16x16x32_bf16 v[44:47], v[234:237], v[202:205], v[44:47]
	v_mfma_f32_16x16x32_bf16 v[28:31], v[226:229], v[210:213], v[28:31]
	v_mfma_f32_16x16x32_bf16 v[24:27], v[234:237], v[210:213], v[24:27]
	v_mfma_f32_16x16x32_bf16 v[12:15], v[226:229], v[218:221], v[12:15]
	v_mfma_f32_16x16x32_bf16 v[8:11], v[234:237], v[218:221], v[8:11]
	s_setprio 0
	v_add_u32_e32 v132, s72, v149
	s_barrier
	ds_read_b128 v[174:177], v132
	ds_read_b128 v[178:181], v132 offset:1024
	ds_read_b128 v[182:185], v132 offset:2048
	ds_read_b128 v[186:189], v132 offset:3072
	s_mov_b32 m0, s30
	v_cndmask_b32_e32 v132, v134, v170, vcc
	ds_read_b128 v[190:193], v167 offset:32768
	ds_read_b128 v[194:197], v167 offset:33792
	ds_read_b128 v[198:201], v167 offset:34816
	ds_read_b128 v[202:205], v167 offset:35840
	ds_read_b128 v[206:209], v167 offset:36864
	ds_read_b128 v[210:213], v167 offset:37888
	ds_read_b128 v[214:217], v167 offset:38912
	ds_read_b128 v[218:221], v167 offset:39936
	v_cndmask_b32_e32 v135, v138, v172, vcc
	global_load_lds_dwordx4 v132, s[0:1]
	s_mov_b32 m0, s31
	s_nop 0
	global_load_lds_dwordx4 v135, s[0:1]
	s_waitcnt lgkmcnt(8)
	s_barrier
	s_setprio 1
	s_waitcnt lgkmcnt(7)
	v_mfma_f32_16x16x32_bf16 v[124:127], v[174:177], v[190:193], v[124:127]
	v_mfma_f32_16x16x32_bf16 v[120:123], v[182:185], v[190:193], v[120:123]
	s_waitcnt lgkmcnt(5)
	v_mfma_f32_16x16x32_bf16 v[108:111], v[174:177], v[198:201], v[108:111]
	v_mfma_f32_16x16x32_bf16 v[104:107], v[182:185], v[198:201], v[104:107]
	s_waitcnt lgkmcnt(3)
	v_mfma_f32_16x16x32_bf16 v[92:95], v[174:177], v[206:209], v[92:95]
	v_mfma_f32_16x16x32_bf16 v[88:91], v[182:185], v[206:209], v[88:91]
	s_waitcnt lgkmcnt(1)
	v_mfma_f32_16x16x32_bf16 v[76:79], v[174:177], v[214:217], v[76:79]
	v_mfma_f32_16x16x32_bf16 v[72:75], v[182:185], v[214:217], v[72:75]
	v_mfma_f32_16x16x32_bf16 v[124:127], v[178:181], v[194:197], v[124:127]
	v_mfma_f32_16x16x32_bf16 v[120:123], v[186:189], v[194:197], v[120:123]
	v_mfma_f32_16x16x32_bf16 v[108:111], v[178:181], v[202:205], v[108:111]
	v_mfma_f32_16x16x32_bf16 v[104:107], v[186:189], v[202:205], v[104:107]
	v_mfma_f32_16x16x32_bf16 v[92:95], v[178:181], v[210:213], v[92:95]
	v_mfma_f32_16x16x32_bf16 v[88:91], v[186:189], v[210:213], v[88:91]
	s_waitcnt lgkmcnt(0)
	v_mfma_f32_16x16x32_bf16 v[76:79], v[178:181], v[218:221], v[76:79]
	v_mfma_f32_16x16x32_bf16 v[72:75], v[186:189], v[218:221], v[72:75]
	s_setprio 0
	s_barrier
	s_mov_b32 m0, s74
	v_add_u32_e32 v132, s73, v149
	v_lshl_add_u64 v[238:239], v[238:239], 0, s[8:9]
	ds_read_b128 v[222:225], v132
	ds_read_b128 v[226:229], v132 offset:1024
	ds_read_b128 v[230:233], v132 offset:2048
	ds_read_b128 v[234:237], v132 offset:3072
	global_load_lds_dwordx4 v[238:239], off
	v_lshl_add_u64 v[238:239], v[240:241], 0, s[8:9]
	s_mov_b32 m0, s75
	s_nop 0
	global_load_lds_dwordx4 v[238:239], off
	s_barrier
; #define PG8_STAGE(bufoff, gbase, voff) do { _Pragma("unroll") for (int _i = 0; _i < 2; ++_i) \
;         __builtin_amdgcn_global_load_lds((const unsigned*)((const char*)(gbase) + (voff)[_i]), (LAS unsigned*)(lds + (bufoff) + ldsw + _i * 8192), 16, 0, 0); } while (0)
; #define PG8_LDA(dst, b, h) do { _Pragma("unroll") for (int m = 0; m < 4; ++m) _Pragma("unroll") for (int k = 0; k < 2; ++k) dst[m][k] = *(const LAS bf16x8*)(lds + PG8_SA(b, h) + aoff + m * 2048 + k * 1024); } while (0)
; #define PG8_LDB(dst, b, h) do { _Pragma("unroll") for (int n = 0; n < 2; ++n) _Pragma("unroll") for (int k = 0; k < 2; ++k) dst[n][k] = *(const LAS bf16x8*)(lds + PG8_SB(b, h) + boff + n * 2048 + k * 1024); } while (0)
; #define PG8_MMA(ai, bj, At, Bt) do { __builtin_amdgcn_s_setprio(1); _Pragma("unroll") for (int m = 0; m < 4; ++m) _Pragma("unroll") for (int n = 0; n < 2; ++n) _Pragma("unroll") for (int k = 0; k < 2; ++k) \
;         acc[ai][bj][m][n] = __builtin_amdgcn_mfma_f32_16x16x32_bf16(Bt[n][k], At[m][k], acc[ai][bj][m][n], 0, 0, 0); __builtin_amdgcn_s_setprio(0); } while (0)
; #define PG8_WAIT_V(n) asm volatile("s_waitcnt vmcnt(" #n ")" ::: "memory")
; #define PG8_WAIT_L(n) asm volatile("s_waitcnt lgkmcnt(" #n ")" ::: "memory")
; #define PG8_BAR __builtin_amdgcn_s_barrier()
; #define PG8_SCHED __builtin_amdgcn_sched_barrier(0)
; template <class Epi, class Sched>
; __device__ __forceinline__ void gemm_phase(LAS unsigned char* lds, const bf16_t* A, const int K, const Sched& S, const Epi& E, const int wv) {
;     ...
;             PG8_LDB(B1, 1, 1); PG8_STAGE(PG8_SB(1, 0), b3, voffB);
;             PG8_BAR; PG8_WAIT_L(0); PG8_MMA(0, 1, At, B1); PG8_BAR;
;             PG8_LDA(At, 1, 1); PG8_STAGE_A(PG8_SA(1, 0), 0, last, k3);
;             PG8_BAR; PG8_WAIT_L(0); PG8_MMA(1, 0, At, B0); PG8_BAR; PG8_SCHED;
;             PG8_STAGE(PG8_SB(1, 1), b3 + hstep, voffB);
;             PG8_WAIT_V(6); PG8_BAR; PG8_MMA(1, 1, At, B1); PG8_BAR;
;         }
	s_setprio 1
	s_waitcnt lgkmcnt(3)
	v_mfma_f32_16x16x32_bf16 v[116:119], v[222:225], v[190:193], v[116:119]
	s_waitcnt lgkmcnt(1)
	v_mfma_f32_16x16x32_bf16 v[112:115], v[230:233], v[190:193], v[112:115]
	v_mfma_f32_16x16x32_bf16 v[100:103], v[222:225], v[198:201], v[100:103]
	v_mfma_f32_16x16x32_bf16 v[96:99], v[230:233], v[198:201], v[96:99]
	v_mfma_f32_16x16x32_bf16 v[84:87], v[222:225], v[206:209], v[84:87]
	v_mfma_f32_16x16x32_bf16 v[80:83], v[230:233], v[206:209], v[80:83]
	v_mfma_f32_16x16x32_bf16 v[68:71], v[222:225], v[214:217], v[68:71]
	v_mfma_f32_16x16x32_bf16 v[64:67], v[230:233], v[214:217], v[64:67]
	v_mfma_f32_16x16x32_bf16 v[116:119], v[226:229], v[194:197], v[116:119]
	s_waitcnt lgkmcnt(0)
	v_mfma_f32_16x16x32_bf16 v[112:115], v[234:237], v[194:197], v[112:115]
	v_mfma_f32_16x16x32_bf16 v[100:103], v[226:229], v[202:205], v[100:103]
	v_mfma_f32_16x16x32_bf16 v[96:99], v[234:237], v[202:205], v[96:99]
	v_mfma_f32_16x16x32_bf16 v[84:87], v[226:229], v[210:213], v[84:87]
	v_mfma_f32_16x16x32_bf16 v[80:83], v[234:237], v[210:213], v[80:83]
	v_mfma_f32_16x16x32_bf16 v[68:71], v[226:229], v[218:221], v[68:71]
	v_mfma_f32_16x16x32_bf16 v[64:67], v[234:237], v[218:221], v[64:67]
	s_setprio 0
	s_mov_b32 m0, s33
	v_lshl_add_u64 v[238:239], v[244:245], 0, s[8:9]
	s_barrier
	ds_read_b128 v[190:193], v167 offset:49152
	ds_read_b128 v[194:197], v167 offset:50176
	ds_read_b128 v[198:201], v167 offset:51200
	ds_read_b128 v[202:205], v167 offset:52224
	ds_read_b128 v[206:209], v167 offset:53248
	ds_read_b128 v[210:213], v167 offset:54272
	ds_read_b128 v[214:217], v167 offset:55296
	ds_read_b128 v[218:221], v167 offset:56320
	global_load_lds_dwordx4 v[238:239], off
	v_lshl_add_u64 v[238:239], v[242:243], 0, s[8:9]
	s_mov_b32 m0, s34
	s_nop 0
	global_load_lds_dwordx4 v[238:239], off
	s_barrier
	s_setprio 1
	s_waitcnt lgkmcnt(7)
	v_mfma_f32_16x16x32_bf16 v[52:55], v[174:177], v[190:193], v[52:55]
	v_mfma_f32_16x16x32_bf16 v[36:39], v[182:185], v[190:193], v[36:39]
	s_waitcnt lgkmcnt(5)
	v_mfma_f32_16x16x32_bf16 v[40:43], v[174:177], v[198:201], v[40:43]
	v_mfma_f32_16x16x32_bf16 v[32:35], v[182:185], v[198:201], v[32:35]
	s_waitcnt lgkmcnt(3)
	v_mfma_f32_16x16x32_bf16 v[20:23], v[174:177], v[206:209], v[20:23]
	v_mfma_f32_16x16x32_bf16 v[16:19], v[182:185], v[206:209], v[16:19]
	s_waitcnt lgkmcnt(1)
	v_mfma_f32_16x16x32_bf16 v[4:7], v[174:177], v[214:217], v[4:7]
	v_mfma_f32_16x16x32_bf16 v[0:3], v[182:185], v[214:217], v[0:3]
	v_mfma_f32_16x16x32_bf16 v[52:55], v[178:181], v[194:197], v[52:55]
	v_mfma_f32_16x16x32_bf16 v[36:39], v[186:189], v[194:197], v[36:39]
	v_mfma_f32_16x16x32_bf16 v[40:43], v[178:181], v[202:205], v[40:43]
	v_mfma_f32_16x16x32_bf16 v[32:35], v[186:189], v[202:205], v[32:35]
	v_mfma_f32_16x16x32_bf16 v[20:23], v[178:181], v[210:213], v[20:23]
	v_mfma_f32_16x16x32_bf16 v[16:19], v[186:189], v[210:213], v[16:19]
	s_waitcnt lgkmcnt(0)
	v_mfma_f32_16x16x32_bf16 v[4:7], v[178:181], v[218:221], v[4:7]
	v_mfma_f32_16x16x32_bf16 v[0:3], v[186:189], v[218:221], v[0:3]
	s_setprio 0
	s_barrier
	s_add_u32 s0, s24, 0x80080
	s_addc_u32 s1, s25, 0
	s_mov_b32 m0, s76
	v_lshl_add_u64 v[174:175], s[0:1], 0, v[128:129]
	global_load_lds_dwordx4 v[174:175], off
	v_lshl_add_u64 v[174:175], s[0:1], 0, v[130:131]
	s_mov_b32 m0, s77
	s_nop 0
	global_load_lds_dwordx4 v[174:175], off
	s_waitcnt vmcnt(6)
	s_barrier
	s_setprio 1
	v_mfma_f32_16x16x32_bf16 v[60:63], v[222:225], v[190:193], v[60:63]
	v_mfma_f32_16x16x32_bf16 v[56:59], v[230:233], v[190:193], v[56:59]
	v_mfma_f32_16x16x32_bf16 v[48:51], v[222:225], v[198:201], v[48:51]
	v_mfma_f32_16x16x32_bf16 v[44:47], v[230:233], v[198:201], v[44:47]
	v_mfma_f32_16x16x32_bf16 v[28:31], v[222:225], v[206:209], v[28:31]
	v_mfma_f32_16x16x32_bf16 v[24:27], v[230:233], v[206:209], v[24:27]
	v_mfma_f32_16x16x32_bf16 v[12:15], v[222:225], v[214:217], v[12:15]
	v_mfma_f32_16x16x32_bf16 v[8:11], v[230:233], v[214:217], v[8:11]
	v_mfma_f32_16x16x32_bf16 v[60:63], v[226:229], v[194:197], v[60:63]
	v_mfma_f32_16x16x32_bf16 v[56:59], v[234:237], v[194:197], v[56:59]
	v_mfma_f32_16x16x32_bf16 v[48:51], v[226:229], v[202:205], v[48:51]
	v_mfma_f32_16x16x32_bf16 v[44:47], v[234:237], v[202:205], v[44:47]
	v_mfma_f32_16x16x32_bf16 v[28:31], v[226:229], v[210:213], v[28:31]
	v_mfma_f32_16x16x32_bf16 v[24:27], v[234:237], v[210:213], v[24:27]
	v_mfma_f32_16x16x32_bf16 v[12:15], v[226:229], v[218:221], v[12:15]
	v_mfma_f32_16x16x32_bf16 v[8:11], v[234:237], v[218:221], v[8:11]
	s_setprio 0
	s_add_i32 s80, s80, 2
	s_cmp_gt_u32 s80, 29
	s_mov_b64 s[0:1], s[22:23]
	s_cbranch_scc1 .Lmy_kx_2
	s_barrier
	s_branch .LBB0_1008

; #define PG8_STAGE(bufoff, gbase, voff) do { _Pragma("unroll") for (int _i = 0; _i < 2; ++_i) \
;         __builtin_amdgcn_global_load_lds((const unsigned*)((const char*)(gbase) + (voff)[_i]), (LAS unsigned*)(lds + (bufoff) + ldsw + _i * 8192), 16, 0, 0); } while (0)
; #define PG8_LDA(dst, b, h) do { _Pragma("unroll") for (int m = 0; m < 4; ++m) _Pragma("unroll") for (int k = 0; k < 2; ++k) dst[m][k] = *(const LAS bf16x8*)(lds + PG8_SA(b, h) + aoff + m * 2048 + k * 1024); } while (0)
; #define PG8_LDB(dst, b, h) do { _Pragma("unroll") for (int n = 0; n < 2; ++n) _Pragma("unroll") for (int k = 0; k < 2; ++k) dst[n][k] = *(const LAS bf16x8*)(lds + PG8_SB(b, h) + boff + n * 2048 + k * 1024); } while (0)
; #define PG8_MMA(ai, bj, At, Bt) do { __builtin_amdgcn_s_setprio(1); _Pragma("unroll") for (int m = 0; m < 4; ++m) _Pragma("unroll") for (int n = 0; n < 2; ++n) _Pragma("unroll") for (int k = 0; k < 2; ++k) \
;         acc[ai][bj][m][n] = __builtin_amdgcn_mfma_f32_16x16x32_bf16(Bt[n][k], At[m][k], acc[ai][bj][m][n], 0, 0, 0); __builtin_amdgcn_s_setprio(0); } while (0)
; #define PG8_WAIT_L(n) asm volatile("s_waitcnt lgkmcnt(" #n ")" ::: "memory")
; #define PG8_BAR __builtin_amdgcn_s_barrier()
; #define PG8_SCHED __builtin_amdgcn_sched_barrier(0)
; template <class Epi, class Sched>
; __device__ __forceinline__ void gemm_phase(LAS unsigned char* lds, const bf16_t* A, const int K, const Sched& S, const Epi& E, const int wv) {
;     ...
;         for (int t = 0; t < nt; t += 2) {
;             const bool last = (t == nt - 2);
;             const size_t k1 = (size_t)(t + 1) * kstep;
;             const size_t k2 = last ? 0 : (size_t)(t + 2) * kstep, k3 = k2 + kstep;
;             const char* b2 = last ? nB : cB + (size_t)(t + 2) * kstep; const char* b3 = b2 + kstep;
;             PG8_LDB(B0, 0, 0); PG8_SCHED; PG8_LDA(At, 0, 0); PG8_STAGE_A(PG8_SA(1, 1), 1, false, k1);
;             PG8_WAIT_L(8); PG8_BAR; PG8_WAIT_L(0); PG8_MMA(0, 0, At, B0); PG8_BAR; PG8_SCHED;
;             PG8_LDB(B1, 0, 1); PG8_STAGE(PG8_SB(0, 0), b2, voffB);
;             PG8_BAR; PG8_WAIT_L(0); PG8_MMA(0, 1, At, B1); PG8_BAR;
;             PG8_LDA(At, 0, 1); PG8_STAGE_A(PG8_SA(0, 0), 0, last, k2);
;             PG8_BAR; PG8_WAIT_L(0); PG8_MMA(1, 0, At, B0); PG8_BAR; PG8_SCHED;
.Lmy_ph_3:
.LBB0_1170:
	v_add_u32_e32 v132, s64, v150
	s_add_u32 s22, s0, 0x100
	ds_read_b128 v[174:177], v132
	ds_read_b128 v[178:181], v132 offset:1024
	ds_read_b128 v[182:185], v132 offset:2048
	ds_read_b128 v[186:189], v132 offset:3072
	s_addc_u32 s23, s1, 0
	s_add_u32 s81, s17, s0
	s_addc_u32 s82, s19, s1
	s_cmpk_eq_i32 s0, 0x700
	s_cselect_b64 vcc, -1, 0
	s_and_b64 s[24:25], vcc, exec
	s_cselect_b32 s83, 0, s22
	s_cselect_b32 s25, s21, s82
	s_cselect_b32 s24, s20, s81
	s_mov_b32 m0, s66
	v_lshl_add_u64 v[222:223], v[142:143], 0, s[0:1]
	ds_read_b128 v[190:193], v168
	ds_read_b128 v[194:197], v168 offset:1024
	ds_read_b128 v[198:201], v168 offset:2048
	ds_read_b128 v[202:205], v168 offset:3072
	ds_read_b128 v[206:209], v168 offset:4096
	ds_read_b128 v[210:213], v168 offset:5120
	ds_read_b128 v[214:217], v168 offset:6144
	ds_read_b128 v[218:221], v168 offset:7168
	global_load_lds_dwordx4 v[222:223], off
	v_lshl_add_u64 v[222:223], v[140:141], 0, s[0:1]
	s_mov_b32 m0, s67
	s_nop 0
	global_load_lds_dwordx4 v[222:223], off
	s_waitcnt lgkmcnt(8)
	s_barrier
	s_setprio 1
	s_waitcnt lgkmcnt(7)
	v_mfma_f32_16x16x32_bf16 v[124:127], v[174:177], v[190:193], v[124:127]
	v_mfma_f32_16x16x32_bf16 v[120:123], v[182:185], v[190:193], v[120:123]
	s_waitcnt lgkmcnt(5)
	v_mfma_f32_16x16x32_bf16 v[116:119], v[174:177], v[198:201], v[116:119]
	v_mfma_f32_16x16x32_bf16 v[108:111], v[182:185], v[198:201], v[108:111]
	s_waitcnt lgkmcnt(3)
	v_mfma_f32_16x16x32_bf16 v[100:103], v[174:177], v[206:209], v[100:103]
	v_mfma_f32_16x16x32_bf16 v[92:95], v[182:185], v[206:209], v[92:95]
	s_waitcnt lgkmcnt(1)
	v_mfma_f32_16x16x32_bf16 v[84:87], v[174:177], v[214:217], v[84:87]
	v_mfma_f32_16x16x32_bf16 v[76:79], v[182:185], v[214:217], v[76:79]
	v_mfma_f32_16x16x32_bf16 v[124:127], v[178:181], v[194:197], v[124:127]
	v_mfma_f32_16x16x32_bf16 v[120:123], v[186:189], v[194:197], v[120:123]
	v_mfma_f32_16x16x32_bf16 v[116:119], v[178:181], v[202:205], v[116:119]
	v_mfma_f32_16x16x32_bf16 v[108:111], v[186:189], v[202:205], v[108:111]
	v_mfma_f32_16x16x32_bf16 v[100:103], v[178:181], v[210:213], v[100:103]
	v_mfma_f32_16x16x32_bf16 v[92:95], v[186:189], v[210:213], v[92:95]
	s_waitcnt lgkmcnt(0)
	v_mfma_f32_16x16x32_bf16 v[84:87], v[178:181], v[218:221], v[84:87]
	v_mfma_f32_16x16x32_bf16 v[76:79], v[186:189], v[218:221], v[76:79]
	s_setprio 0
	s_barrier
	s_mov_b32 m0, s68
	v_add_u32_e32 v132, s65, v150
	v_lshl_add_u64 v[238:239], s[24:25], 0, v[128:129]
	ds_read_b128 v[222:225], v132
	ds_read_b128 v[226:229], v132 offset:1024
	ds_read_b128 v[230:233], v132 offset:2048
	ds_read_b128 v[234:237], v132 offset:3072
	global_load_lds_dwordx4 v[238:239], off
	v_lshl_add_u64 v[240:241], s[24:25], 0, v[130:131]
	s_mov_b32 m0, s69
	s_nop 0
	global_load_lds_dwordx4 v[240:241], off
	s_barrier
	s_setprio 1
	s_waitcnt lgkmcnt(3)
	v_mfma_f32_16x16x32_bf16 v[112:115], v[222:225], v[190:193], v[112:115]
	s_waitcnt lgkmcnt(1)
	v_mfma_f32_16x16x32_bf16 v[104:107], v[230:233], v[190:193], v[104:107]
	v_mfma_f32_16x16x32_bf16 v[96:99], v[222:225], v[198:201], v[96:99]
	v_mfma_f32_16x16x32_bf16 v[88:91], v[230:233], v[198:201], v[88:91]
	v_mfma_f32_16x16x32_bf16 v[80:83], v[222:225], v[206:209], v[80:83]
	v_mfma_f32_16x16x32_bf16 v[72:75], v[230:233], v[206:209], v[72:75]
	v_mfma_f32_16x16x32_bf16 v[52:55], v[222:225], v[214:217], v[52:55]
	v_mfma_f32_16x16x32_bf16 v[48:51], v[230:233], v[214:217], v[48:51]
	v_mfma_f32_16x16x32_bf16 v[112:115], v[226:229], v[194:197], v[112:115]
	s_waitcnt lgkmcnt(0)
	v_mfma_f32_16x16x32_bf16 v[104:107], v[234:237], v[194:197], v[104:107]
	v_mfma_f32_16x16x32_bf16 v[96:99], v[226:229], v[202:205], v[96:99]
	v_mfma_f32_16x16x32_bf16 v[88:91], v[234:237], v[202:205], v[88:91]
	v_mfma_f32_16x16x32_bf16 v[80:83], v[226:229], v[210:213], v[80:83]
	v_mfma_f32_16x16x32_bf16 v[72:75], v[234:237], v[210:213], v[72:75]
	v_mfma_f32_16x16x32_bf16 v[52:55], v[226:229], v[218:221], v[52:55]
	v_mfma_f32_16x16x32_bf16 v[48:51], v[234:237], v[218:221], v[48:51]
	s_setprio 0
	s_add_u32 s0, s2, s83
	s_mov_b32 m0, s13
	s_addc_u32 s1, s3, 0
	v_cndmask_b32_e32 v132, v135, v170, vcc
	s_barrier
	ds_read_b128 v[190:193], v168 offset:16384
	ds_read_b128 v[194:197], v168 offset:17408
	ds_read_b128 v[198:201], v168 offset:18432
	ds_read_b128 v[202:205], v168 offset:19456
	ds_read_b128 v[206:209], v168 offset:20480
	ds_read_b128 v[210:213], v168 offset:21504
	ds_read_b128 v[214:217], v168 offset:22528
	ds_read_b128 v[218:221], v168 offset:23552
	v_cndmask_b32_e32 v242, v134, v172, vcc
	global_load_lds_dwordx4 v132, s[0:1]
	s_mov_b32 m0, s29
	v_mov_b32_e32 v243, v133
	global_load_lds_dwordx4 v242, s[0:1]
	s_barrier
	v_lshl_add_u64 v[244:245], s[0:1], 0, v[132:133]
	v_lshl_add_u64 v[242:243], s[0:1], 0, v[242:243]
	s_setprio 1
	s_waitcnt lgkmcnt(7)
	v_mfma_f32_16x16x32_bf16 v[20:23], v[174:177], v[190:193], v[20:23]
	v_mfma_f32_16x16x32_bf16 v[8:11], v[182:185], v[190:193], v[8:11]
	s_waitcnt lgkmcnt(5)
	v_mfma_f32_16x16x32_bf16 v[40:43], v[174:177], v[198:201], v[40:43]
	v_mfma_f32_16x16x32_bf16 v[44:47], v[182:185], v[198:201], v[44:47]
	s_waitcnt lgkmcnt(3)
	v_mfma_f32_16x16x32_bf16 v[24:27], v[174:177], v[206:209], v[24:27]
	v_mfma_f32_16x16x32_bf16 v[28:31], v[182:185], v[206:209], v[28:31]
	s_waitcnt lgkmcnt(1)
	v_mfma_f32_16x16x32_bf16 v[0:3], v[174:177], v[214:217], v[0:3]
	v_mfma_f32_16x16x32_bf16 v[4:7], v[182:185], v[214:217], v[4:7]
	v_mfma_f32_16x16x32_bf16 v[20:23], v[178:181], v[194:197], v[20:23]
	v_mfma_f32_16x16x32_bf16 v[8:11], v[186:189], v[194:197], v[8:11]
	v_mfma_f32_16x16x32_bf16 v[40:43], v[178:181], v[202:205], v[40:43]
	v_mfma_f32_16x16x32_bf16 v[44:47], v[186:189], v[202:205], v[44:47]
	v_mfma_f32_16x16x32_bf16 v[24:27], v[178:181], v[210:213], v[24:27]
	v_mfma_f32_16x16x32_bf16 v[28:31], v[186:189], v[210:213], v[28:31]
	s_waitcnt lgkmcnt(0)
	v_mfma_f32_16x16x32_bf16 v[0:3], v[178:181], v[218:221], v[0:3]
	v_mfma_f32_16x16x32_bf16 v[4:7], v[186:189], v[218:221], v[4:7]
	s_setprio 0
	s_barrier
; #define PG8_STAGE(bufoff, gbase, voff) do { _Pragma("unroll") for (int _i = 0; _i < 2; ++_i) \
;         __builtin_amdgcn_global_load_lds((const unsigned*)((const char*)(gbase) + (voff)[_i]), (LAS unsigned*)(lds + (bufoff) + ldsw + _i * 8192), 16, 0, 0); } while (0)
; #define PG8_LDA(dst, b, h) do { _Pragma("unroll") for (int m = 0; m < 4; ++m) _Pragma("unroll") for (int k = 0; k < 2; ++k) dst[m][k] = *(const LAS bf16x8*)(lds + PG8_SA(b, h) + aoff + m * 2048 + k * 1024); } while (0)
; #define PG8_LDB(dst, b, h) do { _Pragma("unroll") for (int n = 0; n < 2; ++n) _Pragma("unroll") for (int k = 0; k < 2; ++k) dst[n][k] = *(const LAS bf16x8*)(lds + PG8_SB(b, h) + boff + n * 2048 + k * 1024); } while (0)
; #define PG8_MMA(ai, bj, At, Bt) do { __builtin_amdgcn_s_setprio(1); _Pragma("unroll") for (int m = 0; m < 4; ++m) _Pragma("unroll") for (int n = 0; n < 2; ++n) _Pragma("unroll") for (int k = 0; k < 2; ++k) \
;         acc[ai][bj][m][n] = __builtin_amdgcn_mfma_f32_16x16x32_bf16(Bt[n][k], At[m][k], acc[ai][bj][m][n], 0, 0, 0); __builtin_amdgcn_s_setprio(0); } while (0)
; #define PG8_WAIT_V(n) asm volatile("s_waitcnt vmcnt(" #n ")" ::: "memory")
; #define PG8_WAIT_L(n) asm volatile("s_waitcnt lgkmcnt(" #n ")" ::: "memory")
; #define PG8_BAR __builtin_amdgcn_s_barrier()
; #define PG8_SCHED __builtin_amdgcn_sched_barrier(0)
; template <class Epi, class Sched>
; __device__ __forceinline__ void gemm_phase(LAS unsigned char* lds, const bf16_t* A, const int K, const Sched& S, const Epi& E, const int wv) {
;     ...
;             PG8_STAGE(PG8_SB(0, 1), b2 + hstep, voffB);
;             PG8_WAIT_V(6); PG8_BAR; PG8_MMA(1, 1, At, B1); PG8_BAR;
;             PG8_LDB(B0, 1, 0); PG8_SCHED; PG8_LDA(At, 1, 0); PG8_STAGE_A(PG8_SA(0, 1), 1, last, k2);
;             PG8_WAIT_L(8); PG8_BAR; PG8_WAIT_L(0); PG8_MMA(0, 0, At, B0); PG8_BAR; PG8_SCHED;
;             PG8_LDB(B1, 1, 1); PG8_STAGE(PG8_SB(1, 0), b3, voffB);
	s_add_u32 s82, s24, 0x40000
	s_addc_u32 s83, s25, 0
	s_mov_b32 m0, s70
	v_lshl_add_u64 v[174:175], s[82:83], 0, v[128:129]
	global_load_lds_dwordx4 v[174:175], off
	v_lshl_add_u64 v[174:175], s[82:83], 0, v[130:131]
	s_mov_b32 m0, s71
	s_nop 0
	global_load_lds_dwordx4 v[174:175], off
	s_waitcnt vmcnt(6)
	s_barrier
	s_setprio 1
	v_mfma_f32_16x16x32_bf16 v[64:67], v[222:225], v[190:193], v[64:67]
	v_mfma_f32_16x16x32_bf16 v[68:71], v[230:233], v[190:193], v[68:71]
	v_mfma_f32_16x16x32_bf16 v[56:59], v[222:225], v[198:201], v[56:59]
	v_mfma_f32_16x16x32_bf16 v[60:63], v[230:233], v[198:201], v[60:63]
	v_mfma_f32_16x16x32_bf16 v[32:35], v[222:225], v[206:209], v[32:35]
	v_mfma_f32_16x16x32_bf16 v[36:39], v[230:233], v[206:209], v[36:39]
	v_mfma_f32_16x16x32_bf16 v[12:15], v[222:225], v[214:217], v[12:15]
	v_mfma_f32_16x16x32_bf16 v[16:19], v[230:233], v[214:217], v[16:19]
	v_mfma_f32_16x16x32_bf16 v[64:67], v[226:229], v[194:197], v[64:67]
	v_mfma_f32_16x16x32_bf16 v[68:71], v[234:237], v[194:197], v[68:71]
	v_mfma_f32_16x16x32_bf16 v[56:59], v[226:229], v[202:205], v[56:59]
	v_mfma_f32_16x16x32_bf16 v[60:63], v[234:237], v[202:205], v[60:63]
	v_mfma_f32_16x16x32_bf16 v[32:35], v[226:229], v[210:213], v[32:35]
	v_mfma_f32_16x16x32_bf16 v[36:39], v[234:237], v[210:213], v[36:39]
	v_mfma_f32_16x16x32_bf16 v[12:15], v[226:229], v[218:221], v[12:15]
	v_mfma_f32_16x16x32_bf16 v[16:19], v[234:237], v[218:221], v[16:19]
	s_setprio 0
	v_add_u32_e32 v132, s72, v150
	s_barrier
	ds_read_b128 v[174:177], v132
	ds_read_b128 v[178:181], v132 offset:1024
	ds_read_b128 v[182:185], v132 offset:2048
	ds_read_b128 v[186:189], v132 offset:3072
	s_mov_b32 m0, s30
	v_cndmask_b32_e32 v132, v136, v171, vcc
	ds_read_b128 v[190:193], v168 offset:32768
	ds_read_b128 v[194:197], v168 offset:33792
	ds_read_b128 v[198:201], v168 offset:34816
	ds_read_b128 v[202:205], v168 offset:35840
	ds_read_b128 v[206:209], v168 offset:36864
	ds_read_b128 v[210:213], v168 offset:37888
	ds_read_b128 v[214:217], v168 offset:38912
	ds_read_b128 v[218:221], v168 offset:39936
	v_cndmask_b32_e32 v137, v138, v173, vcc
	global_load_lds_dwordx4 v132, s[0:1]
	s_mov_b32 m0, s31
	s_nop 0
	global_load_lds_dwordx4 v137, s[0:1]
	s_waitcnt lgkmcnt(8)
	s_barrier
	s_setprio 1
	s_waitcnt lgkmcnt(7)
	v_mfma_f32_16x16x32_bf16 v[124:127], v[174:177], v[190:193], v[124:127]
	v_mfma_f32_16x16x32_bf16 v[120:123], v[182:185], v[190:193], v[120:123]
	s_waitcnt lgkmcnt(5)
	v_mfma_f32_16x16x32_bf16 v[116:119], v[174:177], v[198:201], v[116:119]
	v_mfma_f32_16x16x32_bf16 v[108:111], v[182:185], v[198:201], v[108:111]
	s_waitcnt lgkmcnt(3)
	v_mfma_f32_16x16x32_bf16 v[100:103], v[174:177], v[206:209], v[100:103]
	v_mfma_f32_16x16x32_bf16 v[92:95], v[182:185], v[206:209], v[92:95]
	s_waitcnt lgkmcnt(1)
	v_mfma_f32_16x16x32_bf16 v[84:87], v[174:177], v[214:217], v[84:87]
	v_mfma_f32_16x16x32_bf16 v[76:79], v[182:185], v[214:217], v[76:79]
	v_mfma_f32_16x16x32_bf16 v[124:127], v[178:181], v[194:197], v[124:127]
	v_mfma_f32_16x16x32_bf16 v[120:123], v[186:189], v[194:197], v[120:123]
	v_mfma_f32_16x16x32_bf16 v[116:119], v[178:181], v[202:205], v[116:119]
	v_mfma_f32_16x16x32_bf16 v[108:111], v[186:189], v[202:205], v[108:111]
	v_mfma_f32_16x16x32_bf16 v[100:103], v[178:181], v[210:213], v[100:103]
	v_mfma_f32_16x16x32_bf16 v[92:95], v[186:189], v[210:213], v[92:95]
	s_waitcnt lgkmcnt(0)
	v_mfma_f32_16x16x32_bf16 v[84:87], v[178:181], v[218:221], v[84:87]
	v_mfma_f32_16x16x32_bf16 v[76:79], v[186:189], v[218:221], v[76:79]
	s_setprio 0
	s_barrier
	s_mov_b32 m0, s74
	v_add_u32_e32 v132, s73, v150
	v_lshl_add_u64 v[238:239], v[238:239], 0, s[8:9]
	ds_read_b128 v[222:225], v132
	ds_read_b128 v[226:229], v132 offset:1024
	ds_read_b128 v[230:233], v132 offset:2048
	ds_read_b128 v[234:237], v132 offset:3072
	global_load_lds_dwordx4 v[238:239], off
	v_lshl_add_u64 v[238:239], v[240:241], 0, s[8:9]
	s_mov_b32 m0, s75
	s_nop 0
	global_load_lds_dwordx4 v[238:239], off
	s_barrier
; #define PG8_STAGE(bufoff, gbase, voff) do { _Pragma("unroll") for (int _i = 0; _i < 2; ++_i) \
;         __builtin_amdgcn_global_load_lds((const unsigned*)((const char*)(gbase) + (voff)[_i]), (LAS unsigned*)(lds + (bufoff) + ldsw + _i * 8192), 16, 0, 0); } while (0)
; #define PG8_LDA(dst, b, h) do { _Pragma("unroll") for (int m = 0; m < 4; ++m) _Pragma("unroll") for (int k = 0; k < 2; ++k) dst[m][k] = *(const LAS bf16x8*)(lds + PG8_SA(b, h) + aoff + m * 2048 + k * 1024); } while (0)
; #define PG8_LDB(dst, b, h) do { _Pragma("unroll") for (int n = 0; n < 2; ++n) _Pragma("unroll") for (int k = 0; k < 2; ++k) dst[n][k] = *(const LAS bf16x8*)(lds + PG8_SB(b, h) + boff + n * 2048 + k * 1024); } while (0)
; #define PG8_MMA(ai, bj, At, Bt) do { __builtin_amdgcn_s_setprio(1); _Pragma("unroll") for (int m = 0; m < 4; ++m) _Pragma("unroll") for (int n = 0; n < 2; ++n) _Pragma("unroll") for (int k = 0; k < 2; ++k) \
;         acc[ai][bj][m][n] = __builtin_amdgcn_mfma_f32_16x16x32_bf16(Bt[n][k], At[m][k], acc[ai][bj][m][n], 0, 0, 0); __builtin_amdgcn_s_setprio(0); } while (0)
; #define PG8_WAIT_V(n) asm volatile("s_waitcnt vmcnt(" #n ")" ::: "memory")
; #define PG8_WAIT_L(n) asm volatile("s_waitcnt lgkmcnt(" #n ")" ::: "memory")
; #define PG8_BAR __builtin_amdgcn_s_barrier()
; #define PG8_SCHED __builtin_amdgcn_sched_barrier(0)
; template <class Epi, class Sched>
; __device__ __forceinline__ void gemm_phase(LAS unsigned char* lds, const bf16_t* A, const int K, const Sched& S, const Epi& E, const int wv) {
;     ...
;             PG8_LDB(B1, 1, 1); PG8_STAGE(PG8_SB(1, 0), b3, voffB);
;             PG8_BAR; PG8_WAIT_L(0); PG8_MMA(0, 1, At, B1); PG8_BAR;
;             PG8_LDA(At, 1, 1); PG8_STAGE_A(PG8_SA(1, 0), 0, last, k3);
;             PG8_BAR; PG8_WAIT_L(0); PG8_MMA(1, 0, At, B0); PG8_BAR; PG8_SCHED;
;             PG8_STAGE(PG8_SB(1, 1), b3 + hstep, voffB);
;             PG8_WAIT_V(6); PG8_BAR; PG8_MMA(1, 1, At, B1); PG8_BAR;
;         }
	s_setprio 1
	s_waitcnt lgkmcnt(3)
	v_mfma_f32_16x16x32_bf16 v[112:115], v[222:225], v[190:193], v[112:115]
	s_waitcnt lgkmcnt(1)
	v_mfma_f32_16x16x32_bf16 v[104:107], v[230:233], v[190:193], v[104:107]
	v_mfma_f32_16x16x32_bf16 v[96:99], v[222:225], v[198:201], v[96:99]
	v_mfma_f32_16x16x32_bf16 v[88:91], v[230:233], v[198:201], v[88:91]
	v_mfma_f32_16x16x32_bf16 v[80:83], v[222:225], v[206:209], v[80:83]
	v_mfma_f32_16x16x32_bf16 v[72:75], v[230:233], v[206:209], v[72:75]
	v_mfma_f32_16x16x32_bf16 v[52:55], v[222:225], v[214:217], v[52:55]
	v_mfma_f32_16x16x32_bf16 v[48:51], v[230:233], v[214:217], v[48:51]
	v_mfma_f32_16x16x32_bf16 v[112:115], v[226:229], v[194:197], v[112:115]
	s_waitcnt lgkmcnt(0)
	v_mfma_f32_16x16x32_bf16 v[104:107], v[234:237], v[194:197], v[104:107]
	v_mfma_f32_16x16x32_bf16 v[96:99], v[226:229], v[202:205], v[96:99]
	v_mfma_f32_16x16x32_bf16 v[88:91], v[234:237], v[202:205], v[88:91]
	v_mfma_f32_16x16x32_bf16 v[80:83], v[226:229], v[210:213], v[80:83]
	v_mfma_f32_16x16x32_bf16 v[72:75], v[234:237], v[210:213], v[72:75]
	v_mfma_f32_16x16x32_bf16 v[52:55], v[226:229], v[218:221], v[52:55]
	v_mfma_f32_16x16x32_bf16 v[48:51], v[234:237], v[218:221], v[48:51]
	s_setprio 0
	s_mov_b32 m0, s34
	v_lshl_add_u64 v[238:239], v[244:245], 0, s[8:9]
	s_barrier
	ds_read_b128 v[190:193], v168 offset:49152
	ds_read_b128 v[194:197], v168 offset:50176
	ds_read_b128 v[198:201], v168 offset:51200
	ds_read_b128 v[202:205], v168 offset:52224
	ds_read_b128 v[206:209], v168 offset:53248
	ds_read_b128 v[210:213], v168 offset:54272
	ds_read_b128 v[214:217], v168 offset:55296
	ds_read_b128 v[218:221], v168 offset:56320
	global_load_lds_dwordx4 v[238:239], off
	v_lshl_add_u64 v[238:239], v[242:243], 0, s[8:9]
	s_mov_b32 m0, s35
	s_nop 0
	global_load_lds_dwordx4 v[238:239], off
	s_barrier
	s_setprio 1
	s_waitcnt lgkmcnt(7)
	v_mfma_f32_16x16x32_bf16 v[20:23], v[174:177], v[190:193], v[20:23]
	v_mfma_f32_16x16x32_bf16 v[8:11], v[182:185], v[190:193], v[8:11]
	s_waitcnt lgkmcnt(5)
	v_mfma_f32_16x16x32_bf16 v[40:43], v[174:177], v[198:201], v[40:43]
	v_mfma_f32_16x16x32_bf16 v[44:47], v[182:185], v[198:201], v[44:47]
	s_waitcnt lgkmcnt(3)
	v_mfma_f32_16x16x32_bf16 v[24:27], v[174:177], v[206:209], v[24:27]
	v_mfma_f32_16x16x32_bf16 v[28:31], v[182:185], v[206:209], v[28:31]
	s_waitcnt lgkmcnt(1)
	v_mfma_f32_16x16x32_bf16 v[0:3], v[174:177], v[214:217], v[0:3]
	v_mfma_f32_16x16x32_bf16 v[4:7], v[182:185], v[214:217], v[4:7]
	v_mfma_f32_16x16x32_bf16 v[20:23], v[178:181], v[194:197], v[20:23]
	v_mfma_f32_16x16x32_bf16 v[8:11], v[186:189], v[194:197], v[8:11]
	v_mfma_f32_16x16x32_bf16 v[40:43], v[178:181], v[202:205], v[40:43]
	v_mfma_f32_16x16x32_bf16 v[44:47], v[186:189], v[202:205], v[44:47]
	v_mfma_f32_16x16x32_bf16 v[24:27], v[178:181], v[210:213], v[24:27]
	v_mfma_f32_16x16x32_bf16 v[28:31], v[186:189], v[210:213], v[28:31]
	s_waitcnt lgkmcnt(0)
	v_mfma_f32_16x16x32_bf16 v[0:3], v[178:181], v[218:221], v[0:3]
	v_mfma_f32_16x16x32_bf16 v[4:7], v[186:189], v[218:221], v[4:7]
	s_setprio 0
	s_barrier
	s_add_u32 s0, s24, 0x40080
	s_addc_u32 s1, s25, 0
	s_mov_b32 m0, s76
	v_lshl_add_u64 v[174:175], s[0:1], 0, v[128:129]
	global_load_lds_dwordx4 v[174:175], off
	v_lshl_add_u64 v[174:175], s[0:1], 0, v[130:131]
	s_mov_b32 m0, s77
	s_nop 0
	global_load_lds_dwordx4 v[174:175], off
	s_waitcnt vmcnt(6)
	s_barrier
	s_setprio 1
	v_mfma_f32_16x16x32_bf16 v[64:67], v[222:225], v[190:193], v[64:67]
	v_mfma_f32_16x16x32_bf16 v[68:71], v[230:233], v[190:193], v[68:71]
	v_mfma_f32_16x16x32_bf16 v[56:59], v[222:225], v[198:201], v[56:59]
	v_mfma_f32_16x16x32_bf16 v[60:63], v[230:233], v[198:201], v[60:63]
	v_mfma_f32_16x16x32_bf16 v[32:35], v[222:225], v[206:209], v[32:35]
	v_mfma_f32_16x16x32_bf16 v[36:39], v[230:233], v[206:209], v[36:39]
	v_mfma_f32_16x16x32_bf16 v[12:15], v[222:225], v[214:217], v[12:15]
	v_mfma_f32_16x16x32_bf16 v[16:19], v[230:233], v[214:217], v[16:19]
	v_mfma_f32_16x16x32_bf16 v[64:67], v[226:229], v[194:197], v[64:67]
	v_mfma_f32_16x16x32_bf16 v[68:71], v[234:237], v[194:197], v[68:71]
	v_mfma_f32_16x16x32_bf16 v[56:59], v[226:229], v[202:205], v[56:59]
	v_mfma_f32_16x16x32_bf16 v[60:63], v[234:237], v[202:205], v[60:63]
	v_mfma_f32_16x16x32_bf16 v[32:35], v[226:229], v[210:213], v[32:35]
	v_mfma_f32_16x16x32_bf16 v[36:39], v[234:237], v[210:213], v[36:39]
	v_mfma_f32_16x16x32_bf16 v[12:15], v[226:229], v[218:221], v[12:15]
	v_mfma_f32_16x16x32_bf16 v[16:19], v[234:237], v[218:221], v[16:19]
	s_setprio 0
	s_add_i32 s80, s80, 2
	s_cmp_gt_u32 s80, 13
	s_mov_b64 s[0:1], s[22:23]
	s_cbranch_scc1 .Lmy_kx_3
	s_barrier
	s_branch .LBB0_1170

; #define PG8_STAGE(bufoff, gbase, voff) do { _Pragma("unroll") for (int _i = 0; _i < 2; ++_i) \
;         __builtin_amdgcn_global_load_lds((const unsigned*)((const char*)(gbase) + (voff)[_i]), (LAS unsigned*)(lds + (bufoff) + ldsw + _i * 8192), 16, 0, 0); } while (0)
; #define PG8_LDA(dst, b, h) do { _Pragma("unroll") for (int m = 0; m < 4; ++m) _Pragma("unroll") for (int k = 0; k < 2; ++k) dst[m][k] = *(const LAS bf16x8*)(lds + PG8_SA(b, h) + aoff + m * 2048 + k * 1024); } while (0)
; #define PG8_LDB(dst, b, h) do { _Pragma("unroll") for (int n = 0; n < 2; ++n) _Pragma("unroll") for (int k = 0; k < 2; ++k) dst[n][k] = *(const LAS bf16x8*)(lds + PG8_SB(b, h) + boff + n * 2048 + k * 1024); } while (0)
; #define PG8_MMA(ai, bj, At, Bt) do { __builtin_amdgcn_s_setprio(1); _Pragma("unroll") for (int m = 0; m < 4; ++m) _Pragma("unroll") for (int n = 0; n < 2; ++n) _Pragma("unroll") for (int k = 0; k < 2; ++k) \
;         acc[ai][bj][m][n] = __builtin_amdgcn_mfma_f32_16x16x32_bf16(Bt[n][k], At[m][k], acc[ai][bj][m][n], 0, 0, 0); __builtin_amdgcn_s_setprio(0); } while (0)
; #define PG8_WAIT_L(n) asm volatile("s_waitcnt lgkmcnt(" #n ")" ::: "memory")
; #define PG8_BAR __builtin_amdgcn_s_barrier()
; #define PG8_SCHED __builtin_amdgcn_sched_barrier(0)
; template <class Epi, class Sched>
; __device__ __forceinline__ void gemm_phase(LAS unsigned char* lds, const bf16_t* A, const int K, const Sched& S, const Epi& E, const int wv) {
;     ...
;         for (int t = 0; t < nt; t += 2) {
;             const bool last = (t == nt - 2);
;             const size_t k1 = (size_t)(t + 1) * kstep;
;             const size_t k2 = last ? 0 : (size_t)(t + 2) * kstep, k3 = k2 + kstep;
;             const char* b2 = last ? nB : cB + (size_t)(t + 2) * kstep; const char* b3 = b2 + kstep;
;             PG8_LDB(B0, 0, 0); PG8_SCHED; PG8_LDA(At, 0, 0); PG8_STAGE_A(PG8_SA(1, 1), 1, false, k1);
;             PG8_WAIT_L(8); PG8_BAR; PG8_WAIT_L(0); PG8_MMA(0, 0, At, B0); PG8_BAR; PG8_SCHED;
;             PG8_LDB(B1, 0, 1); PG8_STAGE(PG8_SB(0, 0), b2, voffB);
;             PG8_BAR; PG8_WAIT_L(0); PG8_MMA(0, 1, At, B1); PG8_BAR;
;             PG8_LDA(At, 0, 1); PG8_STAGE_A(PG8_SA(0, 0), 0, last, k2);
;             PG8_BAR; PG8_WAIT_L(0); PG8_MMA(1, 0, At, B0); PG8_BAR; PG8_SCHED;
.Lmy_ph_4:
.LBB0_1376:
	s_add_u32 s42, s10, 0x100
	ds_read_b128 v[132:135], v208
	ds_read_b128 v[136:139], v208 offset:1024
	ds_read_b128 v[140:143], v208 offset:2048
	ds_read_b128 v[144:147], v208 offset:3072
	s_addc_u32 s43, s11, 0
	s_add_u32 s80, s17, s10
	s_addc_u32 s81, s33, s11
	s_cmp_eq_u32 s77, 28
	s_cselect_b64 s[78:79], -1, 0
	s_and_b64 s[48:49], s[78:79], exec
	s_cselect_b32 s82, 0, s42
	s_cselect_b32 s49, s15, s81
	s_cselect_b32 s48, s18, s80
	v_lshl_add_u64 v[218:219], v[128:129], 0, s[10:11]
	s_add_i32 m0, s61, 0xc000
	ds_read_b128 v[148:151], v209
	ds_read_b128 v[152:155], v209 offset:1024
	ds_read_b128 v[156:159], v209 offset:2048
	ds_read_b128 v[192:195], v209 offset:3072
	ds_read_b128 v[196:199], v209 offset:4096
	ds_read_b128 v[200:203], v209 offset:5120
	ds_read_b128 v[204:207], v209 offset:6144
	ds_read_b128 v[214:217], v209 offset:7168
	global_load_lds_dwordx4 v[218:219], off
	v_lshl_add_u64 v[218:219], v[130:131], 0, s[10:11]
	s_add_i32 m0, s61, 0xe000
	s_nop 0
	global_load_lds_dwordx4 v[218:219], off
	s_waitcnt lgkmcnt(8)
	s_barrier
	s_setprio 1
	s_waitcnt lgkmcnt(7)
	v_mfma_f32_16x16x32_bf16 v[124:127], v[132:135], v[148:151], v[124:127]
	v_mfma_f32_16x16x32_bf16 v[120:123], v[140:143], v[148:151], v[120:123]
	s_waitcnt lgkmcnt(5)
	v_mfma_f32_16x16x32_bf16 v[108:111], v[132:135], v[156:159], v[108:111]
	v_mfma_f32_16x16x32_bf16 v[104:107], v[140:143], v[156:159], v[104:107]
	s_waitcnt lgkmcnt(3)
	v_mfma_f32_16x16x32_bf16 v[92:95], v[132:135], v[196:199], v[92:95]
	v_mfma_f32_16x16x32_bf16 v[88:91], v[140:143], v[196:199], v[88:91]
	s_waitcnt lgkmcnt(1)
	v_mfma_f32_16x16x32_bf16 v[76:79], v[132:135], v[204:207], v[76:79]
	v_mfma_f32_16x16x32_bf16 v[72:75], v[140:143], v[204:207], v[72:75]
	v_mfma_f32_16x16x32_bf16 v[124:127], v[136:139], v[152:155], v[124:127]
	v_mfma_f32_16x16x32_bf16 v[120:123], v[144:147], v[152:155], v[120:123]
	v_mfma_f32_16x16x32_bf16 v[108:111], v[136:139], v[192:195], v[108:111]
	v_mfma_f32_16x16x32_bf16 v[104:107], v[144:147], v[192:195], v[104:107]
	v_mfma_f32_16x16x32_bf16 v[92:95], v[136:139], v[200:203], v[92:95]
	v_mfma_f32_16x16x32_bf16 v[88:91], v[144:147], v[200:203], v[88:91]
	s_waitcnt lgkmcnt(0)
	v_mfma_f32_16x16x32_bf16 v[76:79], v[136:139], v[214:217], v[76:79]
	v_mfma_f32_16x16x32_bf16 v[72:75], v[144:147], v[214:217], v[72:75]
	s_setprio 0
	s_barrier
	s_add_i32 s10, s70, s60
	v_lshl_add_u64 v[234:235], s[48:49], 0, v[162:163]
	s_mov_b32 m0, s10
	ds_read_b128 v[218:221], v210
	ds_read_b128 v[222:225], v210 offset:1024
	ds_read_b128 v[226:229], v210 offset:2048
	ds_read_b128 v[230:233], v210 offset:3072
	global_load_lds_dwordx4 v[234:235], off
	v_lshl_add_u64 v[236:237], s[48:49], 0, v[166:167]
	s_add_i32 m0, s10, 0x2000
	s_nop 0
	global_load_lds_dwordx4 v[236:237], off
	s_barrier
	s_setprio 1
	s_waitcnt lgkmcnt(3)
	v_mfma_f32_16x16x32_bf16 v[116:119], v[218:221], v[148:151], v[116:119]
	s_waitcnt lgkmcnt(1)
	v_mfma_f32_16x16x32_bf16 v[112:115], v[226:229], v[148:151], v[112:115]
	v_mfma_f32_16x16x32_bf16 v[100:103], v[218:221], v[156:159], v[100:103]
	v_mfma_f32_16x16x32_bf16 v[96:99], v[226:229], v[156:159], v[96:99]
	v_mfma_f32_16x16x32_bf16 v[84:87], v[218:221], v[196:199], v[84:87]
	v_mfma_f32_16x16x32_bf16 v[80:83], v[226:229], v[196:199], v[80:83]
	v_mfma_f32_16x16x32_bf16 v[68:71], v[218:221], v[204:207], v[68:71]
	v_mfma_f32_16x16x32_bf16 v[64:67], v[226:229], v[204:207], v[64:67]
	v_mfma_f32_16x16x32_bf16 v[116:119], v[222:225], v[152:155], v[116:119]
	s_waitcnt lgkmcnt(0)
	v_mfma_f32_16x16x32_bf16 v[112:115], v[230:233], v[152:155], v[112:115]
	v_mfma_f32_16x16x32_bf16 v[100:103], v[222:225], v[192:195], v[100:103]
	v_mfma_f32_16x16x32_bf16 v[96:99], v[230:233], v[192:195], v[96:99]
	v_mfma_f32_16x16x32_bf16 v[84:87], v[222:225], v[200:203], v[84:87]
	v_mfma_f32_16x16x32_bf16 v[80:83], v[230:233], v[200:203], v[80:83]
	v_mfma_f32_16x16x32_bf16 v[68:71], v[222:225], v[214:217], v[68:71]
	v_mfma_f32_16x16x32_bf16 v[64:67], v[230:233], v[214:217], v[64:67]
	s_setprio 0
	s_and_b64 s[10:11], s[8:9], s[78:79]
	s_and_b64 s[10:11], s[10:11], exec
	s_cselect_b32 s10, s28, s2
	s_cselect_b32 s11, s29, s3
	s_add_u32 s10, s10, s82
	s_addc_u32 s11, s11, 0
	s_mov_b32 m0, s61
	v_lshl_add_u64 v[238:239], s[10:11], 0, v[160:161]
	s_barrier
	ds_read_b128 v[148:151], v209 offset:16384
	ds_read_b128 v[152:155], v209 offset:17408
	ds_read_b128 v[156:159], v209 offset:18432
	ds_read_b128 v[192:195], v209 offset:19456
	ds_read_b128 v[196:199], v209 offset:20480
	ds_read_b128 v[200:203], v209 offset:21504
	ds_read_b128 v[204:207], v209 offset:22528
	ds_read_b128 v[214:217], v209 offset:23552
	global_load_lds_dwordx4 v[238:239], off
	v_lshl_add_u64 v[240:241], s[10:11], 0, v[164:165]
	s_mov_b32 m0, s62
	s_nop 0
	global_load_lds_dwordx4 v[240:241], off
	s_barrier
	s_setprio 1
	s_waitcnt lgkmcnt(7)
	v_mfma_f32_16x16x32_bf16 v[60:63], v[132:135], v[148:151], v[60:63]
	v_mfma_f32_16x16x32_bf16 v[56:59], v[140:143], v[148:151], v[56:59]
	s_waitcnt lgkmcnt(5)
	v_mfma_f32_16x16x32_bf16 v[44:47], v[132:135], v[156:159], v[44:47]
	v_mfma_f32_16x16x32_bf16 v[40:43], v[140:143], v[156:159], v[40:43]
	s_waitcnt lgkmcnt(3)
	v_mfma_f32_16x16x32_bf16 v[28:31], v[132:135], v[196:199], v[28:31]
	v_mfma_f32_16x16x32_bf16 v[24:27], v[140:143], v[196:199], v[24:27]
	s_waitcnt lgkmcnt(1)
	v_mfma_f32_16x16x32_bf16 v[12:15], v[132:135], v[204:207], v[12:15]
	v_mfma_f32_16x16x32_bf16 v[8:11], v[140:143], v[204:207], v[8:11]
	v_mfma_f32_16x16x32_bf16 v[60:63], v[136:139], v[152:155], v[60:63]
	v_mfma_f32_16x16x32_bf16 v[56:59], v[144:147], v[152:155], v[56:59]
	v_mfma_f32_16x16x32_bf16 v[44:47], v[136:139], v[192:195], v[44:47]
	v_mfma_f32_16x16x32_bf16 v[40:43], v[144:147], v[192:195], v[40:43]
	v_mfma_f32_16x16x32_bf16 v[28:31], v[136:139], v[200:203], v[28:31]
	v_mfma_f32_16x16x32_bf16 v[24:27], v[144:147], v[200:203], v[24:27]
	s_waitcnt lgkmcnt(0)
	v_mfma_f32_16x16x32_bf16 v[12:15], v[136:139], v[214:217], v[12:15]
	v_mfma_f32_16x16x32_bf16 v[8:11], v[144:147], v[214:217], v[8:11]
	s_setprio 0
	s_barrier
; #define PG8_STAGE(bufoff, gbase, voff) do { _Pragma("unroll") for (int _i = 0; _i < 2; ++_i) \
;         __builtin_amdgcn_global_load_lds((const unsigned*)((const char*)(gbase) + (voff)[_i]), (LAS unsigned*)(lds + (bufoff) + ldsw + _i * 8192), 16, 0, 0); } while (0)
; #define PG8_LDA(dst, b, h) do { _Pragma("unroll") for (int m = 0; m < 4; ++m) _Pragma("unroll") for (int k = 0; k < 2; ++k) dst[m][k] = *(const LAS bf16x8*)(lds + PG8_SA(b, h) + aoff + m * 2048 + k * 1024); } while (0)
; #define PG8_LDB(dst, b, h) do { _Pragma("unroll") for (int n = 0; n < 2; ++n) _Pragma("unroll") for (int k = 0; k < 2; ++k) dst[n][k] = *(const LAS bf16x8*)(lds + PG8_SB(b, h) + boff + n * 2048 + k * 1024); } while (0)
; #define PG8_MMA(ai, bj, At, Bt) do { __builtin_amdgcn_s_setprio(1); _Pragma("unroll") for (int m = 0; m < 4; ++m) _Pragma("unroll") for (int n = 0; n < 2; ++n) _Pragma("unroll") for (int k = 0; k < 2; ++k) \
;         acc[ai][bj][m][n] = __builtin_amdgcn_mfma_f32_16x16x32_bf16(Bt[n][k], At[m][k], acc[ai][bj][m][n], 0, 0, 0); __builtin_amdgcn_s_setprio(0); } while (0)
; #define PG8_WAIT_V(n) asm volatile("s_waitcnt vmcnt(" #n ")" ::: "memory")
; #define PG8_WAIT_L(n) asm volatile("s_waitcnt lgkmcnt(" #n ")" ::: "memory")
; #define PG8_BAR __builtin_amdgcn_s_barrier()
; #define PG8_SCHED __builtin_amdgcn_sched_barrier(0)
; template <class Epi, class Sched>
; __device__ __forceinline__ void gemm_phase(LAS unsigned char* lds, const bf16_t* A, const int K, const Sched& S, const Epi& E, const int wv) {
;     ...
;             PG8_STAGE(PG8_SB(0, 1), b2 + hstep, voffB);
;             PG8_WAIT_V(6); PG8_BAR; PG8_MMA(1, 1, At, B1); PG8_BAR;
;             PG8_LDB(B0, 1, 0); PG8_SCHED; PG8_LDA(At, 1, 0); PG8_STAGE_A(PG8_SA(0, 1), 1, last, k2);
;             PG8_WAIT_L(8); PG8_BAR; PG8_WAIT_L(0); PG8_MMA(0, 0, At, B0); PG8_BAR; PG8_SCHED;
;             PG8_LDB(B1, 1, 1); PG8_STAGE(PG8_SB(1, 0), b3, voffB);
	s_add_u32 s78, s48, 0x80000
	s_addc_u32 s79, s49, 0
	s_add_i32 s80, s71, s60
	v_lshl_add_u64 v[132:133], s[78:79], 0, v[162:163]
	s_mov_b32 m0, s80
	s_nop 0
	global_load_lds_dwordx4 v[132:133], off
	v_lshl_add_u64 v[132:133], s[78:79], 0, v[166:167]
	s_add_i32 m0, s80, 0x2000
	s_nop 0
	global_load_lds_dwordx4 v[132:133], off
	s_waitcnt vmcnt(6)
	s_barrier
	s_setprio 1
	v_mfma_f32_16x16x32_bf16 v[52:55], v[218:221], v[148:151], v[52:55]
	v_mfma_f32_16x16x32_bf16 v[48:51], v[226:229], v[148:151], v[48:51]
	v_mfma_f32_16x16x32_bf16 v[36:39], v[218:221], v[156:159], v[36:39]
	v_mfma_f32_16x16x32_bf16 v[32:35], v[226:229], v[156:159], v[32:35]
	v_mfma_f32_16x16x32_bf16 v[20:23], v[218:221], v[196:199], v[20:23]
	v_mfma_f32_16x16x32_bf16 v[16:19], v[226:229], v[196:199], v[16:19]
	v_mfma_f32_16x16x32_bf16 v[4:7], v[218:221], v[204:207], v[4:7]
	v_mfma_f32_16x16x32_bf16 v[0:3], v[226:229], v[204:207], v[0:3]
	v_mfma_f32_16x16x32_bf16 v[52:55], v[222:225], v[152:155], v[52:55]
	v_mfma_f32_16x16x32_bf16 v[48:51], v[230:233], v[152:155], v[48:51]
	v_mfma_f32_16x16x32_bf16 v[36:39], v[222:225], v[192:195], v[36:39]
	v_mfma_f32_16x16x32_bf16 v[32:35], v[230:233], v[192:195], v[32:35]
	v_mfma_f32_16x16x32_bf16 v[20:23], v[222:225], v[200:203], v[20:23]
	v_mfma_f32_16x16x32_bf16 v[16:19], v[230:233], v[200:203], v[16:19]
	v_mfma_f32_16x16x32_bf16 v[4:7], v[222:225], v[214:217], v[4:7]
	v_mfma_f32_16x16x32_bf16 v[0:3], v[230:233], v[214:217], v[0:3]
	s_setprio 0
	s_add_i32 s78, 0, 0x18000
	v_add_u32_e32 v144, s78, v173
	s_barrier
	ds_read_b128 v[132:135], v144
	ds_read_b128 v[136:139], v144 offset:1024
	ds_read_b128 v[140:143], v144 offset:2048
	ds_read_b128 v[144:147], v144 offset:3072
	s_add_u32 s10, s10, 0x80000
	s_addc_u32 s11, s11, 0
	s_mov_b32 m0, s63
	v_lshl_add_u64 v[218:219], s[10:11], 0, v[160:161]
	ds_read_b128 v[148:151], v209 offset:32768
	ds_read_b128 v[152:155], v209 offset:33792
	ds_read_b128 v[156:159], v209 offset:34816
	ds_read_b128 v[192:195], v209 offset:35840
	ds_read_b128 v[196:199], v209 offset:36864
	ds_read_b128 v[200:203], v209 offset:37888
	ds_read_b128 v[204:207], v209 offset:38912
	ds_read_b128 v[214:217], v209 offset:39936
	global_load_lds_dwordx4 v[218:219], off
	v_lshl_add_u64 v[218:219], s[10:11], 0, v[164:165]
	s_mov_b32 m0, s64
	s_nop 0
	global_load_lds_dwordx4 v[218:219], off
	s_waitcnt lgkmcnt(8)
	s_barrier
	s_setprio 1
	s_waitcnt lgkmcnt(7)
	v_mfma_f32_16x16x32_bf16 v[124:127], v[132:135], v[148:151], v[124:127]
	v_mfma_f32_16x16x32_bf16 v[120:123], v[140:143], v[148:151], v[120:123]
	s_waitcnt lgkmcnt(5)
	v_mfma_f32_16x16x32_bf16 v[108:111], v[132:135], v[156:159], v[108:111]
	v_mfma_f32_16x16x32_bf16 v[104:107], v[140:143], v[156:159], v[104:107]
	s_waitcnt lgkmcnt(3)
	v_mfma_f32_16x16x32_bf16 v[92:95], v[132:135], v[196:199], v[92:95]
	v_mfma_f32_16x16x32_bf16 v[88:91], v[140:143], v[196:199], v[88:91]
	s_waitcnt lgkmcnt(1)
	v_mfma_f32_16x16x32_bf16 v[76:79], v[132:135], v[204:207], v[76:79]
	v_mfma_f32_16x16x32_bf16 v[72:75], v[140:143], v[204:207], v[72:75]
	v_mfma_f32_16x16x32_bf16 v[124:127], v[136:139], v[152:155], v[124:127]
	v_mfma_f32_16x16x32_bf16 v[120:123], v[144:147], v[152:155], v[120:123]
	v_mfma_f32_16x16x32_bf16 v[108:111], v[136:139], v[192:195], v[108:111]
	v_mfma_f32_16x16x32_bf16 v[104:107], v[144:147], v[192:195], v[104:107]
	v_mfma_f32_16x16x32_bf16 v[92:95], v[136:139], v[200:203], v[92:95]
	v_mfma_f32_16x16x32_bf16 v[88:91], v[144:147], v[200:203], v[88:91]
	s_waitcnt lgkmcnt(0)
	v_mfma_f32_16x16x32_bf16 v[76:79], v[136:139], v[214:217], v[76:79]
	v_mfma_f32_16x16x32_bf16 v[72:75], v[144:147], v[214:217], v[72:75]
	s_setprio 0
	s_barrier
	s_add_i32 s79, 0, 0x1c000
	s_add_i32 s10, s78, s60
	v_add_u32_e32 v168, s79, v173
	v_lshl_add_u64 v[234:235], v[234:235], 0, s[26:27]
	s_mov_b32 m0, s10
	ds_read_b128 v[218:221], v168
	ds_read_b128 v[222:225], v168 offset:1024
	ds_read_b128 v[226:229], v168 offset:2048
	ds_read_b128 v[230:233], v168 offset:3072
	global_load_lds_dwordx4 v[234:235], off
	v_lshl_add_u64 v[234:235], v[236:237], 0, s[26:27]
	s_add_i32 m0, s10, 0x2000
	s_nop 0
	global_load_lds_dwordx4 v[234:235], off
	s_barrier
; #define PG8_STAGE(bufoff, gbase, voff) do { _Pragma("unroll") for (int _i = 0; _i < 2; ++_i) \
;         __builtin_amdgcn_global_load_lds((const unsigned*)((const char*)(gbase) + (voff)[_i]), (LAS unsigned*)(lds + (bufoff) + ldsw + _i * 8192), 16, 0, 0); } while (0)
; #define PG8_LDA(dst, b, h) do { _Pragma("unroll") for (int m = 0; m < 4; ++m) _Pragma("unroll") for (int k = 0; k < 2; ++k) dst[m][k] = *(const LAS bf16x8*)(lds + PG8_SA(b, h) + aoff + m * 2048 + k * 1024); } while (0)
; #define PG8_LDB(dst, b, h) do { _Pragma("unroll") for (int n = 0; n < 2; ++n) _Pragma("unroll") for (int k = 0; k < 2; ++k) dst[n][k] = *(const LAS bf16x8*)(lds + PG8_SB(b, h) + boff + n * 2048 + k * 1024); } while (0)
; #define PG8_MMA(ai, bj, At, Bt) do { __builtin_amdgcn_s_setprio(1); _Pragma("unroll") for (int m = 0; m < 4; ++m) _Pragma("unroll") for (int n = 0; n < 2; ++n) _Pragma("unroll") for (int k = 0; k < 2; ++k) \
;         acc[ai][bj][m][n] = __builtin_amdgcn_mfma_f32_16x16x32_bf16(Bt[n][k], At[m][k], acc[ai][bj][m][n], 0, 0, 0); __builtin_amdgcn_s_setprio(0); } while (0)
; #define PG8_WAIT_V(n) asm volatile("s_waitcnt vmcnt(" #n ")" ::: "memory")
; #define PG8_WAIT_L(n) asm volatile("s_waitcnt lgkmcnt(" #n ")" ::: "memory")
; #define PG8_BAR __builtin_amdgcn_s_barrier()
; #define PG8_SCHED __builtin_amdgcn_sched_barrier(0)
; template <class Epi, class Sched>
; __device__ __forceinline__ void gemm_phase(LAS unsigned char* lds, const bf16_t* A, const int K, const Sched& S, const Epi& E, const int wv) {
;     ...
;             PG8_LDB(B1, 1, 1); PG8_STAGE(PG8_SB(1, 0), b3, voffB);
;             PG8_BAR; PG8_WAIT_L(0); PG8_MMA(0, 1, At, B1); PG8_BAR;
;             PG8_LDA(At, 1, 1); PG8_STAGE_A(PG8_SA(1, 0), 0, last, k3);
;             PG8_BAR; PG8_WAIT_L(0); PG8_MMA(1, 0, At, B0); PG8_BAR; PG8_SCHED;
;             PG8_STAGE(PG8_SB(1, 1), b3 + hstep, voffB);
;             PG8_WAIT_V(6); PG8_BAR; PG8_MMA(1, 1, At, B1); PG8_BAR;
;         }
	s_setprio 1
	s_waitcnt lgkmcnt(3)
	v_mfma_f32_16x16x32_bf16 v[116:119], v[218:221], v[148:151], v[116:119]
	s_waitcnt lgkmcnt(1)
	v_mfma_f32_16x16x32_bf16 v[112:115], v[226:229], v[148:151], v[112:115]
	v_mfma_f32_16x16x32_bf16 v[100:103], v[218:221], v[156:159], v[100:103]
	v_mfma_f32_16x16x32_bf16 v[96:99], v[226:229], v[156:159], v[96:99]
	v_mfma_f32_16x16x32_bf16 v[84:87], v[218:221], v[196:199], v[84:87]
	v_mfma_f32_16x16x32_bf16 v[80:83], v[226:229], v[196:199], v[80:83]
	v_mfma_f32_16x16x32_bf16 v[68:71], v[218:221], v[204:207], v[68:71]
	v_mfma_f32_16x16x32_bf16 v[64:67], v[226:229], v[204:207], v[64:67]
	v_mfma_f32_16x16x32_bf16 v[116:119], v[222:225], v[152:155], v[116:119]
	s_waitcnt lgkmcnt(0)
	v_mfma_f32_16x16x32_bf16 v[112:115], v[230:233], v[152:155], v[112:115]
	v_mfma_f32_16x16x32_bf16 v[100:103], v[222:225], v[192:195], v[100:103]
	v_mfma_f32_16x16x32_bf16 v[96:99], v[230:233], v[192:195], v[96:99]
	v_mfma_f32_16x16x32_bf16 v[84:87], v[222:225], v[200:203], v[84:87]
	v_mfma_f32_16x16x32_bf16 v[80:83], v[230:233], v[200:203], v[80:83]
	v_mfma_f32_16x16x32_bf16 v[68:71], v[222:225], v[214:217], v[68:71]
	v_mfma_f32_16x16x32_bf16 v[64:67], v[230:233], v[214:217], v[64:67]
	s_setprio 0
	s_mov_b32 m0, s66
	v_lshl_add_u64 v[234:235], v[238:239], 0, s[26:27]
	s_barrier
	ds_read_b128 v[148:151], v209 offset:49152
	ds_read_b128 v[152:155], v209 offset:50176
	ds_read_b128 v[156:159], v209 offset:51200
	ds_read_b128 v[192:195], v209 offset:52224
	ds_read_b128 v[196:199], v209 offset:53248
	ds_read_b128 v[200:203], v209 offset:54272
	ds_read_b128 v[204:207], v209 offset:55296
	ds_read_b128 v[214:217], v209 offset:56320
	global_load_lds_dwordx4 v[234:235], off
	v_lshl_add_u64 v[234:235], v[240:241], 0, s[26:27]
	s_mov_b32 m0, s67
	s_nop 0
	global_load_lds_dwordx4 v[234:235], off
	s_barrier
	s_setprio 1
	s_waitcnt lgkmcnt(7)
	v_mfma_f32_16x16x32_bf16 v[60:63], v[132:135], v[148:151], v[60:63]
	v_mfma_f32_16x16x32_bf16 v[56:59], v[140:143], v[148:151], v[56:59]
	s_waitcnt lgkmcnt(5)
	v_mfma_f32_16x16x32_bf16 v[44:47], v[132:135], v[156:159], v[44:47]
	v_mfma_f32_16x16x32_bf16 v[40:43], v[140:143], v[156:159], v[40:43]
	s_waitcnt lgkmcnt(3)
	v_mfma_f32_16x16x32_bf16 v[28:31], v[132:135], v[196:199], v[28:31]
	v_mfma_f32_16x16x32_bf16 v[24:27], v[140:143], v[196:199], v[24:27]
	s_waitcnt lgkmcnt(1)
	v_mfma_f32_16x16x32_bf16 v[12:15], v[132:135], v[204:207], v[12:15]
	v_mfma_f32_16x16x32_bf16 v[8:11], v[140:143], v[204:207], v[8:11]
	v_mfma_f32_16x16x32_bf16 v[60:63], v[136:139], v[152:155], v[60:63]
	v_mfma_f32_16x16x32_bf16 v[56:59], v[144:147], v[152:155], v[56:59]
	v_mfma_f32_16x16x32_bf16 v[44:47], v[136:139], v[192:195], v[44:47]
	v_mfma_f32_16x16x32_bf16 v[40:43], v[144:147], v[192:195], v[40:43]
	v_mfma_f32_16x16x32_bf16 v[28:31], v[136:139], v[200:203], v[28:31]
	v_mfma_f32_16x16x32_bf16 v[24:27], v[144:147], v[200:203], v[24:27]
	s_waitcnt lgkmcnt(0)
	v_mfma_f32_16x16x32_bf16 v[12:15], v[136:139], v[214:217], v[12:15]
	v_mfma_f32_16x16x32_bf16 v[8:11], v[144:147], v[214:217], v[8:11]
	s_setprio 0
	s_barrier
	s_add_u32 s10, s48, 0x80080
	s_addc_u32 s11, s49, 0
	s_add_i32 s48, s79, s60
	v_lshl_add_u64 v[132:133], s[10:11], 0, v[162:163]
	s_mov_b32 m0, s48
	s_nop 0
	global_load_lds_dwordx4 v[132:133], off
	v_lshl_add_u64 v[132:133], s[10:11], 0, v[166:167]
	s_add_i32 m0, s48, 0x2000
	s_nop 0
	global_load_lds_dwordx4 v[132:133], off
	s_waitcnt vmcnt(6)
	s_barrier
	s_setprio 1
	v_mfma_f32_16x16x32_bf16 v[52:55], v[218:221], v[148:151], v[52:55]
	v_mfma_f32_16x16x32_bf16 v[48:51], v[226:229], v[148:151], v[48:51]
	v_mfma_f32_16x16x32_bf16 v[36:39], v[218:221], v[156:159], v[36:39]
	v_mfma_f32_16x16x32_bf16 v[32:35], v[226:229], v[156:159], v[32:35]
	v_mfma_f32_16x16x32_bf16 v[20:23], v[218:221], v[196:199], v[20:23]
	v_mfma_f32_16x16x32_bf16 v[16:19], v[226:229], v[196:199], v[16:19]
	v_mfma_f32_16x16x32_bf16 v[4:7], v[218:221], v[204:207], v[4:7]
	v_mfma_f32_16x16x32_bf16 v[0:3], v[226:229], v[204:207], v[0:3]
	v_mfma_f32_16x16x32_bf16 v[52:55], v[222:225], v[152:155], v[52:55]
	v_mfma_f32_16x16x32_bf16 v[48:51], v[230:233], v[152:155], v[48:51]
	v_mfma_f32_16x16x32_bf16 v[36:39], v[222:225], v[192:195], v[36:39]
	v_mfma_f32_16x16x32_bf16 v[32:35], v[230:233], v[192:195], v[32:35]
	v_mfma_f32_16x16x32_bf16 v[20:23], v[222:225], v[200:203], v[20:23]
	v_mfma_f32_16x16x32_bf16 v[16:19], v[230:233], v[200:203], v[16:19]
	v_mfma_f32_16x16x32_bf16 v[4:7], v[222:225], v[214:217], v[4:7]
	v_mfma_f32_16x16x32_bf16 v[0:3], v[230:233], v[214:217], v[0:3]
	s_setprio 0
	s_add_i32 s77, s77, 2
	s_cmp_gt_u32 s77, 29
	s_mov_b64 s[10:11], s[42:43]
	s_cbranch_scc1 .Lmy_kx_4
	s_barrier
	s_branch .LBB0_1376

; #define PG8_STAGE(bufoff, gbase, voff) do { _Pragma("unroll") for (int _i = 0; _i < 2; ++_i) \
;         __builtin_amdgcn_global_load_lds((const unsigned*)((const char*)(gbase) + (voff)[_i]), (LAS unsigned*)(lds + (bufoff) + ldsw + _i * 8192), 16, 0, 0); } while (0)
; #define PG8_LDA(dst, b, h) do { _Pragma("unroll") for (int m = 0; m < 4; ++m) _Pragma("unroll") for (int k = 0; k < 2; ++k) dst[m][k] = *(const LAS bf16x8*)(lds + PG8_SA(b, h) + aoff + m * 2048 + k * 1024); } while (0)
; #define PG8_LDB(dst, b, h) do { _Pragma("unroll") for (int n = 0; n < 2; ++n) _Pragma("unroll") for (int k = 0; k < 2; ++k) dst[n][k] = *(const LAS bf16x8*)(lds + PG8_SB(b, h) + boff + n * 2048 + k * 1024); } while (0)
; #define PG8_MMA(ai, bj, At, Bt) do { __builtin_amdgcn_s_setprio(1); _Pragma("unroll") for (int m = 0; m < 4; ++m) _Pragma("unroll") for (int n = 0; n < 2; ++n) _Pragma("unroll") for (int k = 0; k < 2; ++k) \
;         acc[ai][bj][m][n] = __builtin_amdgcn_mfma_f32_16x16x32_bf16(Bt[n][k], At[m][k], acc[ai][bj][m][n], 0, 0, 0); __builtin_amdgcn_s_setprio(0); } while (0)
; #define PG8_WAIT_L(n) asm volatile("s_waitcnt lgkmcnt(" #n ")" ::: "memory")
; #define PG8_BAR __builtin_amdgcn_s_barrier()
; #define PG8_SCHED __builtin_amdgcn_sched_barrier(0)
; template <class Epi, class Sched>
; __device__ __forceinline__ void gemm_phase(LAS unsigned char* lds, const bf16_t* A, const int K, const Sched& S, const Epi& E, const int wv) {
;     ...
;         for (int t = 0; t < nt; t += 2) {
;             const bool last = (t == nt - 2);
;             const size_t k1 = (size_t)(t + 1) * kstep;
;             const size_t k2 = last ? 0 : (size_t)(t + 2) * kstep, k3 = k2 + kstep;
;             const char* b2 = last ? nB : cB + (size_t)(t + 2) * kstep; const char* b3 = b2 + kstep;
;             PG8_LDB(B0, 0, 0); PG8_SCHED; PG8_LDA(At, 0, 0); PG8_STAGE_A(PG8_SA(1, 1), 1, false, k1);
;             PG8_WAIT_L(8); PG8_BAR; PG8_WAIT_L(0); PG8_MMA(0, 0, At, B0); PG8_BAR; PG8_SCHED;
;             PG8_LDB(B1, 0, 1); PG8_STAGE(PG8_SB(0, 0), b2, voffB);
;             PG8_BAR; PG8_WAIT_L(0); PG8_MMA(0, 1, At, B1); PG8_BAR;
;             PG8_LDA(At, 0, 1); PG8_STAGE_A(PG8_SA(0, 0), 0, last, k2);
;             PG8_BAR; PG8_WAIT_L(0); PG8_MMA(1, 0, At, B0); PG8_BAR; PG8_SCHED;
.Lmy_ph_5:
.LBB0_1905:
	s_add_u32 s34, s30, 0x100
	ds_read_b128 v[132:135], v165
	ds_read_b128 v[136:139], v165 offset:1024
	ds_read_b128 v[140:143], v165 offset:2048
	ds_read_b128 v[156:159], v165 offset:3072
	s_addc_u32 s35, s31, 0
	s_add_u32 s65, s21, s30
	s_addc_u32 s68, s63, s31
	s_cmp_eq_u32 s64, 28
	s_cselect_b64 s[66:67], -1, 0
	s_and_b64 s[36:37], s[66:67], exec
	s_cselect_b32 s69, 0, s34
	s_cselect_b32 s37, s19, s68
	s_cselect_b32 s36, s62, s65
	v_lshl_add_u64 v[160:161], v[128:129], 0, s[30:31]
	s_add_i32 m0, s27, 0xc000
	ds_read_b128 v[168:171], v166
	ds_read_b128 v[172:175], v166 offset:1024
	ds_read_b128 v[176:179], v166 offset:2048
	ds_read_b128 v[180:183], v166 offset:3072
	ds_read_b128 v[184:187], v166 offset:4096
	ds_read_b128 v[188:191], v166 offset:5120
	ds_read_b128 v[192:195], v166 offset:6144
	ds_read_b128 v[196:199], v166 offset:7168
	global_load_lds_dwordx4 v[160:161], off
	v_lshl_add_u64 v[160:161], v[130:131], 0, s[30:31]
	s_add_i32 m0, s27, 0xe000
	s_nop 0
	global_load_lds_dwordx4 v[160:161], off
	s_waitcnt lgkmcnt(8)
	s_barrier
	s_setprio 1
	s_waitcnt lgkmcnt(7)
	v_mfma_f32_16x16x32_bf16 v[124:127], v[132:135], v[168:171], v[124:127]
	v_mfma_f32_16x16x32_bf16 v[120:123], v[140:143], v[168:171], v[120:123]
	s_waitcnt lgkmcnt(5)
	v_mfma_f32_16x16x32_bf16 v[116:119], v[132:135], v[176:179], v[116:119]
	v_mfma_f32_16x16x32_bf16 v[112:115], v[140:143], v[176:179], v[112:115]
	s_waitcnt lgkmcnt(3)
	v_mfma_f32_16x16x32_bf16 v[108:111], v[132:135], v[184:187], v[108:111]
	v_mfma_f32_16x16x32_bf16 v[96:99], v[140:143], v[184:187], v[96:99]
	s_waitcnt lgkmcnt(1)
	v_mfma_f32_16x16x32_bf16 v[80:83], v[132:135], v[192:195], v[80:83]
	v_mfma_f32_16x16x32_bf16 v[72:75], v[140:143], v[192:195], v[72:75]
	v_mfma_f32_16x16x32_bf16 v[124:127], v[136:139], v[172:175], v[124:127]
	v_mfma_f32_16x16x32_bf16 v[120:123], v[156:159], v[172:175], v[120:123]
	v_mfma_f32_16x16x32_bf16 v[116:119], v[136:139], v[180:183], v[116:119]
	v_mfma_f32_16x16x32_bf16 v[112:115], v[156:159], v[180:183], v[112:115]
	v_mfma_f32_16x16x32_bf16 v[108:111], v[136:139], v[188:191], v[108:111]
	v_mfma_f32_16x16x32_bf16 v[96:99], v[156:159], v[188:191], v[96:99]
	s_waitcnt lgkmcnt(0)
	v_mfma_f32_16x16x32_bf16 v[80:83], v[136:139], v[196:199], v[80:83]
	v_mfma_f32_16x16x32_bf16 v[72:75], v[156:159], v[196:199], v[72:75]
	s_setprio 0
	s_barrier
	s_add_i32 s30, s55, s43
	v_lshl_add_u64 v[160:161], s[36:37], 0, v[144:145]
	s_mov_b32 m0, s30
	ds_read_b128 v[200:203], v167
	ds_read_b128 v[204:207], v167 offset:1024
	ds_read_b128 v[208:211], v167 offset:2048
	ds_read_b128 v[212:215], v167 offset:3072
	global_load_lds_dwordx4 v[160:161], off
	v_lshl_add_u64 v[216:217], s[36:37], 0, v[146:147]
	s_add_i32 m0, s30, 0x2000
	s_nop 0
	global_load_lds_dwordx4 v[216:217], off
	s_barrier
	s_setprio 1
	s_waitcnt lgkmcnt(3)
	v_mfma_f32_16x16x32_bf16 v[104:107], v[200:203], v[168:171], v[104:107]
	s_waitcnt lgkmcnt(1)
	v_mfma_f32_16x16x32_bf16 v[100:103], v[208:211], v[168:171], v[100:103]
	v_mfma_f32_16x16x32_bf16 v[92:95], v[200:203], v[176:179], v[92:95]
	v_mfma_f32_16x16x32_bf16 v[88:91], v[208:211], v[176:179], v[88:91]
	v_mfma_f32_16x16x32_bf16 v[84:87], v[200:203], v[184:187], v[84:87]
	v_mfma_f32_16x16x32_bf16 v[76:79], v[208:211], v[184:187], v[76:79]
	v_mfma_f32_16x16x32_bf16 v[68:71], v[200:203], v[192:195], v[68:71]
	v_mfma_f32_16x16x32_bf16 v[64:67], v[208:211], v[192:195], v[64:67]
	v_mfma_f32_16x16x32_bf16 v[104:107], v[204:207], v[172:175], v[104:107]
	s_waitcnt lgkmcnt(0)
	v_mfma_f32_16x16x32_bf16 v[100:103], v[212:215], v[172:175], v[100:103]
	v_mfma_f32_16x16x32_bf16 v[92:95], v[204:207], v[180:183], v[92:95]
	v_mfma_f32_16x16x32_bf16 v[88:91], v[212:215], v[180:183], v[88:91]
	v_mfma_f32_16x16x32_bf16 v[84:87], v[204:207], v[188:191], v[84:87]
	v_mfma_f32_16x16x32_bf16 v[76:79], v[212:215], v[188:191], v[76:79]
	v_mfma_f32_16x16x32_bf16 v[68:71], v[204:207], v[196:199], v[68:71]
	v_mfma_f32_16x16x32_bf16 v[64:67], v[212:215], v[196:199], v[64:67]
	s_setprio 0
	s_and_b64 s[30:31], s[4:5], s[66:67]
	s_and_b64 s[30:31], s[30:31], exec
	s_cselect_b32 s30, s24, s28
	s_cselect_b32 s31, s25, s29
	s_add_u32 s30, s30, s69
	s_addc_u32 s31, s31, 0
	s_mov_b32 m0, s27
	v_lshl_add_u64 v[218:219], s[30:31], 0, v[144:145]
	s_barrier
	ds_read_b128 v[168:171], v166 offset:16384
	ds_read_b128 v[172:175], v166 offset:17408
	ds_read_b128 v[176:179], v166 offset:18432
	ds_read_b128 v[180:183], v166 offset:19456
	ds_read_b128 v[184:187], v166 offset:20480
	ds_read_b128 v[188:191], v166 offset:21504
	ds_read_b128 v[192:195], v166 offset:22528
	ds_read_b128 v[196:199], v166 offset:23552
	global_load_lds_dwordx4 v[218:219], off
	v_lshl_add_u64 v[220:221], s[30:31], 0, v[146:147]
	s_mov_b32 m0, s44
	s_nop 0
	global_load_lds_dwordx4 v[220:221], off
	s_barrier
	s_setprio 1
	s_waitcnt lgkmcnt(7)
	v_mfma_f32_16x16x32_bf16 v[60:63], v[132:135], v[168:171], v[60:63]
	v_mfma_f32_16x16x32_bf16 v[56:59], v[140:143], v[168:171], v[56:59]
	s_waitcnt lgkmcnt(5)
	v_mfma_f32_16x16x32_bf16 v[52:55], v[132:135], v[176:179], v[52:55]
	v_mfma_f32_16x16x32_bf16 v[48:51], v[140:143], v[176:179], v[48:51]
	s_waitcnt lgkmcnt(3)
	v_mfma_f32_16x16x32_bf16 v[44:47], v[132:135], v[184:187], v[44:47]
	v_mfma_f32_16x16x32_bf16 v[32:35], v[140:143], v[184:187], v[32:35]
	s_waitcnt lgkmcnt(1)
	v_mfma_f32_16x16x32_bf16 v[16:19], v[132:135], v[192:195], v[16:19]
	v_mfma_f32_16x16x32_bf16 v[8:11], v[140:143], v[192:195], v[8:11]
	v_mfma_f32_16x16x32_bf16 v[60:63], v[136:139], v[172:175], v[60:63]
	v_mfma_f32_16x16x32_bf16 v[56:59], v[156:159], v[172:175], v[56:59]
	v_mfma_f32_16x16x32_bf16 v[52:55], v[136:139], v[180:183], v[52:55]
	v_mfma_f32_16x16x32_bf16 v[48:51], v[156:159], v[180:183], v[48:51]
	v_mfma_f32_16x16x32_bf16 v[44:47], v[136:139], v[188:191], v[44:47]
	v_mfma_f32_16x16x32_bf16 v[32:35], v[156:159], v[188:191], v[32:35]
	s_waitcnt lgkmcnt(0)
	v_mfma_f32_16x16x32_bf16 v[16:19], v[136:139], v[196:199], v[16:19]
	v_mfma_f32_16x16x32_bf16 v[8:11], v[156:159], v[196:199], v[8:11]
	s_setprio 0
	s_barrier
; #define PG8_STAGE(bufoff, gbase, voff) do { _Pragma("unroll") for (int _i = 0; _i < 2; ++_i) \
;         __builtin_amdgcn_global_load_lds((const unsigned*)((const char*)(gbase) + (voff)[_i]), (LAS unsigned*)(lds + (bufoff) + ldsw + _i * 8192), 16, 0, 0); } while (0)
; #define PG8_LDA(dst, b, h) do { _Pragma("unroll") for (int m = 0; m < 4; ++m) _Pragma("unroll") for (int k = 0; k < 2; ++k) dst[m][k] = *(const LAS bf16x8*)(lds + PG8_SA(b, h) + aoff + m * 2048 + k * 1024); } while (0)
; #define PG8_LDB(dst, b, h) do { _Pragma("unroll") for (int n = 0; n < 2; ++n) _Pragma("unroll") for (int k = 0; k < 2; ++k) dst[n][k] = *(const LAS bf16x8*)(lds + PG8_SB(b, h) + boff + n * 2048 + k * 1024); } while (0)
; #define PG8_MMA(ai, bj, At, Bt) do { __builtin_amdgcn_s_setprio(1); _Pragma("unroll") for (int m = 0; m < 4; ++m) _Pragma("unroll") for (int n = 0; n < 2; ++n) _Pragma("unroll") for (int k = 0; k < 2; ++k) \
;         acc[ai][bj][m][n] = __builtin_amdgcn_mfma_f32_16x16x32_bf16(Bt[n][k], At[m][k], acc[ai][bj][m][n], 0, 0, 0); __builtin_amdgcn_s_setprio(0); } while (0)
; #define PG8_WAIT_V(n) asm volatile("s_waitcnt vmcnt(" #n ")" ::: "memory")
; #define PG8_WAIT_L(n) asm volatile("s_waitcnt lgkmcnt(" #n ")" ::: "memory")
; #define PG8_BAR __builtin_amdgcn_s_barrier()
; #define PG8_SCHED __builtin_amdgcn_sched_barrier(0)
; template <class Epi, class Sched>
; __device__ __forceinline__ void gemm_phase(LAS unsigned char* lds, const bf16_t* A, const int K, const Sched& S, const Epi& E, const int wv) {
;     ...
;             PG8_STAGE(PG8_SB(0, 1), b2 + hstep, voffB);
;             PG8_WAIT_V(6); PG8_BAR; PG8_MMA(1, 1, At, B1); PG8_BAR;
;             PG8_LDB(B0, 1, 0); PG8_SCHED; PG8_LDA(At, 1, 0); PG8_STAGE_A(PG8_SA(0, 1), 1, last, k2);
;             PG8_WAIT_L(8); PG8_BAR; PG8_WAIT_L(0); PG8_MMA(0, 0, At, B0); PG8_BAR; PG8_SCHED;
;             PG8_LDB(B1, 1, 1); PG8_STAGE(PG8_SB(1, 0), b3, voffB);
	s_add_u32 s66, s36, 0x80000
	s_addc_u32 s67, s37, 0
	s_add_i32 s65, s60, s43
	v_lshl_add_u64 v[132:133], s[66:67], 0, v[144:145]
	s_mov_b32 m0, s65
	s_nop 0
	global_load_lds_dwordx4 v[132:133], off
	v_lshl_add_u64 v[132:133], s[66:67], 0, v[146:147]
	s_add_i32 m0, s65, 0x2000
	s_nop 0
	global_load_lds_dwordx4 v[132:133], off
	s_waitcnt vmcnt(6)
	s_barrier
	s_setprio 1
	v_mfma_f32_16x16x32_bf16 v[40:43], v[200:203], v[168:171], v[40:43]
	v_mfma_f32_16x16x32_bf16 v[36:39], v[208:211], v[168:171], v[36:39]
	v_mfma_f32_16x16x32_bf16 v[28:31], v[200:203], v[176:179], v[28:31]
	v_mfma_f32_16x16x32_bf16 v[24:27], v[208:211], v[176:179], v[24:27]
	v_mfma_f32_16x16x32_bf16 v[20:23], v[200:203], v[184:187], v[20:23]
	v_mfma_f32_16x16x32_bf16 v[12:15], v[208:211], v[184:187], v[12:15]
	v_mfma_f32_16x16x32_bf16 v[4:7], v[200:203], v[192:195], v[4:7]
	v_mfma_f32_16x16x32_bf16 v[0:3], v[208:211], v[192:195], v[0:3]
	v_mfma_f32_16x16x32_bf16 v[40:43], v[204:207], v[172:175], v[40:43]
	v_mfma_f32_16x16x32_bf16 v[36:39], v[212:215], v[172:175], v[36:39]
	v_mfma_f32_16x16x32_bf16 v[28:31], v[204:207], v[180:183], v[28:31]
	v_mfma_f32_16x16x32_bf16 v[24:27], v[212:215], v[180:183], v[24:27]
	v_mfma_f32_16x16x32_bf16 v[20:23], v[204:207], v[188:191], v[20:23]
	v_mfma_f32_16x16x32_bf16 v[12:15], v[212:215], v[188:191], v[12:15]
	v_mfma_f32_16x16x32_bf16 v[4:7], v[204:207], v[196:199], v[4:7]
	v_mfma_f32_16x16x32_bf16 v[0:3], v[212:215], v[196:199], v[0:3]
	s_setprio 0
	s_add_i32 s65, 0, 0x18000
	v_add_u32_e32 v156, s65, v163
	s_barrier
	ds_read_b128 v[132:135], v156
	ds_read_b128 v[136:139], v156 offset:1024
	ds_read_b128 v[140:143], v156 offset:2048
	ds_read_b128 v[156:159], v156 offset:3072
	s_add_u32 s30, s30, 0x80000
	s_addc_u32 s31, s31, 0
	s_mov_b32 m0, s45
	v_lshl_add_u64 v[200:201], s[30:31], 0, v[144:145]
	ds_read_b128 v[168:171], v166 offset:32768
	ds_read_b128 v[172:175], v166 offset:33792
	ds_read_b128 v[176:179], v166 offset:34816
	ds_read_b128 v[180:183], v166 offset:35840
	ds_read_b128 v[184:187], v166 offset:36864
	ds_read_b128 v[188:191], v166 offset:37888
	ds_read_b128 v[192:195], v166 offset:38912
	ds_read_b128 v[196:199], v166 offset:39936
	global_load_lds_dwordx4 v[200:201], off
	v_lshl_add_u64 v[200:201], s[30:31], 0, v[146:147]
	s_mov_b32 m0, s46
	s_nop 0
	global_load_lds_dwordx4 v[200:201], off
	s_waitcnt lgkmcnt(8)
	s_barrier
	s_setprio 1
	s_waitcnt lgkmcnt(7)
	v_mfma_f32_16x16x32_bf16 v[124:127], v[132:135], v[168:171], v[124:127]
	v_mfma_f32_16x16x32_bf16 v[120:123], v[140:143], v[168:171], v[120:123]
	s_waitcnt lgkmcnt(5)
	v_mfma_f32_16x16x32_bf16 v[116:119], v[132:135], v[176:179], v[116:119]
	v_mfma_f32_16x16x32_bf16 v[112:115], v[140:143], v[176:179], v[112:115]
	s_waitcnt lgkmcnt(3)
	v_mfma_f32_16x16x32_bf16 v[108:111], v[132:135], v[184:187], v[108:111]
	v_mfma_f32_16x16x32_bf16 v[96:99], v[140:143], v[184:187], v[96:99]
	s_waitcnt lgkmcnt(1)
	v_mfma_f32_16x16x32_bf16 v[80:83], v[132:135], v[192:195], v[80:83]
	v_mfma_f32_16x16x32_bf16 v[72:75], v[140:143], v[192:195], v[72:75]
	v_mfma_f32_16x16x32_bf16 v[124:127], v[136:139], v[172:175], v[124:127]
	v_mfma_f32_16x16x32_bf16 v[120:123], v[156:159], v[172:175], v[120:123]
	v_mfma_f32_16x16x32_bf16 v[116:119], v[136:139], v[180:183], v[116:119]
	v_mfma_f32_16x16x32_bf16 v[112:115], v[156:159], v[180:183], v[112:115]
	v_mfma_f32_16x16x32_bf16 v[108:111], v[136:139], v[188:191], v[108:111]
	v_mfma_f32_16x16x32_bf16 v[96:99], v[156:159], v[188:191], v[96:99]
	s_waitcnt lgkmcnt(0)
	v_mfma_f32_16x16x32_bf16 v[80:83], v[136:139], v[196:199], v[80:83]
	v_mfma_f32_16x16x32_bf16 v[72:75], v[156:159], v[196:199], v[72:75]
	s_setprio 0
	s_barrier
	s_add_i32 s66, 0, 0x1c000
	s_add_i32 s30, s65, s43
	v_add_u32_e32 v212, s66, v163
	v_lshl_add_u64 v[160:161], v[160:161], 0, s[8:9]
	s_mov_b32 m0, s30
	ds_read_b128 v[200:203], v212
	ds_read_b128 v[204:207], v212 offset:1024
	ds_read_b128 v[208:211], v212 offset:2048
	ds_read_b128 v[212:215], v212 offset:3072
	global_load_lds_dwordx4 v[160:161], off
	v_lshl_add_u64 v[160:161], v[216:217], 0, s[8:9]
	s_add_i32 m0, s30, 0x2000
	s_nop 0
	global_load_lds_dwordx4 v[160:161], off
	s_barrier
; #define PG8_STAGE(bufoff, gbase, voff) do { _Pragma("unroll") for (int _i = 0; _i < 2; ++_i) \
;         __builtin_amdgcn_global_load_lds((const unsigned*)((const char*)(gbase) + (voff)[_i]), (LAS unsigned*)(lds + (bufoff) + ldsw + _i * 8192), 16, 0, 0); } while (0)
; #define PG8_LDA(dst, b, h) do { _Pragma("unroll") for (int m = 0; m < 4; ++m) _Pragma("unroll") for (int k = 0; k < 2; ++k) dst[m][k] = *(const LAS bf16x8*)(lds + PG8_SA(b, h) + aoff + m * 2048 + k * 1024); } while (0)
; #define PG8_LDB(dst, b, h) do { _Pragma("unroll") for (int n = 0; n < 2; ++n) _Pragma("unroll") for (int k = 0; k < 2; ++k) dst[n][k] = *(const LAS bf16x8*)(lds + PG8_SB(b, h) + boff + n * 2048 + k * 1024); } while (0)
; #define PG8_MMA(ai, bj, At, Bt) do { __builtin_amdgcn_s_setprio(1); _Pragma("unroll") for (int m = 0; m < 4; ++m) _Pragma("unroll") for (int n = 0; n < 2; ++n) _Pragma("unroll") for (int k = 0; k < 2; ++k) \
;         acc[ai][bj][m][n] = __builtin_amdgcn_mfma_f32_16x16x32_bf16(Bt[n][k], At[m][k], acc[ai][bj][m][n], 0, 0, 0); __builtin_amdgcn_s_setprio(0); } while (0)
; #define PG8_WAIT_V(n) asm volatile("s_waitcnt vmcnt(" #n ")" ::: "memory")
; #define PG8_WAIT_L(n) asm volatile("s_waitcnt lgkmcnt(" #n ")" ::: "memory")
; #define PG8_BAR __builtin_amdgcn_s_barrier()
; #define PG8_SCHED __builtin_amdgcn_sched_barrier(0)
; template <class Epi, class Sched>
; __device__ __forceinline__ void gemm_phase(LAS unsigned char* lds, const bf16_t* A, const int K, const Sched& S, const Epi& E, const int wv) {
;     ...
;             PG8_LDB(B1, 1, 1); PG8_STAGE(PG8_SB(1, 0), b3, voffB);
;             PG8_BAR; PG8_WAIT_L(0); PG8_MMA(0, 1, At, B1); PG8_BAR;
;             PG8_LDA(At, 1, 1); PG8_STAGE_A(PG8_SA(1, 0), 0, last, k3);
;             PG8_BAR; PG8_WAIT_L(0); PG8_MMA(1, 0, At, B0); PG8_BAR; PG8_SCHED;
;             PG8_STAGE(PG8_SB(1, 1), b3 + hstep, voffB);
;             PG8_WAIT_V(6); PG8_BAR; PG8_MMA(1, 1, At, B1); PG8_BAR;
;         }
	s_setprio 1
	s_waitcnt lgkmcnt(3)
	v_mfma_f32_16x16x32_bf16 v[104:107], v[200:203], v[168:171], v[104:107]
	s_waitcnt lgkmcnt(1)
	v_mfma_f32_16x16x32_bf16 v[100:103], v[208:211], v[168:171], v[100:103]
	v_mfma_f32_16x16x32_bf16 v[92:95], v[200:203], v[176:179], v[92:95]
	v_mfma_f32_16x16x32_bf16 v[88:91], v[208:211], v[176:179], v[88:91]
	v_mfma_f32_16x16x32_bf16 v[84:87], v[200:203], v[184:187], v[84:87]
	v_mfma_f32_16x16x32_bf16 v[76:79], v[208:211], v[184:187], v[76:79]
	v_mfma_f32_16x16x32_bf16 v[68:71], v[200:203], v[192:195], v[68:71]
	v_mfma_f32_16x16x32_bf16 v[64:67], v[208:211], v[192:195], v[64:67]
	v_mfma_f32_16x16x32_bf16 v[104:107], v[204:207], v[172:175], v[104:107]
	s_waitcnt lgkmcnt(0)
	v_mfma_f32_16x16x32_bf16 v[100:103], v[212:215], v[172:175], v[100:103]
	v_mfma_f32_16x16x32_bf16 v[92:95], v[204:207], v[180:183], v[92:95]
	v_mfma_f32_16x16x32_bf16 v[88:91], v[212:215], v[180:183], v[88:91]
	v_mfma_f32_16x16x32_bf16 v[84:87], v[204:207], v[188:191], v[84:87]
	v_mfma_f32_16x16x32_bf16 v[76:79], v[212:215], v[188:191], v[76:79]
	v_mfma_f32_16x16x32_bf16 v[68:71], v[204:207], v[196:199], v[68:71]
	v_mfma_f32_16x16x32_bf16 v[64:67], v[212:215], v[196:199], v[64:67]
	s_setprio 0
	s_mov_b32 m0, s50
	v_lshl_add_u64 v[160:161], v[218:219], 0, s[8:9]
	s_barrier
	ds_read_b128 v[168:171], v166 offset:49152
	ds_read_b128 v[172:175], v166 offset:50176
	ds_read_b128 v[176:179], v166 offset:51200
	ds_read_b128 v[180:183], v166 offset:52224
	ds_read_b128 v[184:187], v166 offset:53248
	ds_read_b128 v[188:191], v166 offset:54272
	ds_read_b128 v[192:195], v166 offset:55296
	ds_read_b128 v[196:199], v166 offset:56320
	global_load_lds_dwordx4 v[160:161], off
	v_lshl_add_u64 v[160:161], v[220:221], 0, s[8:9]
	s_mov_b32 m0, s51
	s_nop 0
	global_load_lds_dwordx4 v[160:161], off
	s_barrier
	s_setprio 1
	s_waitcnt lgkmcnt(7)
	v_mfma_f32_16x16x32_bf16 v[60:63], v[132:135], v[168:171], v[60:63]
	v_mfma_f32_16x16x32_bf16 v[56:59], v[140:143], v[168:171], v[56:59]
	s_waitcnt lgkmcnt(5)
	v_mfma_f32_16x16x32_bf16 v[52:55], v[132:135], v[176:179], v[52:55]
	v_mfma_f32_16x16x32_bf16 v[48:51], v[140:143], v[176:179], v[48:51]
	s_waitcnt lgkmcnt(3)
	v_mfma_f32_16x16x32_bf16 v[44:47], v[132:135], v[184:187], v[44:47]
	v_mfma_f32_16x16x32_bf16 v[32:35], v[140:143], v[184:187], v[32:35]
	s_waitcnt lgkmcnt(1)
	v_mfma_f32_16x16x32_bf16 v[16:19], v[132:135], v[192:195], v[16:19]
	v_mfma_f32_16x16x32_bf16 v[8:11], v[140:143], v[192:195], v[8:11]
	v_mfma_f32_16x16x32_bf16 v[60:63], v[136:139], v[172:175], v[60:63]
	v_mfma_f32_16x16x32_bf16 v[56:59], v[156:159], v[172:175], v[56:59]
	v_mfma_f32_16x16x32_bf16 v[52:55], v[136:139], v[180:183], v[52:55]
	v_mfma_f32_16x16x32_bf16 v[48:51], v[156:159], v[180:183], v[48:51]
	v_mfma_f32_16x16x32_bf16 v[44:47], v[136:139], v[188:191], v[44:47]
	v_mfma_f32_16x16x32_bf16 v[32:35], v[156:159], v[188:191], v[32:35]
	s_waitcnt lgkmcnt(0)
	v_mfma_f32_16x16x32_bf16 v[16:19], v[136:139], v[196:199], v[16:19]
	v_mfma_f32_16x16x32_bf16 v[8:11], v[156:159], v[196:199], v[8:11]
	s_setprio 0
	s_barrier
	s_add_u32 s30, s36, 0x80080
	s_addc_u32 s31, s37, 0
	s_add_i32 s36, s66, s43
	v_lshl_add_u64 v[132:133], s[30:31], 0, v[144:145]
	s_mov_b32 m0, s36
	s_nop 0
	global_load_lds_dwordx4 v[132:133], off
	v_lshl_add_u64 v[132:133], s[30:31], 0, v[146:147]
	s_add_i32 m0, s36, 0x2000
	s_nop 0
	global_load_lds_dwordx4 v[132:133], off
	s_waitcnt vmcnt(6)
	s_barrier
	s_setprio 1
	v_mfma_f32_16x16x32_bf16 v[40:43], v[200:203], v[168:171], v[40:43]
	v_mfma_f32_16x16x32_bf16 v[36:39], v[208:211], v[168:171], v[36:39]
	v_mfma_f32_16x16x32_bf16 v[28:31], v[200:203], v[176:179], v[28:31]
	v_mfma_f32_16x16x32_bf16 v[24:27], v[208:211], v[176:179], v[24:27]
	v_mfma_f32_16x16x32_bf16 v[20:23], v[200:203], v[184:187], v[20:23]
	v_mfma_f32_16x16x32_bf16 v[12:15], v[208:211], v[184:187], v[12:15]
	v_mfma_f32_16x16x32_bf16 v[4:7], v[200:203], v[192:195], v[4:7]
	v_mfma_f32_16x16x32_bf16 v[0:3], v[208:211], v[192:195], v[0:3]
	v_mfma_f32_16x16x32_bf16 v[40:43], v[204:207], v[172:175], v[40:43]
	v_mfma_f32_16x16x32_bf16 v[36:39], v[212:215], v[172:175], v[36:39]
	v_mfma_f32_16x16x32_bf16 v[28:31], v[204:207], v[180:183], v[28:31]
	v_mfma_f32_16x16x32_bf16 v[24:27], v[212:215], v[180:183], v[24:27]
	v_mfma_f32_16x16x32_bf16 v[20:23], v[204:207], v[188:191], v[20:23]
	v_mfma_f32_16x16x32_bf16 v[12:15], v[212:215], v[188:191], v[12:15]
	v_mfma_f32_16x16x32_bf16 v[4:7], v[204:207], v[196:199], v[4:7]
	v_mfma_f32_16x16x32_bf16 v[0:3], v[212:215], v[196:199], v[0:3]
	s_setprio 0
	s_add_i32 s64, s64, 2
	s_cmp_gt_u32 s64, 29
	s_mov_b64 s[30:31], s[34:35]
	s_cbranch_scc1 .Lmy_kx_5
	s_barrier
	s_branch .LBB0_1905

; #define PG8_STAGE(bufoff, gbase, voff) do { _Pragma("unroll") for (int _i = 0; _i < 2; ++_i) \
;         __builtin_amdgcn_global_load_lds((const unsigned*)((const char*)(gbase) + (voff)[_i]), (LAS unsigned*)(lds + (bufoff) + ldsw + _i * 8192), 16, 0, 0); } while (0)
; #define PG8_LDA(dst, b, h) do { _Pragma("unroll") for (int m = 0; m < 4; ++m) _Pragma("unroll") for (int k = 0; k < 2; ++k) dst[m][k] = *(const LAS bf16x8*)(lds + PG8_SA(b, h) + aoff + m * 2048 + k * 1024); } while (0)
; #define PG8_LDB(dst, b, h) do { _Pragma("unroll") for (int n = 0; n < 2; ++n) _Pragma("unroll") for (int k = 0; k < 2; ++k) dst[n][k] = *(const LAS bf16x8*)(lds + PG8_SB(b, h) + boff + n * 2048 + k * 1024); } while (0)
; #define PG8_MMA(ai, bj, At, Bt) do { __builtin_amdgcn_s_setprio(1); _Pragma("unroll") for (int m = 0; m < 4; ++m) _Pragma("unroll") for (int n = 0; n < 2; ++n) _Pragma("unroll") for (int k = 0; k < 2; ++k) \
;         acc[ai][bj][m][n] = __builtin_amdgcn_mfma_f32_16x16x32_bf16(Bt[n][k], At[m][k], acc[ai][bj][m][n], 0, 0, 0); __builtin_amdgcn_s_setprio(0); } while (0)
; #define PG8_WAIT_L(n) asm volatile("s_waitcnt lgkmcnt(" #n ")" ::: "memory")
; #define PG8_BAR __builtin_amdgcn_s_barrier()
; #define PG8_SCHED __builtin_amdgcn_sched_barrier(0)
; template <class Epi, class Sched>
; __device__ __forceinline__ void gemm_phase(LAS unsigned char* lds, const bf16_t* A, const int K, const Sched& S, const Epi& E, const int wv) {
;     ...
;         for (int t = 0; t < nt; t += 2) {
;             const bool last = (t == nt - 2);
;             const size_t k1 = (size_t)(t + 1) * kstep;
;             const size_t k2 = last ? 0 : (size_t)(t + 2) * kstep, k3 = k2 + kstep;
;             const char* b2 = last ? nB : cB + (size_t)(t + 2) * kstep; const char* b3 = b2 + kstep;
;             PG8_LDB(B0, 0, 0); PG8_SCHED; PG8_LDA(At, 0, 0); PG8_STAGE_A(PG8_SA(1, 1), 1, false, k1);
;             PG8_WAIT_L(8); PG8_BAR; PG8_WAIT_L(0); PG8_MMA(0, 0, At, B0); PG8_BAR; PG8_SCHED;
;             PG8_LDB(B1, 0, 1); PG8_STAGE(PG8_SB(0, 0), b2, voffB);
;             PG8_BAR; PG8_WAIT_L(0); PG8_MMA(0, 1, At, B1); PG8_BAR;
;             PG8_LDA(At, 0, 1); PG8_STAGE_A(PG8_SA(0, 0), 0, last, k2);
;             PG8_BAR; PG8_WAIT_L(0); PG8_MMA(1, 0, At, B0); PG8_BAR; PG8_SCHED;
.Lmy_ph_6:
.LBB0_2080:
	v_add_u32_e32 v132, s52, v149
	s_add_u32 s22, s0, 0x100
	ds_read_b128 v[174:177], v132
	ds_read_b128 v[178:181], v132 offset:1024
	ds_read_b128 v[182:185], v132 offset:2048
	ds_read_b128 v[186:189], v132 offset:3072
	s_addc_u32 s23, s1, 0
	s_add_u32 s71, s15, s0
	s_addc_u32 s72, s17, s1
	s_cmpk_eq_i32 s0, 0xf00
	s_cselect_b64 vcc, -1, 0
	s_and_b64 s[24:25], vcc, exec
	s_cselect_b32 s73, 0, s22
	s_cselect_b32 s25, s19, s72
	s_cselect_b32 s24, s18, s71
	s_mov_b32 m0, s54
	v_lshl_add_u64 v[222:223], v[142:143], 0, s[0:1]
	ds_read_b128 v[190:193], v167
	ds_read_b128 v[194:197], v167 offset:1024
	ds_read_b128 v[198:201], v167 offset:2048
	ds_read_b128 v[202:205], v167 offset:3072
	ds_read_b128 v[206:209], v167 offset:4096
	ds_read_b128 v[210:213], v167 offset:5120
	ds_read_b128 v[214:217], v167 offset:6144
	ds_read_b128 v[218:221], v167 offset:7168
	global_load_lds_dwordx4 v[222:223], off
	v_lshl_add_u64 v[222:223], v[140:141], 0, s[0:1]
	s_mov_b32 m0, s55
	s_nop 0
	global_load_lds_dwordx4 v[222:223], off
	s_waitcnt lgkmcnt(8)
	s_barrier
	s_setprio 1
	s_waitcnt lgkmcnt(7)
	v_mfma_f32_16x16x32_bf16 v[124:127], v[174:177], v[190:193], v[124:127]
	v_mfma_f32_16x16x32_bf16 v[120:123], v[182:185], v[190:193], v[120:123]
	s_waitcnt lgkmcnt(5)
	v_mfma_f32_16x16x32_bf16 v[108:111], v[174:177], v[198:201], v[108:111]
	v_mfma_f32_16x16x32_bf16 v[104:107], v[182:185], v[198:201], v[104:107]
	s_waitcnt lgkmcnt(3)
	v_mfma_f32_16x16x32_bf16 v[92:95], v[174:177], v[206:209], v[92:95]
	v_mfma_f32_16x16x32_bf16 v[88:91], v[182:185], v[206:209], v[88:91]
	s_waitcnt lgkmcnt(1)
	v_mfma_f32_16x16x32_bf16 v[76:79], v[174:177], v[214:217], v[76:79]
	v_mfma_f32_16x16x32_bf16 v[72:75], v[182:185], v[214:217], v[72:75]
	v_mfma_f32_16x16x32_bf16 v[124:127], v[178:181], v[194:197], v[124:127]
	v_mfma_f32_16x16x32_bf16 v[120:123], v[186:189], v[194:197], v[120:123]
	v_mfma_f32_16x16x32_bf16 v[108:111], v[178:181], v[202:205], v[108:111]
	v_mfma_f32_16x16x32_bf16 v[104:107], v[186:189], v[202:205], v[104:107]
	v_mfma_f32_16x16x32_bf16 v[92:95], v[178:181], v[210:213], v[92:95]
	v_mfma_f32_16x16x32_bf16 v[88:91], v[186:189], v[210:213], v[88:91]
	s_waitcnt lgkmcnt(0)
	v_mfma_f32_16x16x32_bf16 v[76:79], v[178:181], v[218:221], v[76:79]
	v_mfma_f32_16x16x32_bf16 v[72:75], v[186:189], v[218:221], v[72:75]
	s_setprio 0
	s_barrier
	s_mov_b32 m0, s56
	v_add_u32_e32 v132, s53, v149
	v_lshl_add_u64 v[238:239], s[24:25], 0, v[128:129]
	ds_read_b128 v[222:225], v132
	ds_read_b128 v[226:229], v132 offset:1024
	ds_read_b128 v[230:233], v132 offset:2048
	ds_read_b128 v[234:237], v132 offset:3072
	global_load_lds_dwordx4 v[238:239], off
	v_lshl_add_u64 v[240:241], s[24:25], 0, v[130:131]
	s_mov_b32 m0, s57
	s_nop 0
	global_load_lds_dwordx4 v[240:241], off
	s_barrier
	s_setprio 1
	s_waitcnt lgkmcnt(3)
	v_mfma_f32_16x16x32_bf16 v[116:119], v[222:225], v[190:193], v[116:119]
	s_waitcnt lgkmcnt(1)
	v_mfma_f32_16x16x32_bf16 v[112:115], v[230:233], v[190:193], v[112:115]
	v_mfma_f32_16x16x32_bf16 v[100:103], v[222:225], v[198:201], v[100:103]
	v_mfma_f32_16x16x32_bf16 v[96:99], v[230:233], v[198:201], v[96:99]
	v_mfma_f32_16x16x32_bf16 v[84:87], v[222:225], v[206:209], v[84:87]
	v_mfma_f32_16x16x32_bf16 v[80:83], v[230:233], v[206:209], v[80:83]
	v_mfma_f32_16x16x32_bf16 v[68:71], v[222:225], v[214:217], v[68:71]
	v_mfma_f32_16x16x32_bf16 v[64:67], v[230:233], v[214:217], v[64:67]
	v_mfma_f32_16x16x32_bf16 v[116:119], v[226:229], v[194:197], v[116:119]
	s_waitcnt lgkmcnt(0)
	v_mfma_f32_16x16x32_bf16 v[112:115], v[234:237], v[194:197], v[112:115]
	v_mfma_f32_16x16x32_bf16 v[100:103], v[226:229], v[202:205], v[100:103]
	v_mfma_f32_16x16x32_bf16 v[96:99], v[234:237], v[202:205], v[96:99]
	v_mfma_f32_16x16x32_bf16 v[84:87], v[226:229], v[210:213], v[84:87]
	v_mfma_f32_16x16x32_bf16 v[80:83], v[234:237], v[210:213], v[80:83]
	v_mfma_f32_16x16x32_bf16 v[68:71], v[226:229], v[218:221], v[68:71]
	v_mfma_f32_16x16x32_bf16 v[64:67], v[234:237], v[218:221], v[64:67]
	s_setprio 0
	s_add_u32 s0, s2, s73
	s_mov_b32 m0, s21
	s_addc_u32 s1, s3, 0
	v_cndmask_b32_e32 v132, v173, v169, vcc
	s_barrier
	ds_read_b128 v[190:193], v167 offset:16384
	ds_read_b128 v[194:197], v167 offset:17408
	ds_read_b128 v[198:201], v167 offset:18432
	ds_read_b128 v[202:205], v167 offset:19456
	ds_read_b128 v[206:209], v167 offset:20480
	ds_read_b128 v[210:213], v167 offset:21504
	ds_read_b128 v[214:217], v167 offset:22528
	ds_read_b128 v[218:221], v167 offset:23552
	v_cndmask_b32_e32 v242, v136, v171, vcc
	global_load_lds_dwordx4 v132, s[0:1]
	s_mov_b32 m0, s29
	v_mov_b32_e32 v243, v133
	global_load_lds_dwordx4 v242, s[0:1]
	s_barrier
	v_lshl_add_u64 v[244:245], s[0:1], 0, v[132:133]
	v_lshl_add_u64 v[242:243], s[0:1], 0, v[242:243]
	s_setprio 1
	s_waitcnt lgkmcnt(7)
	v_mfma_f32_16x16x32_bf16 v[52:55], v[174:177], v[190:193], v[52:55]
	v_mfma_f32_16x16x32_bf16 v[36:39], v[182:185], v[190:193], v[36:39]
	s_waitcnt lgkmcnt(5)
	v_mfma_f32_16x16x32_bf16 v[40:43], v[174:177], v[198:201], v[40:43]
	v_mfma_f32_16x16x32_bf16 v[32:35], v[182:185], v[198:201], v[32:35]
	s_waitcnt lgkmcnt(3)
	v_mfma_f32_16x16x32_bf16 v[20:23], v[174:177], v[206:209], v[20:23]
	v_mfma_f32_16x16x32_bf16 v[16:19], v[182:185], v[206:209], v[16:19]
	s_waitcnt lgkmcnt(1)
	v_mfma_f32_16x16x32_bf16 v[4:7], v[174:177], v[214:217], v[4:7]
	v_mfma_f32_16x16x32_bf16 v[0:3], v[182:185], v[214:217], v[0:3]
	v_mfma_f32_16x16x32_bf16 v[52:55], v[178:181], v[194:197], v[52:55]
	v_mfma_f32_16x16x32_bf16 v[36:39], v[186:189], v[194:197], v[36:39]
	v_mfma_f32_16x16x32_bf16 v[40:43], v[178:181], v[202:205], v[40:43]
	v_mfma_f32_16x16x32_bf16 v[32:35], v[186:189], v[202:205], v[32:35]
	v_mfma_f32_16x16x32_bf16 v[20:23], v[178:181], v[210:213], v[20:23]
	v_mfma_f32_16x16x32_bf16 v[16:19], v[186:189], v[210:213], v[16:19]
	s_waitcnt lgkmcnt(0)
	v_mfma_f32_16x16x32_bf16 v[4:7], v[178:181], v[218:221], v[4:7]
	v_mfma_f32_16x16x32_bf16 v[0:3], v[186:189], v[218:221], v[0:3]
	s_setprio 0
	s_barrier
; #define PG8_STAGE(bufoff, gbase, voff) do { _Pragma("unroll") for (int _i = 0; _i < 2; ++_i) \
;         __builtin_amdgcn_global_load_lds((const unsigned*)((const char*)(gbase) + (voff)[_i]), (LAS unsigned*)(lds + (bufoff) + ldsw + _i * 8192), 16, 0, 0); } while (0)
; #define PG8_LDA(dst, b, h) do { _Pragma("unroll") for (int m = 0; m < 4; ++m) _Pragma("unroll") for (int k = 0; k < 2; ++k) dst[m][k] = *(const LAS bf16x8*)(lds + PG8_SA(b, h) + aoff + m * 2048 + k * 1024); } while (0)
; #define PG8_LDB(dst, b, h) do { _Pragma("unroll") for (int n = 0; n < 2; ++n) _Pragma("unroll") for (int k = 0; k < 2; ++k) dst[n][k] = *(const LAS bf16x8*)(lds + PG8_SB(b, h) + boff + n * 2048 + k * 1024); } while (0)
; #define PG8_MMA(ai, bj, At, Bt) do { __builtin_amdgcn_s_setprio(1); _Pragma("unroll") for (int m = 0; m < 4; ++m) _Pragma("unroll") for (int n = 0; n < 2; ++n) _Pragma("unroll") for (int k = 0; k < 2; ++k) \
;         acc[ai][bj][m][n] = __builtin_amdgcn_mfma_f32_16x16x32_bf16(Bt[n][k], At[m][k], acc[ai][bj][m][n], 0, 0, 0); __builtin_amdgcn_s_setprio(0); } while (0)
; #define PG8_WAIT_V(n) asm volatile("s_waitcnt vmcnt(" #n ")" ::: "memory")
; #define PG8_WAIT_L(n) asm volatile("s_waitcnt lgkmcnt(" #n ")" ::: "memory")
; #define PG8_BAR __builtin_amdgcn_s_barrier()
; #define PG8_SCHED __builtin_amdgcn_sched_barrier(0)
; template <class Epi, class Sched>
; __device__ __forceinline__ void gemm_phase(LAS unsigned char* lds, const bf16_t* A, const int K, const Sched& S, const Epi& E, const int wv) {
;     ...
;             PG8_STAGE(PG8_SB(0, 1), b2 + hstep, voffB);
;             PG8_WAIT_V(6); PG8_BAR; PG8_MMA(1, 1, At, B1); PG8_BAR;
;             PG8_LDB(B0, 1, 0); PG8_SCHED; PG8_LDA(At, 1, 0); PG8_STAGE_A(PG8_SA(0, 1), 1, last, k2);
;             PG8_WAIT_L(8); PG8_BAR; PG8_WAIT_L(0); PG8_MMA(0, 0, At, B0); PG8_BAR; PG8_SCHED;
;             PG8_LDB(B1, 1, 1); PG8_STAGE(PG8_SB(1, 0), b3, voffB);
	s_add_u32 s72, s24, 0x80000
	s_addc_u32 s73, s25, 0
	s_mov_b32 m0, s60
	v_lshl_add_u64 v[174:175], s[72:73], 0, v[128:129]
	global_load_lds_dwordx4 v[174:175], off
	v_lshl_add_u64 v[174:175], s[72:73], 0, v[130:131]
	s_mov_b32 m0, s61
	s_nop 0
	global_load_lds_dwordx4 v[174:175], off
	s_waitcnt vmcnt(6)
	s_barrier
	s_setprio 1
	v_mfma_f32_16x16x32_bf16 v[60:63], v[222:225], v[190:193], v[60:63]
	v_mfma_f32_16x16x32_bf16 v[56:59], v[230:233], v[190:193], v[56:59]
	v_mfma_f32_16x16x32_bf16 v[48:51], v[222:225], v[198:201], v[48:51]
	v_mfma_f32_16x16x32_bf16 v[44:47], v[230:233], v[198:201], v[44:47]
	v_mfma_f32_16x16x32_bf16 v[28:31], v[222:225], v[206:209], v[28:31]
	v_mfma_f32_16x16x32_bf16 v[24:27], v[230:233], v[206:209], v[24:27]
	v_mfma_f32_16x16x32_bf16 v[12:15], v[222:225], v[214:217], v[12:15]
	v_mfma_f32_16x16x32_bf16 v[8:11], v[230:233], v[214:217], v[8:11]
	v_mfma_f32_16x16x32_bf16 v[60:63], v[226:229], v[194:197], v[60:63]
	v_mfma_f32_16x16x32_bf16 v[56:59], v[234:237], v[194:197], v[56:59]
	v_mfma_f32_16x16x32_bf16 v[48:51], v[226:229], v[202:205], v[48:51]
	v_mfma_f32_16x16x32_bf16 v[44:47], v[234:237], v[202:205], v[44:47]
	v_mfma_f32_16x16x32_bf16 v[28:31], v[226:229], v[210:213], v[28:31]
	v_mfma_f32_16x16x32_bf16 v[24:27], v[234:237], v[210:213], v[24:27]
	v_mfma_f32_16x16x32_bf16 v[12:15], v[226:229], v[218:221], v[12:15]
	v_mfma_f32_16x16x32_bf16 v[8:11], v[234:237], v[218:221], v[8:11]
	s_setprio 0
	v_add_u32_e32 v132, s62, v149
	s_barrier
	ds_read_b128 v[174:177], v132
	ds_read_b128 v[178:181], v132 offset:1024
	ds_read_b128 v[182:185], v132 offset:2048
	ds_read_b128 v[186:189], v132 offset:3072
	s_mov_b32 m0, s30
	v_cndmask_b32_e32 v132, v134, v170, vcc
	ds_read_b128 v[190:193], v167 offset:32768
	ds_read_b128 v[194:197], v167 offset:33792
	ds_read_b128 v[198:201], v167 offset:34816
	ds_read_b128 v[202:205], v167 offset:35840
	ds_read_b128 v[206:209], v167 offset:36864
	ds_read_b128 v[210:213], v167 offset:37888
	ds_read_b128 v[214:217], v167 offset:38912
	ds_read_b128 v[218:221], v167 offset:39936
	v_cndmask_b32_e32 v135, v138, v172, vcc
	global_load_lds_dwordx4 v132, s[0:1]
	s_mov_b32 m0, s31
	s_nop 0
	global_load_lds_dwordx4 v135, s[0:1]
	s_waitcnt lgkmcnt(8)
	s_barrier
	s_setprio 1
	s_waitcnt lgkmcnt(7)
	v_mfma_f32_16x16x32_bf16 v[124:127], v[174:177], v[190:193], v[124:127]
	v_mfma_f32_16x16x32_bf16 v[120:123], v[182:185], v[190:193], v[120:123]
	s_waitcnt lgkmcnt(5)
	v_mfma_f32_16x16x32_bf16 v[108:111], v[174:177], v[198:201], v[108:111]
	v_mfma_f32_16x16x32_bf16 v[104:107], v[182:185], v[198:201], v[104:107]
	s_waitcnt lgkmcnt(3)
	v_mfma_f32_16x16x32_bf16 v[92:95], v[174:177], v[206:209], v[92:95]
	v_mfma_f32_16x16x32_bf16 v[88:91], v[182:185], v[206:209], v[88:91]
	s_waitcnt lgkmcnt(1)
	v_mfma_f32_16x16x32_bf16 v[76:79], v[174:177], v[214:217], v[76:79]
	v_mfma_f32_16x16x32_bf16 v[72:75], v[182:185], v[214:217], v[72:75]
	v_mfma_f32_16x16x32_bf16 v[124:127], v[178:181], v[194:197], v[124:127]
	v_mfma_f32_16x16x32_bf16 v[120:123], v[186:189], v[194:197], v[120:123]
	v_mfma_f32_16x16x32_bf16 v[108:111], v[178:181], v[202:205], v[108:111]
	v_mfma_f32_16x16x32_bf16 v[104:107], v[186:189], v[202:205], v[104:107]
	v_mfma_f32_16x16x32_bf16 v[92:95], v[178:181], v[210:213], v[92:95]
	v_mfma_f32_16x16x32_bf16 v[88:91], v[186:189], v[210:213], v[88:91]
	s_waitcnt lgkmcnt(0)
	v_mfma_f32_16x16x32_bf16 v[76:79], v[178:181], v[218:221], v[76:79]
	v_mfma_f32_16x16x32_bf16 v[72:75], v[186:189], v[218:221], v[72:75]
	s_setprio 0
	s_barrier
	s_mov_b32 m0, s64
	v_add_u32_e32 v132, s63, v149
	v_lshl_add_u64 v[238:239], v[238:239], 0, s[8:9]
	ds_read_b128 v[222:225], v132
	ds_read_b128 v[226:229], v132 offset:1024
	ds_read_b128 v[230:233], v132 offset:2048
	ds_read_b128 v[234:237], v132 offset:3072
	global_load_lds_dwordx4 v[238:239], off
	v_lshl_add_u64 v[238:239], v[240:241], 0, s[8:9]
	s_mov_b32 m0, s65
	s_nop 0
	global_load_lds_dwordx4 v[238:239], off
	s_barrier
; #define PG8_STAGE(bufoff, gbase, voff) do { _Pragma("unroll") for (int _i = 0; _i < 2; ++_i) \
;         __builtin_amdgcn_global_load_lds((const unsigned*)((const char*)(gbase) + (voff)[_i]), (LAS unsigned*)(lds + (bufoff) + ldsw + _i * 8192), 16, 0, 0); } while (0)
; #define PG8_LDA(dst, b, h) do { _Pragma("unroll") for (int m = 0; m < 4; ++m) _Pragma("unroll") for (int k = 0; k < 2; ++k) dst[m][k] = *(const LAS bf16x8*)(lds + PG8_SA(b, h) + aoff + m * 2048 + k * 1024); } while (0)
; #define PG8_LDB(dst, b, h) do { _Pragma("unroll") for (int n = 0; n < 2; ++n) _Pragma("unroll") for (int k = 0; k < 2; ++k) dst[n][k] = *(const LAS bf16x8*)(lds + PG8_SB(b, h) + boff + n * 2048 + k * 1024); } while (0)
; #define PG8_MMA(ai, bj, At, Bt) do { __builtin_amdgcn_s_setprio(1); _Pragma("unroll") for (int m = 0; m < 4; ++m) _Pragma("unroll") for (int n = 0; n < 2; ++n) _Pragma("unroll") for (int k = 0; k < 2; ++k) \
;         acc[ai][bj][m][n] = __builtin_amdgcn_mfma_f32_16x16x32_bf16(Bt[n][k], At[m][k], acc[ai][bj][m][n], 0, 0, 0); __builtin_amdgcn_s_setprio(0); } while (0)
; #define PG8_WAIT_V(n) asm volatile("s_waitcnt vmcnt(" #n ")" ::: "memory")
; #define PG8_WAIT_L(n) asm volatile("s_waitcnt lgkmcnt(" #n ")" ::: "memory")
; #define PG8_BAR __builtin_amdgcn_s_barrier()
; #define PG8_SCHED __builtin_amdgcn_sched_barrier(0)
; template <class Epi, class Sched>
; __device__ __forceinline__ void gemm_phase(LAS unsigned char* lds, const bf16_t* A, const int K, const Sched& S, const Epi& E, const int wv) {
;     ...
;             PG8_LDB(B1, 1, 1); PG8_STAGE(PG8_SB(1, 0), b3, voffB);
;             PG8_BAR; PG8_WAIT_L(0); PG8_MMA(0, 1, At, B1); PG8_BAR;
;             PG8_LDA(At, 1, 1); PG8_STAGE_A(PG8_SA(1, 0), 0, last, k3);
;             PG8_BAR; PG8_WAIT_L(0); PG8_MMA(1, 0, At, B0); PG8_BAR; PG8_SCHED;
;             PG8_STAGE(PG8_SB(1, 1), b3 + hstep, voffB);
;             PG8_WAIT_V(6); PG8_BAR; PG8_MMA(1, 1, At, B1); PG8_BAR;
;         }
	s_setprio 1
	s_waitcnt lgkmcnt(3)
	v_mfma_f32_16x16x32_bf16 v[116:119], v[222:225], v[190:193], v[116:119]
	s_waitcnt lgkmcnt(1)
	v_mfma_f32_16x16x32_bf16 v[112:115], v[230:233], v[190:193], v[112:115]
	v_mfma_f32_16x16x32_bf16 v[100:103], v[222:225], v[198:201], v[100:103]
	v_mfma_f32_16x16x32_bf16 v[96:99], v[230:233], v[198:201], v[96:99]
	v_mfma_f32_16x16x32_bf16 v[84:87], v[222:225], v[206:209], v[84:87]
	v_mfma_f32_16x16x32_bf16 v[80:83], v[230:233], v[206:209], v[80:83]
	v_mfma_f32_16x16x32_bf16 v[68:71], v[222:225], v[214:217], v[68:71]
	v_mfma_f32_16x16x32_bf16 v[64:67], v[230:233], v[214:217], v[64:67]
	v_mfma_f32_16x16x32_bf16 v[116:119], v[226:229], v[194:197], v[116:119]
	s_waitcnt lgkmcnt(0)
	v_mfma_f32_16x16x32_bf16 v[112:115], v[234:237], v[194:197], v[112:115]
	v_mfma_f32_16x16x32_bf16 v[100:103], v[226:229], v[202:205], v[100:103]
	v_mfma_f32_16x16x32_bf16 v[96:99], v[234:237], v[202:205], v[96:99]
	v_mfma_f32_16x16x32_bf16 v[84:87], v[226:229], v[210:213], v[84:87]
	v_mfma_f32_16x16x32_bf16 v[80:83], v[234:237], v[210:213], v[80:83]
	v_mfma_f32_16x16x32_bf16 v[68:71], v[226:229], v[218:221], v[68:71]
	v_mfma_f32_16x16x32_bf16 v[64:67], v[234:237], v[218:221], v[64:67]
	s_setprio 0
	s_mov_b32 m0, s33
	v_lshl_add_u64 v[238:239], v[244:245], 0, s[8:9]
	s_barrier
	ds_read_b128 v[190:193], v167 offset:49152
	ds_read_b128 v[194:197], v167 offset:50176
	ds_read_b128 v[198:201], v167 offset:51200
	ds_read_b128 v[202:205], v167 offset:52224
	ds_read_b128 v[206:209], v167 offset:53248
	ds_read_b128 v[210:213], v167 offset:54272
	ds_read_b128 v[214:217], v167 offset:55296
	ds_read_b128 v[218:221], v167 offset:56320
	global_load_lds_dwordx4 v[238:239], off
	v_lshl_add_u64 v[238:239], v[242:243], 0, s[8:9]
	s_mov_b32 m0, s34
	s_nop 0
	global_load_lds_dwordx4 v[238:239], off
	s_barrier
	s_setprio 1
	s_waitcnt lgkmcnt(7)
	v_mfma_f32_16x16x32_bf16 v[52:55], v[174:177], v[190:193], v[52:55]
	v_mfma_f32_16x16x32_bf16 v[36:39], v[182:185], v[190:193], v[36:39]
	s_waitcnt lgkmcnt(5)
	v_mfma_f32_16x16x32_bf16 v[40:43], v[174:177], v[198:201], v[40:43]
	v_mfma_f32_16x16x32_bf16 v[32:35], v[182:185], v[198:201], v[32:35]
	s_waitcnt lgkmcnt(3)
	v_mfma_f32_16x16x32_bf16 v[20:23], v[174:177], v[206:209], v[20:23]
	v_mfma_f32_16x16x32_bf16 v[16:19], v[182:185], v[206:209], v[16:19]
	s_waitcnt lgkmcnt(1)
	v_mfma_f32_16x16x32_bf16 v[4:7], v[174:177], v[214:217], v[4:7]
	v_mfma_f32_16x16x32_bf16 v[0:3], v[182:185], v[214:217], v[0:3]
	v_mfma_f32_16x16x32_bf16 v[52:55], v[178:181], v[194:197], v[52:55]
	v_mfma_f32_16x16x32_bf16 v[36:39], v[186:189], v[194:197], v[36:39]
	v_mfma_f32_16x16x32_bf16 v[40:43], v[178:181], v[202:205], v[40:43]
	v_mfma_f32_16x16x32_bf16 v[32:35], v[186:189], v[202:205], v[32:35]
	v_mfma_f32_16x16x32_bf16 v[20:23], v[178:181], v[210:213], v[20:23]
	v_mfma_f32_16x16x32_bf16 v[16:19], v[186:189], v[210:213], v[16:19]
	s_waitcnt lgkmcnt(0)
	v_mfma_f32_16x16x32_bf16 v[4:7], v[178:181], v[218:221], v[4:7]
	v_mfma_f32_16x16x32_bf16 v[0:3], v[186:189], v[218:221], v[0:3]
	s_setprio 0
	s_barrier
	s_add_u32 s0, s24, 0x80080
	s_addc_u32 s1, s25, 0
	s_mov_b32 m0, s66
	v_lshl_add_u64 v[174:175], s[0:1], 0, v[128:129]
	global_load_lds_dwordx4 v[174:175], off
	v_lshl_add_u64 v[174:175], s[0:1], 0, v[130:131]
	s_mov_b32 m0, s67
	s_nop 0
	global_load_lds_dwordx4 v[174:175], off
	s_waitcnt vmcnt(6)
	s_barrier
	s_setprio 1
	v_mfma_f32_16x16x32_bf16 v[60:63], v[222:225], v[190:193], v[60:63]
	v_mfma_f32_16x16x32_bf16 v[56:59], v[230:233], v[190:193], v[56:59]
	v_mfma_f32_16x16x32_bf16 v[48:51], v[222:225], v[198:201], v[48:51]
	v_mfma_f32_16x16x32_bf16 v[44:47], v[230:233], v[198:201], v[44:47]
	v_mfma_f32_16x16x32_bf16 v[28:31], v[222:225], v[206:209], v[28:31]
	v_mfma_f32_16x16x32_bf16 v[24:27], v[230:233], v[206:209], v[24:27]
	v_mfma_f32_16x16x32_bf16 v[12:15], v[222:225], v[214:217], v[12:15]
	v_mfma_f32_16x16x32_bf16 v[8:11], v[230:233], v[214:217], v[8:11]
	v_mfma_f32_16x16x32_bf16 v[60:63], v[226:229], v[194:197], v[60:63]
	v_mfma_f32_16x16x32_bf16 v[56:59], v[234:237], v[194:197], v[56:59]
	v_mfma_f32_16x16x32_bf16 v[48:51], v[226:229], v[202:205], v[48:51]
	v_mfma_f32_16x16x32_bf16 v[44:47], v[234:237], v[202:205], v[44:47]
	v_mfma_f32_16x16x32_bf16 v[28:31], v[226:229], v[210:213], v[28:31]
	v_mfma_f32_16x16x32_bf16 v[24:27], v[234:237], v[210:213], v[24:27]
	v_mfma_f32_16x16x32_bf16 v[12:15], v[226:229], v[218:221], v[12:15]
	v_mfma_f32_16x16x32_bf16 v[8:11], v[234:237], v[218:221], v[8:11]
	s_setprio 0
	s_add_i32 s70, s70, 2
	s_cmp_gt_u32 s70, 29
	s_mov_b64 s[0:1], s[22:23]
	s_cbranch_scc1 .Lmy_kx_6
	s_barrier
	s_branch .LBB0_2080

; #define PG8_STAGE(bufoff, gbase, voff) do { _Pragma("unroll") for (int _i = 0; _i < 2; ++_i) \
;         __builtin_amdgcn_global_load_lds((const unsigned*)((const char*)(gbase) + (voff)[_i]), (LAS unsigned*)(lds + (bufoff) + ldsw + _i * 8192), 16, 0, 0); } while (0)
; #define PG8_LDA(dst, b, h) do { _Pragma("unroll") for (int m = 0; m < 4; ++m) _Pragma("unroll") for (int k = 0; k < 2; ++k) dst[m][k] = *(const LAS bf16x8*)(lds + PG8_SA(b, h) + aoff + m * 2048 + k * 1024); } while (0)
; #define PG8_LDB(dst, b, h) do { _Pragma("unroll") for (int n = 0; n < 2; ++n) _Pragma("unroll") for (int k = 0; k < 2; ++k) dst[n][k] = *(const LAS bf16x8*)(lds + PG8_SB(b, h) + boff + n * 2048 + k * 1024); } while (0)
; #define PG8_MMA(ai, bj, At, Bt) do { __builtin_amdgcn_s_setprio(1); _Pragma("unroll") for (int m = 0; m < 4; ++m) _Pragma("unroll") for (int n = 0; n < 2; ++n) _Pragma("unroll") for (int k = 0; k < 2; ++k) \
;         acc[ai][bj][m][n] = __builtin_amdgcn_mfma_f32_16x16x32_bf16(Bt[n][k], At[m][k], acc[ai][bj][m][n], 0, 0, 0); __builtin_amdgcn_s_setprio(0); } while (0)
; #define PG8_WAIT_L(n) asm volatile("s_waitcnt lgkmcnt(" #n ")" ::: "memory")
; #define PG8_BAR __builtin_amdgcn_s_barrier()
; #define PG8_SCHED __builtin_amdgcn_sched_barrier(0)
; template <class Epi, class Sched>
; __device__ __forceinline__ void gemm_phase(LAS unsigned char* lds, const bf16_t* A, const int K, const Sched& S, const Epi& E, const int wv) {
;     ...
;         for (int t = 0; t < nt; t += 2) {
;             const bool last = (t == nt - 2);
;             const size_t k1 = (size_t)(t + 1) * kstep;
;             const size_t k2 = last ? 0 : (size_t)(t + 2) * kstep, k3 = k2 + kstep;
;             const char* b2 = last ? nB : cB + (size_t)(t + 2) * kstep; const char* b3 = b2 + kstep;
;             PG8_LDB(B0, 0, 0); PG8_SCHED; PG8_LDA(At, 0, 0); PG8_STAGE_A(PG8_SA(1, 1), 1, false, k1);
;             PG8_WAIT_L(8); PG8_BAR; PG8_WAIT_L(0); PG8_MMA(0, 0, At, B0); PG8_BAR; PG8_SCHED;
;             PG8_LDB(B1, 0, 1); PG8_STAGE(PG8_SB(0, 0), b2, voffB);
;             PG8_BAR; PG8_WAIT_L(0); PG8_MMA(0, 1, At, B1); PG8_BAR;
;             PG8_LDA(At, 0, 1); PG8_STAGE_A(PG8_SA(0, 0), 0, last, k2);
;             PG8_BAR; PG8_WAIT_L(0); PG8_MMA(1, 0, At, B0); PG8_BAR; PG8_SCHED;
.Lmy_ph_7:
.LBB0_2221:
	v_add_u32_e32 v132, s52, v150
	s_add_u32 s22, s0, 0x100
	ds_read_b128 v[174:177], v132
	ds_read_b128 v[178:181], v132 offset:1024
	ds_read_b128 v[182:185], v132 offset:2048
	ds_read_b128 v[186:189], v132 offset:3072
	s_addc_u32 s23, s1, 0
	s_add_u32 s69, s17, s0
	s_addc_u32 s70, s19, s1
	s_cmpk_eq_i32 s0, 0x700
	s_cselect_b64 vcc, -1, 0
	s_and_b64 s[24:25], vcc, exec
	s_cselect_b32 s71, 0, s22
	s_cselect_b32 s25, s21, s70
	s_cselect_b32 s24, s20, s69
	s_mov_b32 m0, s54
	v_lshl_add_u64 v[222:223], v[142:143], 0, s[0:1]
	ds_read_b128 v[190:193], v168
	ds_read_b128 v[194:197], v168 offset:1024
	ds_read_b128 v[198:201], v168 offset:2048
	ds_read_b128 v[202:205], v168 offset:3072
	ds_read_b128 v[206:209], v168 offset:4096
	ds_read_b128 v[210:213], v168 offset:5120
	ds_read_b128 v[214:217], v168 offset:6144
	ds_read_b128 v[218:221], v168 offset:7168
	global_load_lds_dwordx4 v[222:223], off
	v_lshl_add_u64 v[222:223], v[140:141], 0, s[0:1]
	s_mov_b32 m0, s55
	s_nop 0
	global_load_lds_dwordx4 v[222:223], off
	s_waitcnt lgkmcnt(8)
	s_barrier
	s_setprio 1
	s_waitcnt lgkmcnt(7)
	v_mfma_f32_16x16x32_bf16 v[124:127], v[174:177], v[190:193], v[124:127]
	v_mfma_f32_16x16x32_bf16 v[120:123], v[182:185], v[190:193], v[120:123]
	s_waitcnt lgkmcnt(5)
	v_mfma_f32_16x16x32_bf16 v[116:119], v[174:177], v[198:201], v[116:119]
	v_mfma_f32_16x16x32_bf16 v[108:111], v[182:185], v[198:201], v[108:111]
	s_waitcnt lgkmcnt(3)
	v_mfma_f32_16x16x32_bf16 v[100:103], v[174:177], v[206:209], v[100:103]
	v_mfma_f32_16x16x32_bf16 v[92:95], v[182:185], v[206:209], v[92:95]
	s_waitcnt lgkmcnt(1)
	v_mfma_f32_16x16x32_bf16 v[84:87], v[174:177], v[214:217], v[84:87]
	v_mfma_f32_16x16x32_bf16 v[76:79], v[182:185], v[214:217], v[76:79]
	v_mfma_f32_16x16x32_bf16 v[124:127], v[178:181], v[194:197], v[124:127]
	v_mfma_f32_16x16x32_bf16 v[120:123], v[186:189], v[194:197], v[120:123]
	v_mfma_f32_16x16x32_bf16 v[116:119], v[178:181], v[202:205], v[116:119]
	v_mfma_f32_16x16x32_bf16 v[108:111], v[186:189], v[202:205], v[108:111]
	v_mfma_f32_16x16x32_bf16 v[100:103], v[178:181], v[210:213], v[100:103]
	v_mfma_f32_16x16x32_bf16 v[92:95], v[186:189], v[210:213], v[92:95]
	s_waitcnt lgkmcnt(0)
	v_mfma_f32_16x16x32_bf16 v[84:87], v[178:181], v[218:221], v[84:87]
	v_mfma_f32_16x16x32_bf16 v[76:79], v[186:189], v[218:221], v[76:79]
	s_setprio 0
	s_barrier
	s_mov_b32 m0, s56
	v_add_u32_e32 v132, s53, v150
	v_lshl_add_u64 v[238:239], s[24:25], 0, v[128:129]
	ds_read_b128 v[222:225], v132
	ds_read_b128 v[226:229], v132 offset:1024
	ds_read_b128 v[230:233], v132 offset:2048
	ds_read_b128 v[234:237], v132 offset:3072
	global_load_lds_dwordx4 v[238:239], off
	v_lshl_add_u64 v[240:241], s[24:25], 0, v[130:131]
	s_mov_b32 m0, s57
	s_nop 0
	global_load_lds_dwordx4 v[240:241], off
	s_barrier
	s_setprio 1
	s_waitcnt lgkmcnt(3)
	v_mfma_f32_16x16x32_bf16 v[112:115], v[222:225], v[190:193], v[112:115]
	s_waitcnt lgkmcnt(1)
	v_mfma_f32_16x16x32_bf16 v[104:107], v[230:233], v[190:193], v[104:107]
	v_mfma_f32_16x16x32_bf16 v[96:99], v[222:225], v[198:201], v[96:99]
	v_mfma_f32_16x16x32_bf16 v[88:91], v[230:233], v[198:201], v[88:91]
	v_mfma_f32_16x16x32_bf16 v[80:83], v[222:225], v[206:209], v[80:83]
	v_mfma_f32_16x16x32_bf16 v[72:75], v[230:233], v[206:209], v[72:75]
	v_mfma_f32_16x16x32_bf16 v[52:55], v[222:225], v[214:217], v[52:55]
	v_mfma_f32_16x16x32_bf16 v[48:51], v[230:233], v[214:217], v[48:51]
	v_mfma_f32_16x16x32_bf16 v[112:115], v[226:229], v[194:197], v[112:115]
	s_waitcnt lgkmcnt(0)
	v_mfma_f32_16x16x32_bf16 v[104:107], v[234:237], v[194:197], v[104:107]
	v_mfma_f32_16x16x32_bf16 v[96:99], v[226:229], v[202:205], v[96:99]
	v_mfma_f32_16x16x32_bf16 v[88:91], v[234:237], v[202:205], v[88:91]
	v_mfma_f32_16x16x32_bf16 v[80:83], v[226:229], v[210:213], v[80:83]
	v_mfma_f32_16x16x32_bf16 v[72:75], v[234:237], v[210:213], v[72:75]
	v_mfma_f32_16x16x32_bf16 v[52:55], v[226:229], v[218:221], v[52:55]
	v_mfma_f32_16x16x32_bf16 v[48:51], v[234:237], v[218:221], v[48:51]
	s_setprio 0
	s_add_u32 s0, s2, s71
	s_mov_b32 m0, s13
	s_addc_u32 s1, s3, 0
	v_cndmask_b32_e32 v132, v135, v170, vcc
	s_barrier
	ds_read_b128 v[190:193], v168 offset:16384
	ds_read_b128 v[194:197], v168 offset:17408
	ds_read_b128 v[198:201], v168 offset:18432
	ds_read_b128 v[202:205], v168 offset:19456
	ds_read_b128 v[206:209], v168 offset:20480
	ds_read_b128 v[210:213], v168 offset:21504
	ds_read_b128 v[214:217], v168 offset:22528
	ds_read_b128 v[218:221], v168 offset:23552
	v_cndmask_b32_e32 v242, v134, v172, vcc
	global_load_lds_dwordx4 v132, s[0:1]
	s_mov_b32 m0, s29
	v_mov_b32_e32 v243, v133
	global_load_lds_dwordx4 v242, s[0:1]
	s_barrier
	v_lshl_add_u64 v[244:245], s[0:1], 0, v[132:133]
	v_lshl_add_u64 v[242:243], s[0:1], 0, v[242:243]
	s_setprio 1
	s_waitcnt lgkmcnt(7)
	v_mfma_f32_16x16x32_bf16 v[20:23], v[174:177], v[190:193], v[20:23]
	v_mfma_f32_16x16x32_bf16 v[8:11], v[182:185], v[190:193], v[8:11]
	s_waitcnt lgkmcnt(5)
	v_mfma_f32_16x16x32_bf16 v[40:43], v[174:177], v[198:201], v[40:43]
	v_mfma_f32_16x16x32_bf16 v[44:47], v[182:185], v[198:201], v[44:47]
	s_waitcnt lgkmcnt(3)
	v_mfma_f32_16x16x32_bf16 v[24:27], v[174:177], v[206:209], v[24:27]
	v_mfma_f32_16x16x32_bf16 v[28:31], v[182:185], v[206:209], v[28:31]
	s_waitcnt lgkmcnt(1)
	v_mfma_f32_16x16x32_bf16 v[0:3], v[174:177], v[214:217], v[0:3]
	v_mfma_f32_16x16x32_bf16 v[4:7], v[182:185], v[214:217], v[4:7]
	v_mfma_f32_16x16x32_bf16 v[20:23], v[178:181], v[194:197], v[20:23]
	v_mfma_f32_16x16x32_bf16 v[8:11], v[186:189], v[194:197], v[8:11]
	v_mfma_f32_16x16x32_bf16 v[40:43], v[178:181], v[202:205], v[40:43]
	v_mfma_f32_16x16x32_bf16 v[44:47], v[186:189], v[202:205], v[44:47]
	v_mfma_f32_16x16x32_bf16 v[24:27], v[178:181], v[210:213], v[24:27]
	v_mfma_f32_16x16x32_bf16 v[28:31], v[186:189], v[210:213], v[28:31]
	s_waitcnt lgkmcnt(0)
	v_mfma_f32_16x16x32_bf16 v[0:3], v[178:181], v[218:221], v[0:3]
	v_mfma_f32_16x16x32_bf16 v[4:7], v[186:189], v[218:221], v[4:7]
	s_setprio 0
	s_barrier
; #define PG8_STAGE(bufoff, gbase, voff) do { _Pragma("unroll") for (int _i = 0; _i < 2; ++_i) \
;         __builtin_amdgcn_global_load_lds((const unsigned*)((const char*)(gbase) + (voff)[_i]), (LAS unsigned*)(lds + (bufoff) + ldsw + _i * 8192), 16, 0, 0); } while (0)
; #define PG8_LDA(dst, b, h) do { _Pragma("unroll") for (int m = 0; m < 4; ++m) _Pragma("unroll") for (int k = 0; k < 2; ++k) dst[m][k] = *(const LAS bf16x8*)(lds + PG8_SA(b, h) + aoff + m * 2048 + k * 1024); } while (0)
; #define PG8_LDB(dst, b, h) do { _Pragma("unroll") for (int n = 0; n < 2; ++n) _Pragma("unroll") for (int k = 0; k < 2; ++k) dst[n][k] = *(const LAS bf16x8*)(lds + PG8_SB(b, h) + boff + n * 2048 + k * 1024); } while (0)
; #define PG8_MMA(ai, bj, At, Bt) do { __builtin_amdgcn_s_setprio(1); _Pragma("unroll") for (int m = 0; m < 4; ++m) _Pragma("unroll") for (int n = 0; n < 2; ++n) _Pragma("unroll") for (int k = 0; k < 2; ++k) \
;         acc[ai][bj][m][n] = __builtin_amdgcn_mfma_f32_16x16x32_bf16(Bt[n][k], At[m][k], acc[ai][bj][m][n], 0, 0, 0); __builtin_amdgcn_s_setprio(0); } while (0)
; #define PG8_WAIT_V(n) asm volatile("s_waitcnt vmcnt(" #n ")" ::: "memory")
; #define PG8_WAIT_L(n) asm volatile("s_waitcnt lgkmcnt(" #n ")" ::: "memory")
; #define PG8_BAR __builtin_amdgcn_s_barrier()
; #define PG8_SCHED __builtin_amdgcn_sched_barrier(0)
; template <class Epi, class Sched>
; __device__ __forceinline__ void gemm_phase(LAS unsigned char* lds, const bf16_t* A, const int K, const Sched& S, const Epi& E, const int wv) {
;     ...
;             PG8_STAGE(PG8_SB(0, 1), b2 + hstep, voffB);
;             PG8_WAIT_V(6); PG8_BAR; PG8_MMA(1, 1, At, B1); PG8_BAR;
;             PG8_LDB(B0, 1, 0); PG8_SCHED; PG8_LDA(At, 1, 0); PG8_STAGE_A(PG8_SA(0, 1), 1, last, k2);
;             PG8_WAIT_L(8); PG8_BAR; PG8_WAIT_L(0); PG8_MMA(0, 0, At, B0); PG8_BAR; PG8_SCHED;
;             PG8_LDB(B1, 1, 1); PG8_STAGE(PG8_SB(1, 0), b3, voffB);
	s_add_u32 s70, s24, 0x40000
	s_addc_u32 s71, s25, 0
	s_mov_b32 m0, s58
	v_lshl_add_u64 v[174:175], s[70:71], 0, v[128:129]
	global_load_lds_dwordx4 v[174:175], off
	v_lshl_add_u64 v[174:175], s[70:71], 0, v[130:131]
	s_mov_b32 m0, s59
	s_nop 0
	global_load_lds_dwordx4 v[174:175], off
	s_waitcnt vmcnt(6)
	s_barrier
	s_setprio 1
	v_mfma_f32_16x16x32_bf16 v[64:67], v[222:225], v[190:193], v[64:67]
	v_mfma_f32_16x16x32_bf16 v[68:71], v[230:233], v[190:193], v[68:71]
	v_mfma_f32_16x16x32_bf16 v[56:59], v[222:225], v[198:201], v[56:59]
	v_mfma_f32_16x16x32_bf16 v[60:63], v[230:233], v[198:201], v[60:63]
	v_mfma_f32_16x16x32_bf16 v[32:35], v[222:225], v[206:209], v[32:35]
	v_mfma_f32_16x16x32_bf16 v[36:39], v[230:233], v[206:209], v[36:39]
	v_mfma_f32_16x16x32_bf16 v[12:15], v[222:225], v[214:217], v[12:15]
	v_mfma_f32_16x16x32_bf16 v[16:19], v[230:233], v[214:217], v[16:19]
	v_mfma_f32_16x16x32_bf16 v[64:67], v[226:229], v[194:197], v[64:67]
	v_mfma_f32_16x16x32_bf16 v[68:71], v[234:237], v[194:197], v[68:71]
	v_mfma_f32_16x16x32_bf16 v[56:59], v[226:229], v[202:205], v[56:59]
	v_mfma_f32_16x16x32_bf16 v[60:63], v[234:237], v[202:205], v[60:63]
	v_mfma_f32_16x16x32_bf16 v[32:35], v[226:229], v[210:213], v[32:35]
	v_mfma_f32_16x16x32_bf16 v[36:39], v[234:237], v[210:213], v[36:39]
	v_mfma_f32_16x16x32_bf16 v[12:15], v[226:229], v[218:221], v[12:15]
	v_mfma_f32_16x16x32_bf16 v[16:19], v[234:237], v[218:221], v[16:19]
	s_setprio 0
	v_add_u32_e32 v132, s60, v150
	s_barrier
	ds_read_b128 v[174:177], v132
	ds_read_b128 v[178:181], v132 offset:1024
	ds_read_b128 v[182:185], v132 offset:2048
	ds_read_b128 v[186:189], v132 offset:3072
	s_mov_b32 m0, s30
	v_cndmask_b32_e32 v132, v136, v171, vcc
	ds_read_b128 v[190:193], v168 offset:32768
	ds_read_b128 v[194:197], v168 offset:33792
	ds_read_b128 v[198:201], v168 offset:34816
	ds_read_b128 v[202:205], v168 offset:35840
	ds_read_b128 v[206:209], v168 offset:36864
	ds_read_b128 v[210:213], v168 offset:37888
	ds_read_b128 v[214:217], v168 offset:38912
	ds_read_b128 v[218:221], v168 offset:39936
	v_cndmask_b32_e32 v137, v138, v173, vcc
	global_load_lds_dwordx4 v132, s[0:1]
	s_mov_b32 m0, s31
	s_nop 0
	global_load_lds_dwordx4 v137, s[0:1]
	s_waitcnt lgkmcnt(8)
	s_barrier
	s_setprio 1
	s_waitcnt lgkmcnt(7)
	v_mfma_f32_16x16x32_bf16 v[124:127], v[174:177], v[190:193], v[124:127]
	v_mfma_f32_16x16x32_bf16 v[120:123], v[182:185], v[190:193], v[120:123]
	s_waitcnt lgkmcnt(5)
	v_mfma_f32_16x16x32_bf16 v[116:119], v[174:177], v[198:201], v[116:119]
	v_mfma_f32_16x16x32_bf16 v[108:111], v[182:185], v[198:201], v[108:111]
	s_waitcnt lgkmcnt(3)
	v_mfma_f32_16x16x32_bf16 v[100:103], v[174:177], v[206:209], v[100:103]
	v_mfma_f32_16x16x32_bf16 v[92:95], v[182:185], v[206:209], v[92:95]
	s_waitcnt lgkmcnt(1)
	v_mfma_f32_16x16x32_bf16 v[84:87], v[174:177], v[214:217], v[84:87]
	v_mfma_f32_16x16x32_bf16 v[76:79], v[182:185], v[214:217], v[76:79]
	v_mfma_f32_16x16x32_bf16 v[124:127], v[178:181], v[194:197], v[124:127]
	v_mfma_f32_16x16x32_bf16 v[120:123], v[186:189], v[194:197], v[120:123]
	v_mfma_f32_16x16x32_bf16 v[116:119], v[178:181], v[202:205], v[116:119]
	v_mfma_f32_16x16x32_bf16 v[108:111], v[186:189], v[202:205], v[108:111]
	v_mfma_f32_16x16x32_bf16 v[100:103], v[178:181], v[210:213], v[100:103]
	v_mfma_f32_16x16x32_bf16 v[92:95], v[186:189], v[210:213], v[92:95]
	s_waitcnt lgkmcnt(0)
	v_mfma_f32_16x16x32_bf16 v[84:87], v[178:181], v[218:221], v[84:87]
	v_mfma_f32_16x16x32_bf16 v[76:79], v[186:189], v[218:221], v[76:79]
	s_setprio 0
	s_barrier
	s_mov_b32 m0, s62
	v_add_u32_e32 v132, s61, v150
	v_lshl_add_u64 v[238:239], v[238:239], 0, s[8:9]
	ds_read_b128 v[222:225], v132
	ds_read_b128 v[226:229], v132 offset:1024
	ds_read_b128 v[230:233], v132 offset:2048
	ds_read_b128 v[234:237], v132 offset:3072
	global_load_lds_dwordx4 v[238:239], off
	v_lshl_add_u64 v[238:239], v[240:241], 0, s[8:9]
	s_mov_b32 m0, s63
	s_nop 0
	global_load_lds_dwordx4 v[238:239], off
	s_barrier
; #define PG8_STAGE(bufoff, gbase, voff) do { _Pragma("unroll") for (int _i = 0; _i < 2; ++_i) \
;         __builtin_amdgcn_global_load_lds((const unsigned*)((const char*)(gbase) + (voff)[_i]), (LAS unsigned*)(lds + (bufoff) + ldsw + _i * 8192), 16, 0, 0); } while (0)
; #define PG8_LDA(dst, b, h) do { _Pragma("unroll") for (int m = 0; m < 4; ++m) _Pragma("unroll") for (int k = 0; k < 2; ++k) dst[m][k] = *(const LAS bf16x8*)(lds + PG8_SA(b, h) + aoff + m * 2048 + k * 1024); } while (0)
; #define PG8_LDB(dst, b, h) do { _Pragma("unroll") for (int n = 0; n < 2; ++n) _Pragma("unroll") for (int k = 0; k < 2; ++k) dst[n][k] = *(const LAS bf16x8*)(lds + PG8_SB(b, h) + boff + n * 2048 + k * 1024); } while (0)
; #define PG8_MMA(ai, bj, At, Bt) do { __builtin_amdgcn_s_setprio(1); _Pragma("unroll") for (int m = 0; m < 4; ++m) _Pragma("unroll") for (int n = 0; n < 2; ++n) _Pragma("unroll") for (int k = 0; k < 2; ++k) \
;         acc[ai][bj][m][n] = __builtin_amdgcn_mfma_f32_16x16x32_bf16(Bt[n][k], At[m][k], acc[ai][bj][m][n], 0, 0, 0); __builtin_amdgcn_s_setprio(0); } while (0)
; #define PG8_WAIT_V(n) asm volatile("s_waitcnt vmcnt(" #n ")" ::: "memory")
; #define PG8_WAIT_L(n) asm volatile("s_waitcnt lgkmcnt(" #n ")" ::: "memory")
; #define PG8_BAR __builtin_amdgcn_s_barrier()
; #define PG8_SCHED __builtin_amdgcn_sched_barrier(0)
; template <class Epi, class Sched>
; __device__ __forceinline__ void gemm_phase(LAS unsigned char* lds, const bf16_t* A, const int K, const Sched& S, const Epi& E, const int wv) {
;     ...
;             PG8_LDB(B1, 1, 1); PG8_STAGE(PG8_SB(1, 0), b3, voffB);
;             PG8_BAR; PG8_WAIT_L(0); PG8_MMA(0, 1, At, B1); PG8_BAR;
;             PG8_LDA(At, 1, 1); PG8_STAGE_A(PG8_SA(1, 0), 0, last, k3);
;             PG8_BAR; PG8_WAIT_L(0); PG8_MMA(1, 0, At, B0); PG8_BAR; PG8_SCHED;
;             PG8_STAGE(PG8_SB(1, 1), b3 + hstep, voffB);
;             PG8_WAIT_V(6); PG8_BAR; PG8_MMA(1, 1, At, B1); PG8_BAR;
;         }
	s_setprio 1
	s_waitcnt lgkmcnt(3)
	v_mfma_f32_16x16x32_bf16 v[112:115], v[222:225], v[190:193], v[112:115]
	s_waitcnt lgkmcnt(1)
	v_mfma_f32_16x16x32_bf16 v[104:107], v[230:233], v[190:193], v[104:107]
	v_mfma_f32_16x16x32_bf16 v[96:99], v[222:225], v[198:201], v[96:99]
	v_mfma_f32_16x16x32_bf16 v[88:91], v[230:233], v[198:201], v[88:91]
	v_mfma_f32_16x16x32_bf16 v[80:83], v[222:225], v[206:209], v[80:83]
	v_mfma_f32_16x16x32_bf16 v[72:75], v[230:233], v[206:209], v[72:75]
	v_mfma_f32_16x16x32_bf16 v[52:55], v[222:225], v[214:217], v[52:55]
	v_mfma_f32_16x16x32_bf16 v[48:51], v[230:233], v[214:217], v[48:51]
	v_mfma_f32_16x16x32_bf16 v[112:115], v[226:229], v[194:197], v[112:115]
	s_waitcnt lgkmcnt(0)
	v_mfma_f32_16x16x32_bf16 v[104:107], v[234:237], v[194:197], v[104:107]
	v_mfma_f32_16x16x32_bf16 v[96:99], v[226:229], v[202:205], v[96:99]
	v_mfma_f32_16x16x32_bf16 v[88:91], v[234:237], v[202:205], v[88:91]
	v_mfma_f32_16x16x32_bf16 v[80:83], v[226:229], v[210:213], v[80:83]
	v_mfma_f32_16x16x32_bf16 v[72:75], v[234:237], v[210:213], v[72:75]
	v_mfma_f32_16x16x32_bf16 v[52:55], v[226:229], v[218:221], v[52:55]
	v_mfma_f32_16x16x32_bf16 v[48:51], v[234:237], v[218:221], v[48:51]
	s_setprio 0
	s_mov_b32 m0, s34
	v_lshl_add_u64 v[238:239], v[244:245], 0, s[8:9]
	s_barrier
	ds_read_b128 v[190:193], v168 offset:49152
	ds_read_b128 v[194:197], v168 offset:50176
	ds_read_b128 v[198:201], v168 offset:51200
	ds_read_b128 v[202:205], v168 offset:52224
	ds_read_b128 v[206:209], v168 offset:53248
	ds_read_b128 v[210:213], v168 offset:54272
	ds_read_b128 v[214:217], v168 offset:55296
	ds_read_b128 v[218:221], v168 offset:56320
	global_load_lds_dwordx4 v[238:239], off
	v_lshl_add_u64 v[238:239], v[242:243], 0, s[8:9]
	s_mov_b32 m0, s35
	s_nop 0
	global_load_lds_dwordx4 v[238:239], off
	s_barrier
	s_setprio 1
	s_waitcnt lgkmcnt(7)
	v_mfma_f32_16x16x32_bf16 v[20:23], v[174:177], v[190:193], v[20:23]
	v_mfma_f32_16x16x32_bf16 v[8:11], v[182:185], v[190:193], v[8:11]
	s_waitcnt lgkmcnt(5)
	v_mfma_f32_16x16x32_bf16 v[40:43], v[174:177], v[198:201], v[40:43]
	v_mfma_f32_16x16x32_bf16 v[44:47], v[182:185], v[198:201], v[44:47]
	s_waitcnt lgkmcnt(3)
	v_mfma_f32_16x16x32_bf16 v[24:27], v[174:177], v[206:209], v[24:27]
	v_mfma_f32_16x16x32_bf16 v[28:31], v[182:185], v[206:209], v[28:31]
	s_waitcnt lgkmcnt(1)
	v_mfma_f32_16x16x32_bf16 v[0:3], v[174:177], v[214:217], v[0:3]
	v_mfma_f32_16x16x32_bf16 v[4:7], v[182:185], v[214:217], v[4:7]
	v_mfma_f32_16x16x32_bf16 v[20:23], v[178:181], v[194:197], v[20:23]
	v_mfma_f32_16x16x32_bf16 v[8:11], v[186:189], v[194:197], v[8:11]
	v_mfma_f32_16x16x32_bf16 v[40:43], v[178:181], v[202:205], v[40:43]
	v_mfma_f32_16x16x32_bf16 v[44:47], v[186:189], v[202:205], v[44:47]
	v_mfma_f32_16x16x32_bf16 v[24:27], v[178:181], v[210:213], v[24:27]
	v_mfma_f32_16x16x32_bf16 v[28:31], v[186:189], v[210:213], v[28:31]
	s_waitcnt lgkmcnt(0)
	v_mfma_f32_16x16x32_bf16 v[0:3], v[178:181], v[218:221], v[0:3]
	v_mfma_f32_16x16x32_bf16 v[4:7], v[186:189], v[218:221], v[4:7]
	s_setprio 0
	s_barrier
	s_add_u32 s0, s24, 0x40080
	s_addc_u32 s1, s25, 0
	s_mov_b32 m0, s64
	v_lshl_add_u64 v[174:175], s[0:1], 0, v[128:129]
	global_load_lds_dwordx4 v[174:175], off
	v_lshl_add_u64 v[174:175], s[0:1], 0, v[130:131]
	s_mov_b32 m0, s65
	s_nop 0
	global_load_lds_dwordx4 v[174:175], off
	s_waitcnt vmcnt(6)
	s_barrier
	s_setprio 1
	v_mfma_f32_16x16x32_bf16 v[64:67], v[222:225], v[190:193], v[64:67]
	v_mfma_f32_16x16x32_bf16 v[68:71], v[230:233], v[190:193], v[68:71]
	v_mfma_f32_16x16x32_bf16 v[56:59], v[222:225], v[198:201], v[56:59]
	v_mfma_f32_16x16x32_bf16 v[60:63], v[230:233], v[198:201], v[60:63]
	v_mfma_f32_16x16x32_bf16 v[32:35], v[222:225], v[206:209], v[32:35]
	v_mfma_f32_16x16x32_bf16 v[36:39], v[230:233], v[206:209], v[36:39]
	v_mfma_f32_16x16x32_bf16 v[12:15], v[222:225], v[214:217], v[12:15]
	v_mfma_f32_16x16x32_bf16 v[16:19], v[230:233], v[214:217], v[16:19]
	v_mfma_f32_16x16x32_bf16 v[64:67], v[226:229], v[194:197], v[64:67]
	v_mfma_f32_16x16x32_bf16 v[68:71], v[234:237], v[194:197], v[68:71]
	v_mfma_f32_16x16x32_bf16 v[56:59], v[226:229], v[202:205], v[56:59]
	v_mfma_f32_16x16x32_bf16 v[60:63], v[234:237], v[202:205], v[60:63]
	v_mfma_f32_16x16x32_bf16 v[32:35], v[226:229], v[210:213], v[32:35]
	v_mfma_f32_16x16x32_bf16 v[36:39], v[234:237], v[210:213], v[36:39]
	v_mfma_f32_16x16x32_bf16 v[12:15], v[226:229], v[218:221], v[12:15]
	v_mfma_f32_16x16x32_bf16 v[16:19], v[234:237], v[218:221], v[16:19]
	s_setprio 0
	s_add_i32 s68, s68, 2
	s_cmp_gt_u32 s68, 13
	s_mov_b64 s[0:1], s[22:23]
	s_cbranch_scc1 .Lmy_kx_7
	s_barrier
	s_branch .LBB0_2221
